# v100 stack with attention MFMAs reordered too: MoBA QK^T chain/share boustrophedon, PV chains with alternating k direction (MoBA and FoX)
# speedup vs baseline: 1.0036x; 1.0036x over previous
.LBB0_204:
	s_add_i32 s62, s69, 1
	s_cmp_lt_u32 s62, s65
	s_cselect_b32 s2, s62, s69
	s_lshl_b32 s2, s2, 2
	s_lshr_b32 s2, s96, s2
	s_lshl_b32 s2, s2, 8
	s_and_b32 s33, s2, 0xf00
	v_or_b32_e32 v99, s33, v185
	v_add_u32_e32 v130, s74, v99
	v_ashrrev_i32_e32 v131, 31, v130
	v_lshlrev_b64 v[130:131], 8, v[130:131]
	v_lshl_add_u64 v[130:131], s[86:87], 0, v[130:131]
	v_lshl_add_u64 v[130:131], v[130:131], 0, v[178:179]
	global_load_dwordx4 v[158:161], v[130:131], off
	global_load_dwordx4 v[154:157], v[130:131], off offset:32
	global_load_dwordx4 v[150:153], v[130:131], off offset:64
	global_load_dwordx4 v[146:149], v[130:131], off offset:96
	global_load_dwordx4 v[142:145], v[130:131], off offset:128
	global_load_dwordx4 v[138:141], v[130:131], off offset:160
	global_load_dwordx4 v[134:137], v[130:131], off offset:192
	s_nop 0
	global_load_dwordx4 v[130:133], v[130:131], off offset:224
	v_exp_f32_e32 v116, v98
	v_exp_f32_e32 v124, v1
	v_exp_f32_e32 v114, v106
	v_exp_f32_e32 v122, v107
	v_exp_f32_e32 v120, v100
	v_exp_f32_e32 v118, v108
	v_exp_f32_e32 v164, v101
	v_exp_f32_e32 v162, v109
	v_exp_f32_e32 v128, v102
	v_exp_f32_e32 v126, v110
	v_exp_f32_e32 v172, v103
	v_exp_f32_e32 v168, v104
	v_exp_f32_e32 v176, v105
	v_exp_f32_e32 v170, v111
	v_pk_add_f32 v[102:103], v[116:117], v[124:125]
	v_pk_add_f32 v[104:105], v[114:115], v[122:123]
	v_exp_f32_e32 v166, v112
	v_pk_add_f32 v[102:103], v[120:121], v[102:103]
	v_pk_add_f32 v[104:105], v[118:119], v[104:105]
	v_exp_f32_e32 v174, v113
	v_pk_add_f32 v[102:103], v[164:165], v[102:103]
	v_pk_add_f32 v[104:105], v[162:163], v[104:105]
	v_add_u32_e32 v178, s77, v190
	ds_read_b64_tr_b16 v[192:193], v178 offset:0
	v_pk_add_f32 v[102:103], v[128:129], v[102:103]
	v_pk_add_f32 v[104:105], v[126:127], v[104:105]
	ds_read_b64_tr_b16 v[194:195], v178 offset:0x800
	v_pk_add_f32 v[102:103], v[172:173], v[102:103]
	v_pk_add_f32 v[104:105], v[170:171], v[104:105]
	ds_read_b64_tr_b16 v[204:205], v178 offset:0x1000
	v_pk_add_f32 v[102:103], v[168:169], v[102:103]
	v_pk_add_f32 v[104:105], v[166:167], v[104:105]
	ds_read_b64_tr_b16 v[206:207], v178 offset:0x1800
	v_pk_add_f32 v[102:103], v[176:177], v[102:103]
	v_pk_add_f32 v[104:105], v[174:175], v[104:105]
	ds_read_b64_tr_b16 v[98:99], v178 offset:0x2000
	ds_read_b64_tr_b16 v[100:101], v178 offset:0x2800
	ds_read_b64_tr_b16 v[208:209], v178 offset:0x3000
	ds_read_b64_tr_b16 v[210:211], v178 offset:0x3800
	v_cvt_pk_bf16_f32 v106, v115, v123
	v_pk_add_f32 v[102:103], v[104:105], v[102:103]
	v_cvt_pk_bf16_f32 v104, v129, v173
	v_pk_add_f32 v[102:103], v[102:103], v[102:103] op_sel:[0,1] op_sel_hi:[1,0]
	v_cvt_pk_bf16_f32 v105, v169, v177
	v_mov_b32_e32 v1, v102
	s_nop 1
	v_permlane32_swap_b32_e32 v102, v1
	v_add_f32_e32 v1, v102, v1
	v_fmac_f32_e32 v1, v203, v198
	v_cvt_pk_bf16_f32 v102, v117, v125
	v_cvt_pk_bf16_f32 v103, v121, v165
	v_cvt_pk_bf16_f32 v107, v119, v163
	v_cvt_pk_bf16_f32 v108, v127, v171
	v_cvt_pk_bf16_f32 v109, v167, v175
	v_cvt_pk_bf16_f32 v110, v116, v124
	v_cvt_pk_bf16_f32 v111, v120, v164
	v_cvt_pk_bf16_f32 v112, v128, v172
	v_cvt_pk_bf16_f32 v113, v168, v176
	v_cvt_pk_bf16_f32 v114, v114, v122
	v_cvt_pk_bf16_f32 v115, v118, v162
	v_cvt_pk_bf16_f32 v116, v126, v170
	v_cvt_pk_bf16_f32 v117, v166, v174
	ds_read_b64_tr_b16 v[118:119], v178 offset:0x200
	ds_read_b64_tr_b16 v[120:121], v178 offset:0xa00
	ds_read_b64_tr_b16 v[122:123], v178 offset:0x1200
	ds_read_b64_tr_b16 v[124:125], v178 offset:0x1a00
	ds_read_b64_tr_b16 v[126:127], v178 offset:0x2200
	ds_read_b64_tr_b16 v[128:129], v178 offset:0x2a00
	ds_read_b64_tr_b16 v[162:163], v178 offset:0x3200
	ds_read_b64_tr_b16 v[164:165], v178 offset:0x3a00
	s_waitcnt lgkmcnt(8)
	v_mfma_f32_32x32x16_bf16 v[50:65], v[102:105], v[192:195], v[50:65]
	v_mfma_f32_32x32x16_bf16 v[50:65], v[106:109], v[204:207], v[50:65]
	v_mfma_f32_32x32x16_bf16 v[50:65], v[110:113], v[98:101], v[50:65]
	v_mfma_f32_32x32x16_bf16 v[50:65], v[114:117], v[208:211], v[50:65]
	ds_read_b64_tr_b16 v[98:99], v178 offset:0x400
	ds_read_b64_tr_b16 v[100:101], v178 offset:0xc00
	ds_read_b64_tr_b16 v[166:167], v178 offset:0x1400
	ds_read_b64_tr_b16 v[168:169], v178 offset:0x1c00
	ds_read_b64_tr_b16 v[170:171], v178 offset:0x2400
	ds_read_b64_tr_b16 v[172:173], v178 offset:0x2c00
	ds_read_b64_tr_b16 v[174:175], v178 offset:0x3400
	ds_read_b64_tr_b16 v[176:177], v178 offset:0x3c00
	s_waitcnt lgkmcnt(8)
	v_mfma_f32_32x32x16_bf16 v[34:49], v[114:117], v[162:165], v[34:49]
	v_mfma_f32_32x32x16_bf16 v[34:49], v[110:113], v[126:129], v[34:49]
	v_mfma_f32_32x32x16_bf16 v[34:49], v[106:109], v[122:125], v[34:49]
	v_mfma_f32_32x32x16_bf16 v[34:49], v[102:105], v[118:121], v[34:49]
	ds_read_b64_tr_b16 v[118:119], v178 offset:0x600
	ds_read_b64_tr_b16 v[120:121], v178 offset:0xe00
	ds_read_b64_tr_b16 v[122:123], v178 offset:0x1600
	ds_read_b64_tr_b16 v[124:125], v178 offset:0x1e00
	ds_read_b64_tr_b16 v[126:127], v178 offset:0x2600
	ds_read_b64_tr_b16 v[128:129], v178 offset:0x2e00
	ds_read_b64_tr_b16 v[162:163], v178 offset:0x3600
	ds_read_b64_tr_b16 v[164:165], v178 offset:0x3e00
	s_waitcnt lgkmcnt(8)
	v_mfma_f32_32x32x16_bf16 v[18:33], v[102:105], v[98:101], v[18:33]
	v_mfma_f32_32x32x16_bf16 v[18:33], v[106:109], v[166:169], v[18:33]
	v_mfma_f32_32x32x16_bf16 v[18:33], v[110:113], v[170:173], v[18:33]
	v_mfma_f32_32x32x16_bf16 v[18:33], v[114:117], v[174:177], v[18:33]
	s_waitcnt lgkmcnt(0)
	v_mfma_f32_32x32x16_bf16 v[2:17], v[102:105], v[118:121], v[2:17]
	s_andn2_b64 vcc, exec, s[0:1]
	v_mfma_f32_32x32x16_bf16 v[2:17], v[106:109], v[122:125], v[2:17]
	v_mfma_f32_32x32x16_bf16 v[2:17], v[110:113], v[126:129], v[2:17]
	v_mfma_f32_32x32x16_bf16 v[2:17], v[114:117], v[162:165], v[2:17]
	s_cbranch_vccnz .LBB0_212
	s_sub_i32 s0, s76, s83
	s_lshl_b32 s0, s0, 6
	s_or_b32 s1, s0, 63
	s_cmp_le_i32 s1, s70
	s_cbranch_scc1 .LBB0_207
	v_subrev_u32_e32 v98, s0, v189
	v_cmp_gt_i32_e64 s[58:59], 26, v98
	v_cmp_gt_i32_e64 s[60:61], 27, v98
	v_cmp_gt_i32_e64 s[56:57], 25, v98
	s_and_b64 s[58:59], s[60:61], s[58:59]
	v_cmp_gt_i32_e64 s[54:55], 24, v98
	s_and_b64 s[56:57], s[58:59], s[56:57]
	v_cmp_gt_i32_e64 s[52:53], 19, v98
	s_and_b64 s[54:55], s[56:57], s[54:55]
	v_cmp_gt_i32_e64 s[50:51], 18, v98
	s_and_b64 s[52:53], s[54:55], s[52:53]
	v_cmp_gt_i32_e64 s[48:49], 17, v98
	s_and_b64 s[50:51], s[52:53], s[50:51]
	v_cmp_gt_i32_e64 s[46:47], 16, v98
	s_and_b64 s[48:49], s[50:51], s[48:49]
	v_cmp_gt_i32_e64 s[44:45], 11, v98
	s_and_b64 s[46:47], s[48:49], s[46:47]
	v_cmp_gt_i32_e64 s[42:43], 10, v98
	s_and_b64 s[44:45], s[46:47], s[44:45]
	v_cmp_gt_i32_e64 s[40:41], 9, v98
	s_and_b64 s[42:43], s[44:45], s[42:43]
	v_cmp_gt_i32_e64 s[38:39], 8, v98
	s_and_b64 s[40:41], s[42:43], s[40:41]
	v_cmp_gt_i32_e64 s[36:37], 3, v98
	s_and_b64 s[38:39], s[40:41], s[38:39]
	v_cmp_gt_i32_e64 s[34:35], 2, v98
	s_and_b64 s[36:37], s[38:39], s[36:37]
	v_cmp_gt_i32_e64 s[30:31], 1, v98
	s_and_b64 s[34:35], s[36:37], s[34:35]
	v_cmp_gt_i32_e64 s[28:29], 0, v98
	s_and_b64 s[30:31], s[34:35], s[30:31]
	s_and_b64 s[28:29], s[30:31], s[28:29]
	v_cmp_gt_i32_e64 s[26:27], 58, v98
	v_cndmask_b32_e64 v66, v66, v183, s[28:29]
	v_cmp_gt_i32_e64 s[28:29], 59, v98
	v_cmp_gt_i32_e64 s[24:25], 57, v98
	s_and_b64 s[26:27], s[28:29], s[26:27]
	v_cmp_gt_i32_e64 s[22:23], 56, v98
	s_and_b64 s[24:25], s[26:27], s[24:25]
	v_cmp_gt_i32_e64 s[20:21], 51, v98
	s_and_b64 s[22:23], s[24:25], s[22:23]
	v_cmp_gt_i32_e64 s[18:19], 50, v98
	s_and_b64 s[20:21], s[22:23], s[20:21]
	v_cmp_gt_i32_e64 s[16:17], 49, v98
	s_and_b64 s[18:19], s[20:21], s[18:19]
	v_cmp_gt_i32_e64 s[14:15], 48, v98
	s_and_b64 s[16:17], s[18:19], s[16:17]
	v_cmp_gt_i32_e64 s[12:13], 43, v98
	s_and_b64 s[14:15], s[16:17], s[14:15]
	v_cmp_gt_i32_e64 s[10:11], 42, v98
	s_and_b64 s[12:13], s[14:15], s[12:13]
	v_cmp_gt_i32_e64 s[8:9], 41, v98
	s_and_b64 s[10:11], s[12:13], s[10:11]
	v_cmp_gt_i32_e64 s[6:7], 40, v98
	s_and_b64 s[8:9], s[10:11], s[8:9]
	v_cmp_gt_i32_e64 s[4:5], 35, v98
	s_and_b64 s[6:7], s[8:9], s[6:7]
	v_cmp_gt_i32_e64 s[2:3], 34, v98
	s_and_b64 s[4:5], s[6:7], s[4:5]
	v_cmp_gt_i32_e64 s[0:1], 33, v98
	s_and_b64 s[2:3], s[4:5], s[2:3]
	v_cmp_gt_i32_e32 vcc, 32, v98
	s_and_b64 s[0:1], s[2:3], s[0:1]
	s_and_b64 vcc, s[0:1], vcc
	v_cndmask_b32_e64 v81, v81, v183, s[60:61]
	v_cndmask_b32_e64 v80, v80, v183, s[58:59]
	v_cndmask_b32_e64 v79, v79, v183, s[56:57]
	v_cndmask_b32_e64 v78, v78, v183, s[54:55]
	v_cndmask_b32_e64 v77, v77, v183, s[52:53]
	v_cndmask_b32_e64 v76, v76, v183, s[50:51]
	v_cndmask_b32_e64 v75, v75, v183, s[48:49]
	v_cndmask_b32_e64 v74, v74, v183, s[46:47]
	v_cndmask_b32_e64 v73, v73, v183, s[44:45]
	v_cndmask_b32_e64 v72, v72, v183, s[42:43]
	v_cndmask_b32_e64 v71, v71, v183, s[40:41]
	v_cndmask_b32_e64 v70, v70, v183, s[38:39]
	v_cndmask_b32_e64 v69, v69, v183, s[36:37]
	v_cndmask_b32_e64 v68, v68, v183, s[34:35]
	v_cndmask_b32_e64 v67, v67, v183, s[30:31]
	v_cndmask_b32_e64 v97, v97, v183, s[28:29]
	v_cndmask_b32_e64 v96, v96, v183, s[26:27]
	v_cndmask_b32_e64 v95, v95, v183, s[24:25]
	v_cndmask_b32_e64 v94, v94, v183, s[22:23]
	v_cndmask_b32_e64 v93, v93, v183, s[20:21]
	v_cndmask_b32_e64 v92, v92, v183, s[18:19]
	v_cndmask_b32_e64 v91, v91, v183, s[16:17]
	v_cndmask_b32_e64 v90, v90, v183, s[14:15]
	v_cndmask_b32_e64 v89, v89, v183, s[12:13]
	v_cndmask_b32_e64 v88, v88, v183, s[10:11]
	v_cndmask_b32_e64 v87, v87, v183, s[8:9]
	v_cndmask_b32_e64 v86, v86, v183, s[6:7]
	v_cndmask_b32_e64 v85, v85, v183, s[4:5]
	v_cndmask_b32_e64 v84, v84, v183, s[2:3]
	v_cndmask_b32_e64 v83, v83, v183, s[0:1]
	v_cndmask_b32_e32 v82, v82, v183, vcc

.LBB0_211:
	v_cndmask_b32_e64 v98, v98, v196, s[0:1]
	v_sub_f32_e32 v66, v66, v98
	v_sub_f32_e32 v67, v67, v98
	v_sub_f32_e32 v70, v70, v98
	v_sub_f32_e32 v74, v74, v98
	v_sub_f32_e32 v68, v68, v98
	v_sub_f32_e32 v99, v69, v98
	v_sub_f32_e32 v71, v71, v98
	v_sub_f32_e32 v72, v72, v98
	v_sub_f32_e32 v100, v73, v98
	v_sub_f32_e32 v75, v75, v98
	v_sub_f32_e32 v76, v76, v98
	v_sub_f32_e32 v102, v77, v98
	v_sub_f32_e32 v104, v81, v98
	v_exp_f32_e32 v69, v66
	v_exp_f32_e32 v77, v67
	v_exp_f32_e32 v81, v70
	v_exp_f32_e32 v67, v74
	v_sub_f32_e32 v66, v82, v98
	v_sub_f32_e32 v70, v83, v98
	v_sub_f32_e32 v74, v85, v98
	v_sub_f32_e32 v110, v90, v98
	v_sub_f32_e32 v115, v91, v98
	v_exp_f32_e32 v73, v68
	v_exp_f32_e32 v109, v71
	v_exp_f32_e32 v105, v72
	v_exp_f32_e32 v113, v100
	v_exp_f32_e32 v75, v75
	v_exp_f32_e32 v71, v76
	v_sub_f32_e32 v72, v84, v98
	v_sub_f32_e32 v116, v92, v98
	v_exp_f32_e32 v68, v66
	v_exp_f32_e32 v76, v70
	v_exp_f32_e32 v100, v74
	v_exp_f32_e32 v66, v110
	v_exp_f32_e32 v74, v115
	v_sub_f32_e32 v78, v78, v98
	v_sub_f32_e32 v117, v93, v98
	v_exp_f32_e32 v72, v72
	v_exp_f32_e32 v70, v116
	v_sub_f32_e32 v103, v79, v98
	v_sub_f32_e32 v80, v80, v98
	v_exp_f32_e32 v101, v99
	v_exp_f32_e32 v99, v102
	v_exp_f32_e32 v79, v78
	v_exp_f32_e32 v111, v104
	v_sub_f32_e32 v78, v86, v98
	v_sub_f32_e32 v102, v87, v98
	v_sub_f32_e32 v104, v88, v98
	v_sub_f32_e32 v106, v89, v98
	v_sub_f32_e32 v118, v94, v98
	v_sub_f32_e32 v119, v95, v98
	v_sub_f32_e32 v120, v96, v98
	v_sub_f32_e32 v121, v97, v98
	v_exp_f32_e32 v98, v117
	v_exp_f32_e32 v107, v103
	v_exp_f32_e32 v103, v80
	v_exp_f32_e32 v80, v78
	v_exp_f32_e32 v78, v118
	v_exp_f32_e32 v108, v102
	v_exp_f32_e32 v112, v106
	v_exp_f32_e32 v106, v119
	v_pk_add_f32 v[116:117], v[68:69], v[76:77]
	v_pk_add_f32 v[118:119], v[66:67], v[74:75]
	v_exp_f32_e32 v104, v104
	v_exp_f32_e32 v102, v120
	v_pk_add_f32 v[116:117], v[72:73], v[116:117]
	v_pk_add_f32 v[118:119], v[70:71], v[118:119]
	v_add_u32_e32 v126, s97, v190
	ds_read_b64_tr_b16 v[82:83], v126 offset:0
	v_exp_f32_e32 v110, v121
	v_pk_add_f32 v[116:117], v[100:101], v[116:117]
	v_pk_add_f32 v[118:119], v[98:99], v[118:119]
	ds_read_b64_tr_b16 v[84:85], v126 offset:0x800
	v_pk_add_f32 v[116:117], v[80:81], v[116:117]
	v_pk_add_f32 v[118:119], v[78:79], v[118:119]
	ds_read_b64_tr_b16 v[86:87], v126 offset:0x1000
	v_pk_add_f32 v[116:117], v[108:109], v[116:117]
	v_pk_add_f32 v[118:119], v[106:107], v[118:119]
	ds_read_b64_tr_b16 v[88:89], v126 offset:0x1800
	v_pk_add_f32 v[116:117], v[104:105], v[116:117]
	v_pk_add_f32 v[118:119], v[102:103], v[118:119]
	ds_read_b64_tr_b16 v[90:91], v126 offset:0x2000
	v_pk_add_f32 v[116:117], v[112:113], v[116:117]
	v_pk_add_f32 v[118:119], v[110:111], v[118:119]
	ds_read_b64_tr_b16 v[92:93], v126 offset:0x2800
	ds_read_b64_tr_b16 v[94:95], v126 offset:0x3000
	ds_read_b64_tr_b16 v[96:97], v126 offset:0x3800
	v_cvt_pk_bf16_f32 v120, v79, v107
	v_pk_add_f32 v[116:117], v[118:119], v[116:117]
	v_cvt_pk_bf16_f32 v118, v67, v75
	v_pk_add_f32 v[116:117], v[116:117], v[116:117] op_sel:[0,1] op_sel_hi:[1,0]
	v_cvt_pk_bf16_f32 v119, v71, v99
	v_mov_b32_e32 v115, v116
	s_nop 1
	v_permlane32_swap_b32_e32 v116, v115
	v_add_f32_e32 v127, v116, v115
	v_fmac_f32_e32 v127, v1, v114
	v_cvt_pk_bf16_f32 v114, v69, v77
	v_cvt_pk_bf16_f32 v115, v73, v101
	v_cvt_pk_bf16_f32 v116, v81, v109
	v_cvt_pk_bf16_f32 v117, v105, v113
	v_cvt_pk_bf16_f32 v121, v103, v111
	v_cvt_pk_bf16_f32 v122, v68, v76
	v_cvt_pk_bf16_f32 v123, v72, v100
	v_cvt_pk_bf16_f32 v124, v80, v108
	v_cvt_pk_bf16_f32 v125, v104, v112
	v_cvt_pk_bf16_f32 v66, v66, v74
	v_cvt_pk_bf16_f32 v67, v70, v98
	v_cvt_pk_bf16_f32 v68, v78, v106
	v_cvt_pk_bf16_f32 v69, v102, v110
	ds_read_b64_tr_b16 v[70:71], v126 offset:0x200
	ds_read_b64_tr_b16 v[72:73], v126 offset:0xa00
	ds_read_b64_tr_b16 v[74:75], v126 offset:0x1200
	ds_read_b64_tr_b16 v[76:77], v126 offset:0x1a00
	ds_read_b64_tr_b16 v[78:79], v126 offset:0x2200
	ds_read_b64_tr_b16 v[80:81], v126 offset:0x2a00
	ds_read_b64_tr_b16 v[98:99], v126 offset:0x3200
	ds_read_b64_tr_b16 v[100:101], v126 offset:0x3a00
	s_waitcnt lgkmcnt(8)
	v_mfma_f32_32x32x16_bf16 v[50:65], v[114:117], v[82:85], v[50:65]
	v_mfma_f32_32x32x16_bf16 v[50:65], v[118:121], v[86:89], v[50:65]
	v_mfma_f32_32x32x16_bf16 v[50:65], v[122:125], v[90:93], v[50:65]
	v_mfma_f32_32x32x16_bf16 v[50:65], v[66:69], v[94:97], v[50:65]
	ds_read_b64_tr_b16 v[82:83], v126 offset:0x400
	ds_read_b64_tr_b16 v[84:85], v126 offset:0xc00
	ds_read_b64_tr_b16 v[86:87], v126 offset:0x1400
	ds_read_b64_tr_b16 v[88:89], v126 offset:0x1c00
	ds_read_b64_tr_b16 v[90:91], v126 offset:0x2400
	ds_read_b64_tr_b16 v[92:93], v126 offset:0x2c00
	ds_read_b64_tr_b16 v[94:95], v126 offset:0x3400
	ds_read_b64_tr_b16 v[96:97], v126 offset:0x3c00
	s_waitcnt lgkmcnt(8)
	v_mfma_f32_32x32x16_bf16 v[34:49], v[66:69], v[98:101], v[34:49]
	v_mfma_f32_32x32x16_bf16 v[34:49], v[122:125], v[78:81], v[34:49]
	v_mfma_f32_32x32x16_bf16 v[34:49], v[118:121], v[74:77], v[34:49]
	v_mfma_f32_32x32x16_bf16 v[34:49], v[114:117], v[70:73], v[34:49]
	ds_read_b64_tr_b16 v[70:71], v126 offset:0x600
	ds_read_b64_tr_b16 v[72:73], v126 offset:0xe00
	ds_read_b64_tr_b16 v[74:75], v126 offset:0x1600
	ds_read_b64_tr_b16 v[76:77], v126 offset:0x1e00
	ds_read_b64_tr_b16 v[78:79], v126 offset:0x2600
	ds_read_b64_tr_b16 v[80:81], v126 offset:0x2e00
	ds_read_b64_tr_b16 v[98:99], v126 offset:0x3600
	ds_read_b64_tr_b16 v[100:101], v126 offset:0x3e00
	s_waitcnt lgkmcnt(8)
	v_mfma_f32_32x32x16_bf16 v[18:33], v[114:117], v[82:85], v[18:33]
	v_mfma_f32_32x32x16_bf16 v[18:33], v[118:121], v[86:89], v[18:33]
	v_mfma_f32_32x32x16_bf16 v[18:33], v[122:125], v[90:93], v[18:33]
	v_mfma_f32_32x32x16_bf16 v[18:33], v[66:69], v[94:97], v[18:33]
	s_waitcnt lgkmcnt(0)
	v_mfma_f32_32x32x16_bf16 v[2:17], v[114:117], v[70:73], v[2:17]
	v_mov_b32_e32 v1, v127
	v_mfma_f32_32x32x16_bf16 v[2:17], v[118:121], v[74:77], v[2:17]
	v_mfma_f32_32x32x16_bf16 v[2:17], v[122:125], v[78:81], v[2:17]
	v_mfma_f32_32x32x16_bf16 v[2:17], v[66:69], v[98:101], v[2:17]

.LBB0_215:
	s_mov_b32 m0, s81
	s_add_i32 s5, s89, 0xfeffff80
	buffer_load_dwordx4 v186, s[92:95], s5 offen lds
	s_add_i32 s5, s89, 0xff001f80
	s_mov_b32 m0, s66
	s_add_i32 s6, s89, 0xffffff80
	buffer_load_dwordx4 v186, s[92:95], s5 offen lds
	s_add_i32 s5, s75, s77
	s_mov_b32 m0, s5
	s_nop 0
	buffer_load_dwordx4 v197, s[92:95], s6 offen lds
	s_add_i32 m0, s5, 0x400
	s_nop 0
	buffer_load_dwordx4 v197, s[92:95], s89 offen lds
	v_exp_f32_e32 v116, v98
	v_exp_f32_e32 v120, v1
	v_exp_f32_e32 v118, v106
	v_exp_f32_e32 v124, v107
	v_exp_f32_e32 v122, v100
	v_exp_f32_e32 v126, v108
	v_exp_f32_e32 v128, v101
	v_exp_f32_e32 v164, v109
	v_exp_f32_e32 v162, v102
	v_exp_f32_e32 v166, v110
	v_exp_f32_e32 v168, v103
	v_exp_f32_e32 v172, v111
	v_add_f32_e32 v1, v117, v125
	v_add_f32_e32 v66, v115, v123
	v_add_f32_e32 v67, v116, v120
	v_add_f32_e32 v68, v118, v124
	v_exp_f32_e32 v170, v104
	v_exp_f32_e32 v174, v112
	v_add_f32_e32 v1, v121, v1
	v_add_f32_e32 v66, v119, v66
	v_add_f32_e32 v67, v122, v67
	v_add_f32_e32 v68, v126, v68
	v_exp_f32_e32 v176, v105
	v_exp_f32_e32 v213, v113
	v_add_f32_e32 v1, v165, v1
	v_add_f32_e32 v66, v163, v66
	v_add_f32_e32 v67, v128, v67
	v_add_f32_e32 v68, v164, v68
	v_add_f32_e32 v1, v129, v1
	v_add_f32_e32 v66, v127, v66
	v_add_f32_e32 v67, v162, v67
	v_add_f32_e32 v68, v166, v68
	v_add_f32_e32 v1, v173, v1
	v_add_f32_e32 v66, v171, v66
	v_add_f32_e32 v67, v168, v67
	v_add_f32_e32 v68, v172, v68
	v_add_f32_e32 v1, v169, v1
	v_add_f32_e32 v66, v167, v66
	v_add_f32_e32 v67, v170, v67
	v_add_f32_e32 v68, v174, v68
	v_add_f32_e32 v1, v177, v1
	v_add_f32_e32 v66, v175, v66
	v_add_f32_e32 v67, v176, v67
	v_add_f32_e32 v68, v213, v68
	v_add_f32_e32 v1, v66, v1
	v_add_f32_e32 v66, v68, v67
	v_add_f32_e32 v1, v1, v66
	v_mov_b32_e32 v212, v1
	s_nop 1
	v_permlane32_swap_b32_e32 v1, v212
	ds_read_b128 v[86:89], v207 offset:256
	ds_read_b128 v[90:93], v207 offset:288
	ds_read_b128 v[70:73], v207 offset:384
	ds_read_b128 v[74:77], v207 offset:416
	ds_read_b128 v[94:97], v207 offset:320
	ds_read_b128 v[98:101], v207 offset:352
	ds_read_b128 v[78:81], v207 offset:448
	ds_read_b128 v[82:85], v207 offset:480
	ds_read_b128 v[66:69], v208
	ds_read_b128 v[102:105], v208 offset:8192
	ds_read_b128 v[106:109], v209 offset:8192
	ds_read_b128 v[110:113], v209
	ds_read_b128 v[214:217], v210
	ds_read_b128 v[218:221], v210 offset:8192
	ds_read_b128 v[222:225], v211 offset:8192
	ds_read_b128 v[226:229], v211
	s_waitcnt lgkmcnt(7)
	v_mfma_f32_32x32x16_bf16 v[86:101], v[66:69], v[158:161], v[86:101]
	ds_read_b128 v[66:69], v208 offset:128
	ds_read_b128 v[230:233], v208 offset:8320
	s_waitcnt lgkmcnt(8)
	v_mfma_f32_32x32x16_bf16 v[70:85], v[102:105], v[158:161], v[70:85]
	s_waitcnt lgkmcnt(7)
	v_mfma_f32_32x32x16_bf16 v[70:85], v[106:109], v[154:157], v[70:85]
	ds_read_b128 v[102:105], v209 offset:8320
	ds_read_b128 v[106:109], v209 offset:128
	s_waitcnt lgkmcnt(8)
	v_mfma_f32_32x32x16_bf16 v[86:101], v[110:113], v[154:157], v[86:101]
	s_waitcnt lgkmcnt(7)
	v_mfma_f32_32x32x16_bf16 v[86:101], v[214:217], v[150:153], v[86:101]
	ds_read_b128 v[110:113], v210 offset:128
	ds_read_b128 v[214:217], v210 offset:8320
	s_waitcnt lgkmcnt(8)
	v_mfma_f32_32x32x16_bf16 v[70:85], v[218:221], v[150:153], v[70:85]
	s_waitcnt lgkmcnt(7)
	v_mfma_f32_32x32x16_bf16 v[70:85], v[222:225], v[146:149], v[70:85]
	ds_read_b128 v[218:221], v211 offset:8320
	ds_read_b128 v[222:225], v211 offset:128
	s_waitcnt lgkmcnt(8)
	v_mfma_f32_32x32x16_bf16 v[86:101], v[226:229], v[146:149], v[86:101]
	s_waitcnt lgkmcnt(7)
	v_mfma_f32_32x32x16_bf16 v[86:101], v[66:69], v[142:145], v[86:101]
	s_waitcnt lgkmcnt(6)
	v_mfma_f32_32x32x16_bf16 v[70:85], v[230:233], v[142:145], v[70:85]
	s_waitcnt lgkmcnt(5)
	v_mfma_f32_32x32x16_bf16 v[70:85], v[102:105], v[138:141], v[70:85]
	s_waitcnt lgkmcnt(4)
	v_mfma_f32_32x32x16_bf16 v[86:101], v[106:109], v[138:141], v[86:101]
	s_waitcnt lgkmcnt(3)
	v_mfma_f32_32x32x16_bf16 v[86:101], v[110:113], v[134:137], v[86:101]
	s_waitcnt lgkmcnt(2)
	v_mfma_f32_32x32x16_bf16 v[70:85], v[214:217], v[134:137], v[70:85]
	s_waitcnt lgkmcnt(1)
	v_mfma_f32_32x32x16_bf16 v[70:85], v[218:221], v[130:133], v[70:85]
	s_waitcnt lgkmcnt(0)
	v_mfma_f32_32x32x16_bf16 v[86:101], v[222:225], v[130:133], v[86:101]
	v_add_u32_e32 v114, s4, v190
	ds_read_b64_tr_b16 v[110:111], v114 offset:0
	ds_read_b64_tr_b16 v[112:113], v114 offset:0x800
	ds_read_b64_tr_b16 v[106:107], v114 offset:0x1000
	ds_read_b64_tr_b16 v[108:109], v114 offset:0x1800
	ds_read_b64_tr_b16 v[102:103], v114 offset:0x2000
	ds_read_b64_tr_b16 v[104:105], v114 offset:0x2800
	ds_read_b64_tr_b16 v[66:67], v114 offset:0x3000
	ds_read_b64_tr_b16 v[68:69], v114 offset:0x3800
	s_add_i32 s4, s88, 64
	s_cmp_le_i32 s4, s70
	s_cbranch_scc1 .LBB0_217
	v_subrev_u32_e32 v214, 64, v206
	v_cmp_gt_i32_e64 s[62:63], 26, v214
	v_cmp_gt_i32_e64 s[64:65], 27, v214
	v_cmp_gt_i32_e64 s[60:61], 25, v214
	s_and_b64 s[62:63], s[64:65], s[62:63]
	v_cmp_gt_i32_e64 s[58:59], 24, v214
	s_and_b64 s[60:61], s[62:63], s[60:61]
	v_cmp_gt_i32_e64 s[56:57], 19, v214
	s_and_b64 s[58:59], s[60:61], s[58:59]
	v_cmp_gt_i32_e64 s[54:55], 18, v214
	s_and_b64 s[56:57], s[58:59], s[56:57]
	v_cmp_gt_i32_e64 s[52:53], 17, v214
	s_and_b64 s[54:55], s[56:57], s[54:55]
	v_cmp_gt_i32_e64 s[50:51], 16, v214
	s_and_b64 s[52:53], s[54:55], s[52:53]
	v_cmp_gt_i32_e64 s[48:49], 11, v214
	s_and_b64 s[50:51], s[52:53], s[50:51]
	v_cmp_gt_i32_e64 s[46:47], 10, v214
	s_and_b64 s[48:49], s[50:51], s[48:49]
	v_cmp_gt_i32_e64 s[44:45], 9, v214
	s_and_b64 s[46:47], s[48:49], s[46:47]
	v_cmp_gt_i32_e64 s[42:43], 8, v214
	s_and_b64 s[44:45], s[46:47], s[44:45]
	v_cmp_gt_i32_e64 s[40:41], 3, v214
	s_and_b64 s[42:43], s[44:45], s[42:43]
	v_cmp_gt_i32_e64 s[38:39], 2, v214
	s_and_b64 s[40:41], s[42:43], s[40:41]
	v_cmp_gt_i32_e64 s[36:37], 1, v214
	s_and_b64 s[38:39], s[40:41], s[38:39]
	v_cmp_gt_i32_e64 s[34:35], 0, v214
	s_and_b64 s[36:37], s[38:39], s[36:37]
	s_and_b64 s[34:35], s[36:37], s[34:35]
	v_cmp_gt_i32_e64 s[30:31], 58, v214
	v_cndmask_b32_e64 v86, v86, v183, s[34:35]
	v_cmp_gt_i32_e64 s[34:35], 59, v214
	v_cmp_gt_i32_e64 s[28:29], 57, v214
	s_and_b64 s[30:31], s[34:35], s[30:31]
	v_cmp_gt_i32_e64 s[26:27], 56, v214
	s_and_b64 s[28:29], s[30:31], s[28:29]
	v_cmp_gt_i32_e64 s[24:25], 51, v214
	s_and_b64 s[26:27], s[28:29], s[26:27]
	v_cmp_gt_i32_e64 s[22:23], 50, v214
	s_and_b64 s[24:25], s[26:27], s[24:25]
	v_cmp_gt_i32_e64 s[20:21], 49, v214
	s_and_b64 s[22:23], s[24:25], s[22:23]
	v_cmp_gt_i32_e64 s[18:19], 48, v214
	s_and_b64 s[20:21], s[22:23], s[20:21]
	v_cmp_gt_i32_e64 s[16:17], 43, v214
	s_and_b64 s[18:19], s[20:21], s[18:19]
	v_cmp_gt_i32_e64 s[14:15], 42, v214
	s_and_b64 s[16:17], s[18:19], s[16:17]
	v_cmp_gt_i32_e64 s[12:13], 41, v214
	s_and_b64 s[14:15], s[16:17], s[14:15]
	v_cmp_gt_i32_e64 s[10:11], 40, v214
	s_and_b64 s[12:13], s[14:15], s[12:13]
	v_cmp_gt_i32_e64 s[8:9], 35, v214
	s_and_b64 s[10:11], s[12:13], s[10:11]
	v_cmp_gt_i32_e64 s[6:7], 34, v214
	s_and_b64 s[8:9], s[10:11], s[8:9]
	v_cmp_gt_i32_e64 s[4:5], 33, v214
	s_and_b64 s[6:7], s[8:9], s[6:7]
	v_cmp_gt_i32_e32 vcc, 32, v214
	s_and_b64 s[4:5], s[6:7], s[4:5]
	s_and_b64 vcc, s[4:5], vcc
	v_cndmask_b32_e64 v101, v101, v183, s[64:65]
	v_cndmask_b32_e64 v100, v100, v183, s[62:63]
	v_cndmask_b32_e64 v99, v99, v183, s[60:61]
	v_cndmask_b32_e64 v98, v98, v183, s[58:59]
	v_cndmask_b32_e64 v97, v97, v183, s[56:57]
	v_cndmask_b32_e64 v96, v96, v183, s[54:55]
	v_cndmask_b32_e64 v95, v95, v183, s[52:53]
	v_cndmask_b32_e64 v94, v94, v183, s[50:51]
	v_cndmask_b32_e64 v93, v93, v183, s[48:49]
	v_cndmask_b32_e64 v92, v92, v183, s[46:47]
	v_cndmask_b32_e64 v91, v91, v183, s[44:45]
	v_cndmask_b32_e64 v90, v90, v183, s[42:43]
	v_cndmask_b32_e64 v89, v89, v183, s[40:41]
	v_cndmask_b32_e64 v88, v88, v183, s[38:39]
	v_cndmask_b32_e64 v87, v87, v183, s[36:37]
	v_cndmask_b32_e64 v85, v85, v183, s[34:35]
	v_cndmask_b32_e64 v84, v84, v183, s[30:31]
	v_cndmask_b32_e64 v83, v83, v183, s[28:29]
	v_cndmask_b32_e64 v82, v82, v183, s[26:27]
	v_cndmask_b32_e64 v81, v81, v183, s[24:25]
	v_cndmask_b32_e64 v80, v80, v183, s[22:23]
	v_cndmask_b32_e64 v79, v79, v183, s[20:21]
	v_cndmask_b32_e64 v78, v78, v183, s[18:19]
	v_cndmask_b32_e64 v77, v77, v183, s[16:17]
	v_cndmask_b32_e64 v76, v76, v183, s[14:15]
	v_cndmask_b32_e64 v75, v75, v183, s[12:13]
	v_cndmask_b32_e64 v74, v74, v183, s[10:11]
	v_cndmask_b32_e64 v73, v73, v183, s[8:9]
	v_cndmask_b32_e64 v72, v72, v183, s[6:7]
	v_cndmask_b32_e64 v71, v71, v183, s[4:5]
	v_cndmask_b32_e32 v70, v70, v183, vcc
.LBB0_217:
	v_cvt_pk_bf16_f32 v214, v117, v125
	v_cvt_pk_bf16_f32 v117, v126, v164
	s_nop 5
	v_max_f32_e32 v125, v71, v71
	v_max_f32_e32 v126, v70, v70
	v_max_f32_e32 v125, v126, v125
	v_cvt_pk_bf16_f32 v218, v115, v123
	v_max3_f32 v115, v86, v87, v88
	v_max3_f32 v126, v78, v79, v80
	v_max3_f32 v125, v125, v72, v73
	v_cvt_pk_bf16_f32 v120, v116, v120
	v_cvt_pk_bf16_f32 v116, v118, v124
	v_max3_f32 v124, v94, v95, v96
	v_max3_f32 v115, v115, v89, v90
	v_max3_f32 v126, v126, v81, v82
	v_max3_f32 v125, v125, v74, v75
	v_max3_f32 v124, v124, v97, v98
	v_max3_f32 v115, v115, v91, v92
	v_max3_f32 v126, v126, v83, v84
	v_max3_f32 v125, v125, v76, v77
	v_max3_f32 v124, v124, v99, v100
	v_max3_f32 v115, v115, v93, v101
	v_max3_f32 v125, v125, v85, v126
	v_max3_f32 v115, v115, v124, v125
	v_mov_b32_e32 v124, v115
	s_nop 1
	v_permlane32_swap_b32_e32 v115, v124
	v_max_f32_e32 v124, v124, v124
	v_max_f32_e32 v115, v115, v115
	v_max_f32_e32 v115, v115, v124
	v_max_f32_e32 v125, v196, v196
	v_sub_f32_e32 v124, v115, v196
	v_max_f32_e32 v115, v125, v115
	v_sub_f32_e32 v125, v196, v115
	v_exp_f32_e32 v125, v125
	v_cmp_ge_f32_e32 vcc, s78, v124
	s_cmp_eq_u64 vcc, exec
	s_cselect_b64 s[4:5], -1, 0
	v_cvt_pk_bf16_f32 v219, v119, v163
	v_cvt_pk_bf16_f32 v119, v174, v213
	v_cndmask_b32_e64 v213, v125, 1.0, s[4:5]
	v_cvt_pk_bf16_f32 v215, v121, v165
	v_cvt_pk_bf16_f32 v216, v129, v173
	v_cvt_pk_bf16_f32 v217, v169, v177
	v_cvt_pk_bf16_f32 v220, v127, v171
	v_cvt_pk_bf16_f32 v221, v167, v175
	v_cvt_pk_bf16_f32 v121, v122, v128
	v_cvt_pk_bf16_f32 v122, v162, v168
	v_cvt_pk_bf16_f32 v123, v170, v176
	v_cvt_pk_bf16_f32 v118, v166, v172
	ds_read_b64_tr_b16 v[124:125], v114 offset:0x200
	ds_read_b64_tr_b16 v[126:127], v114 offset:0xa00
	ds_read_b64_tr_b16 v[162:163], v114 offset:0x1200
	ds_read_b64_tr_b16 v[164:165], v114 offset:0x1a00
	ds_read_b64_tr_b16 v[166:167], v114 offset:0x2200
	ds_read_b64_tr_b16 v[168:169], v114 offset:0x2a00
	ds_read_b64_tr_b16 v[170:171], v114 offset:0x3200
	ds_read_b64_tr_b16 v[172:173], v114 offset:0x3a00
	s_waitcnt lgkmcnt(8)
	v_mfma_f32_32x32x16_bf16 v[50:65], v[214:217], v[110:113], v[50:65]
	v_mfma_f32_32x32x16_bf16 v[50:65], v[218:221], v[106:109], v[50:65]
	v_mfma_f32_32x32x16_bf16 v[50:65], v[120:123], v[102:105], v[50:65]
	v_mfma_f32_32x32x16_bf16 v[50:65], v[116:119], v[66:69], v[50:65]
	ds_read_b64_tr_b16 v[66:67], v114 offset:0x400
	ds_read_b64_tr_b16 v[68:69], v114 offset:0xc00
	ds_read_b64_tr_b16 v[102:103], v114 offset:0x1400
	ds_read_b64_tr_b16 v[104:105], v114 offset:0x1c00
	ds_read_b64_tr_b16 v[106:107], v114 offset:0x2400
	ds_read_b64_tr_b16 v[108:109], v114 offset:0x2c00
	ds_read_b64_tr_b16 v[110:111], v114 offset:0x3400
	ds_read_b64_tr_b16 v[112:113], v114 offset:0x3c00
	s_waitcnt lgkmcnt(8)
	v_mfma_f32_32x32x16_bf16 v[34:49], v[116:119], v[170:173], v[34:49]
	v_mfma_f32_32x32x16_bf16 v[34:49], v[120:123], v[166:169], v[34:49]
	v_mfma_f32_32x32x16_bf16 v[34:49], v[218:221], v[162:165], v[34:49]
	v_mfma_f32_32x32x16_bf16 v[34:49], v[214:217], v[124:127], v[34:49]
	ds_read_b64_tr_b16 v[124:125], v114 offset:0x600
	ds_read_b64_tr_b16 v[126:127], v114 offset:0xe00
	ds_read_b64_tr_b16 v[162:163], v114 offset:0x1600
	ds_read_b64_tr_b16 v[164:165], v114 offset:0x1e00
	ds_read_b64_tr_b16 v[166:167], v114 offset:0x2600
	ds_read_b64_tr_b16 v[168:169], v114 offset:0x2e00
	ds_read_b64_tr_b16 v[170:171], v114 offset:0x3600
	ds_read_b64_tr_b16 v[172:173], v114 offset:0x3e00
	s_waitcnt lgkmcnt(8)
	v_mfma_f32_32x32x16_bf16 v[18:33], v[214:217], v[66:69], v[18:33]
	v_mfma_f32_32x32x16_bf16 v[18:33], v[218:221], v[102:105], v[18:33]
	v_mfma_f32_32x32x16_bf16 v[18:33], v[120:123], v[106:109], v[18:33]
	v_mfma_f32_32x32x16_bf16 v[18:33], v[116:119], v[110:113], v[18:33]
	s_waitcnt lgkmcnt(0)
	v_mfma_f32_32x32x16_bf16 v[2:17], v[214:217], v[124:127], v[2:17]
	s_waitcnt vmcnt(0)
	v_cmp_gt_f32_e32 vcc, 1.0, v213
	v_mfma_f32_32x32x16_bf16 v[2:17], v[218:221], v[162:165], v[2:17]
	v_mfma_f32_32x32x16_bf16 v[2:17], v[120:123], v[166:169], v[2:17]
	v_mfma_f32_32x32x16_bf16 v[2:17], v[116:119], v[170:173], v[2:17]
	s_cbranch_vccz .LBB0_221
	s_and_saveexec_b64 s[6:7], s[2:3]
	ds_write_b32 v205, v213 offset:128
	s_or_b64 exec, exec, s[6:7]
	s_waitcnt lgkmcnt(0)
	ds_read_b128 v[66:69], v188 offset:224
	ds_read_b128 v[102:105], v188 offset:192
	ds_read_b128 v[106:109], v188 offset:160
	ds_read_b128 v[110:113], v188 offset:128
	s_waitcnt lgkmcnt(3)
	v_pk_mul_f32 v[64:65], v[64:65], v[68:69]
	s_waitcnt lgkmcnt(2)
	v_pk_mul_f32 v[60:61], v[60:61], v[104:105]
	s_waitcnt lgkmcnt(1)
	v_pk_mul_f32 v[56:57], v[56:57], v[108:109]
	s_waitcnt lgkmcnt(0)
	v_pk_mul_f32 v[52:53], v[52:53], v[112:113]
	v_pk_mul_f32 v[62:63], v[62:63], v[66:67]
	v_pk_mul_f32 v[58:59], v[58:59], v[102:103]
	v_pk_mul_f32 v[54:55], v[54:55], v[106:107]
	v_pk_mul_f32 v[50:51], v[50:51], v[110:111]
	v_pk_mul_f32 v[48:49], v[48:49], v[68:69]
	v_pk_mul_f32 v[44:45], v[44:45], v[104:105]
	v_pk_mul_f32 v[40:41], v[40:41], v[108:109]
	v_pk_mul_f32 v[36:37], v[36:37], v[112:113]
	v_pk_mul_f32 v[46:47], v[46:47], v[66:67]
	v_pk_mul_f32 v[42:43], v[42:43], v[102:103]
	v_pk_mul_f32 v[38:39], v[38:39], v[106:107]
	v_pk_mul_f32 v[34:35], v[34:35], v[110:111]
	v_pk_mul_f32 v[32:33], v[32:33], v[68:69]
	v_pk_mul_f32 v[28:29], v[28:29], v[104:105]
	v_pk_mul_f32 v[24:25], v[24:25], v[108:109]
	v_pk_mul_f32 v[20:21], v[20:21], v[112:113]
	v_pk_mul_f32 v[30:31], v[30:31], v[66:67]
	v_pk_mul_f32 v[26:27], v[26:27], v[102:103]
	v_pk_mul_f32 v[22:23], v[22:23], v[106:107]
	v_pk_mul_f32 v[18:19], v[18:19], v[110:111]
	v_pk_mul_f32 v[16:17], v[16:17], v[68:69]
	v_pk_mul_f32 v[12:13], v[12:13], v[104:105]
	v_pk_mul_f32 v[8:9], v[8:9], v[108:109]
	v_pk_mul_f32 v[4:5], v[4:5], v[112:113]
	v_pk_mul_f32 v[14:15], v[14:15], v[66:67]
	v_pk_mul_f32 v[10:11], v[10:11], v[102:103]
	v_pk_mul_f32 v[6:7], v[6:7], v[106:107]
	v_pk_mul_f32 v[2:3], v[2:3], v[110:111]

.LBB0_223:
	v_cndmask_b32_e64 v216, v115, v196, s[4:5]
	v_sub_f32_e32 v66, v86, v216
	v_sub_f32_e32 v67, v87, v216
	v_sub_f32_e32 v68, v88, v216
	v_sub_f32_e32 v69, v89, v216
	v_sub_f32_e32 v86, v90, v216
	v_sub_f32_e32 v87, v91, v216
	v_sub_f32_e32 v88, v92, v216
	v_sub_f32_e32 v89, v93, v216
	v_sub_f32_e32 v90, v94, v216
	v_sub_f32_e32 v91, v95, v216
	v_sub_f32_e32 v92, v96, v216
	v_sub_f32_e32 v93, v97, v216
	v_sub_f32_e32 v94, v98, v216
	v_sub_f32_e32 v95, v99, v216
	v_sub_f32_e32 v96, v100, v216
	v_sub_f32_e32 v97, v101, v216
	v_sub_f32_e32 v98, v70, v216
	v_sub_f32_e32 v99, v71, v216
	v_sub_f32_e32 v100, v72, v216
	v_sub_f32_e32 v101, v73, v216
	v_sub_f32_e32 v102, v74, v216
	v_sub_f32_e32 v103, v75, v216
	v_sub_f32_e32 v104, v76, v216
	v_sub_f32_e32 v105, v77, v216
	v_sub_f32_e32 v106, v78, v216
	v_sub_f32_e32 v107, v79, v216
	v_sub_f32_e32 v108, v80, v216
	v_sub_f32_e32 v109, v81, v216
	v_exp_f32_e32 v66, v66
	v_exp_f32_e32 v67, v67
	v_exp_f32_e32 v68, v68
	v_exp_f32_e32 v69, v69
	v_exp_f32_e32 v70, v86
	v_exp_f32_e32 v71, v87
	v_exp_f32_e32 v72, v88
	v_exp_f32_e32 v73, v89
	v_exp_f32_e32 v74, v90
	v_exp_f32_e32 v75, v91
	v_exp_f32_e32 v76, v92
	v_exp_f32_e32 v77, v93
	v_exp_f32_e32 v78, v94
	v_exp_f32_e32 v79, v95
	v_exp_f32_e32 v80, v96
	v_exp_f32_e32 v81, v97
	v_sub_f32_e32 v110, v82, v216
	v_sub_f32_e32 v95, v83, v216
	v_sub_f32_e32 v96, v84, v216
	v_sub_f32_e32 v97, v85, v216
	v_exp_f32_e32 v82, v98
	v_exp_f32_e32 v83, v99
	v_exp_f32_e32 v90, v106
	v_exp_f32_e32 v91, v107
	v_exp_f32_e32 v84, v100
	v_exp_f32_e32 v92, v108
	v_exp_f32_e32 v85, v101
	v_exp_f32_e32 v93, v109
	v_exp_f32_e32 v86, v102
	v_exp_f32_e32 v94, v110
	v_exp_f32_e32 v87, v103
	v_exp_f32_e32 v95, v95
	v_add_f32_e32 v98, v66, v67
	v_add_f32_e32 v99, v74, v75
	v_add_f32_e32 v100, v82, v83
	v_add_f32_e32 v101, v90, v91
	v_exp_f32_e32 v88, v104
	v_exp_f32_e32 v96, v96
	v_add_f32_e32 v98, v68, v98
	v_add_f32_e32 v99, v76, v99
	v_add_f32_e32 v100, v84, v100
	v_add_f32_e32 v101, v92, v101
	v_exp_f32_e32 v89, v105
	v_exp_f32_e32 v97, v97
	v_add_f32_e32 v98, v69, v98
	v_add_f32_e32 v99, v77, v99
	v_add_f32_e32 v100, v85, v100
	v_add_f32_e32 v101, v93, v101
	v_add_f32_e32 v98, v70, v98
	v_add_f32_e32 v99, v78, v99
	v_add_f32_e32 v100, v86, v100
	v_add_f32_e32 v101, v94, v101
	v_add_f32_e32 v98, v71, v98
	v_add_f32_e32 v99, v79, v99
	v_add_f32_e32 v100, v87, v100
	v_add_f32_e32 v101, v95, v101
	v_add_f32_e32 v98, v72, v98
	v_add_f32_e32 v99, v80, v99
	v_add_f32_e32 v100, v88, v100
	v_add_f32_e32 v101, v96, v101
	v_add_f32_e32 v98, v73, v98
	v_add_f32_e32 v99, v81, v99
	v_add_f32_e32 v100, v89, v100
	v_add_f32_e32 v101, v97, v101
	v_add_f32_e32 v98, v99, v98
	v_add_f32_e32 v99, v101, v100
	v_add_f32_e32 v214, v99, v98
	v_mov_b32_e32 v215, v214
	s_nop 1
	v_permlane32_swap_b32_e32 v214, v215
	ds_read_b128 v[114:117], v207
	ds_read_b128 v[118:121], v207 offset:32
	ds_read_b128 v[98:101], v207 offset:128
	ds_read_b128 v[102:105], v207 offset:160
	ds_read_b128 v[122:125], v207 offset:64
	ds_read_b128 v[126:129], v207 offset:96
	ds_read_b128 v[106:109], v207 offset:192
	ds_read_b128 v[110:113], v207 offset:224
	ds_read_b128 v[162:165], v199 offset:49152
	ds_read_b128 v[166:169], v199 offset:57344
	ds_read_b128 v[170:173], v200 offset:57344
	ds_read_b128 v[174:177], v200 offset:49152
	ds_read_b128 v[218:221], v201 offset:49152
	ds_read_b128 v[222:225], v201 offset:57344
	ds_read_b128 v[226:229], v202 offset:57344
	ds_read_b128 v[230:233], v202 offset:49152
	s_waitcnt lgkmcnt(7)
	v_mfma_f32_32x32x16_bf16 v[114:129], v[162:165], v[158:161], v[114:129]
	ds_read_b128 v[162:165], v199 offset:49280
	ds_read_b128 v[234:237], v199 offset:57472
	s_waitcnt lgkmcnt(8)
	v_mfma_f32_32x32x16_bf16 v[98:113], v[166:169], v[158:161], v[98:113]
	s_waitcnt lgkmcnt(7)
	v_mfma_f32_32x32x16_bf16 v[98:113], v[170:173], v[154:157], v[98:113]
	ds_read_b128 v[166:169], v200 offset:57472
	ds_read_b128 v[170:173], v200 offset:49280
	s_waitcnt lgkmcnt(8)
	v_mfma_f32_32x32x16_bf16 v[114:129], v[174:177], v[154:157], v[114:129]
	s_waitcnt lgkmcnt(7)
	v_mfma_f32_32x32x16_bf16 v[114:129], v[218:221], v[150:153], v[114:129]
	ds_read_b128 v[174:177], v201 offset:49280
	ds_read_b128 v[218:221], v201 offset:57472
	s_waitcnt lgkmcnt(8)
	v_mfma_f32_32x32x16_bf16 v[98:113], v[222:225], v[150:153], v[98:113]
	s_waitcnt lgkmcnt(7)
	v_mfma_f32_32x32x16_bf16 v[98:113], v[226:229], v[146:149], v[98:113]
	ds_read_b128 v[222:225], v202 offset:57472
	ds_read_b128 v[226:229], v202 offset:49280
	s_waitcnt lgkmcnt(8)
	v_mfma_f32_32x32x16_bf16 v[114:129], v[230:233], v[146:149], v[114:129]
	s_waitcnt lgkmcnt(7)
	v_mfma_f32_32x32x16_bf16 v[114:129], v[162:165], v[142:145], v[114:129]
	s_waitcnt lgkmcnt(6)
	v_mfma_f32_32x32x16_bf16 v[98:113], v[234:237], v[142:145], v[98:113]
	s_waitcnt lgkmcnt(5)
	v_mfma_f32_32x32x16_bf16 v[98:113], v[166:169], v[138:141], v[98:113]
	s_waitcnt lgkmcnt(4)
	v_mfma_f32_32x32x16_bf16 v[114:129], v[170:173], v[138:141], v[114:129]
	s_waitcnt lgkmcnt(3)
	v_mfma_f32_32x32x16_bf16 v[114:129], v[174:177], v[134:137], v[114:129]
	s_waitcnt lgkmcnt(2)
	v_mfma_f32_32x32x16_bf16 v[98:113], v[218:221], v[134:137], v[98:113]
	s_waitcnt lgkmcnt(1)
	v_mfma_f32_32x32x16_bf16 v[98:113], v[222:225], v[130:133], v[98:113]
	s_waitcnt lgkmcnt(0)
	v_mfma_f32_32x32x16_bf16 v[114:129], v[226:229], v[130:133], v[114:129]
	v_add_u32_e32 v196, s33, v190
	ds_read_b64_tr_b16 v[174:175], v196 offset:0
	ds_read_b64_tr_b16 v[176:177], v196 offset:0x800
	ds_read_b64_tr_b16 v[170:171], v196 offset:0x1000
	ds_read_b64_tr_b16 v[172:173], v196 offset:0x1800
	ds_read_b64_tr_b16 v[166:167], v196 offset:0x2000
	ds_read_b64_tr_b16 v[168:169], v196 offset:0x2800
	ds_read_b64_tr_b16 v[162:163], v196 offset:0x3000
	ds_read_b64_tr_b16 v[164:165], v196 offset:0x3800
	s_cmp_le_i32 s88, s70
	s_cbranch_scc1 .LBB0_225
	v_cmp_gt_i32_e64 s[62:63], 26, v206
	v_cmp_gt_i32_e64 s[64:65], 27, v206
	v_cmp_gt_i32_e64 s[60:61], 25, v206
	s_and_b64 s[62:63], s[64:65], s[62:63]
	v_cmp_gt_i32_e64 s[58:59], 24, v206
	s_and_b64 s[60:61], s[62:63], s[60:61]
	v_cmp_gt_i32_e64 s[56:57], 19, v206
	s_and_b64 s[58:59], s[60:61], s[58:59]
	v_cmp_gt_i32_e64 s[54:55], 18, v206
	s_and_b64 s[56:57], s[58:59], s[56:57]
	v_cmp_gt_i32_e64 s[52:53], 17, v206
	s_and_b64 s[54:55], s[56:57], s[54:55]
	v_cmp_gt_i32_e64 s[50:51], 16, v206
	s_and_b64 s[52:53], s[54:55], s[52:53]
	v_cmp_gt_i32_e64 s[48:49], 11, v206
	s_and_b64 s[50:51], s[52:53], s[50:51]
	v_cmp_gt_i32_e64 s[46:47], 10, v206
	s_and_b64 s[48:49], s[50:51], s[48:49]
	v_cmp_gt_i32_e64 s[44:45], 9, v206
	s_and_b64 s[46:47], s[48:49], s[46:47]
	v_cmp_gt_i32_e64 s[42:43], 8, v206
	s_and_b64 s[44:45], s[46:47], s[44:45]
	v_cmp_gt_i32_e64 s[40:41], 3, v206
	s_and_b64 s[42:43], s[44:45], s[42:43]
	v_cmp_gt_i32_e64 s[38:39], 2, v206
	s_and_b64 s[40:41], s[42:43], s[40:41]
	v_cmp_gt_i32_e64 s[36:37], 1, v206
	s_and_b64 s[38:39], s[40:41], s[38:39]
	v_cmp_gt_i32_e64 s[34:35], 0, v206
	s_and_b64 s[36:37], s[38:39], s[36:37]
	s_and_b64 s[34:35], s[36:37], s[34:35]
	v_cmp_gt_i32_e64 s[30:31], 58, v206
	v_cndmask_b32_e64 v114, v114, v183, s[34:35]
	v_cmp_gt_i32_e64 s[34:35], 59, v206
	v_cmp_gt_i32_e64 s[28:29], 57, v206
	s_and_b64 s[30:31], s[34:35], s[30:31]
	v_cmp_gt_i32_e64 s[26:27], 56, v206
	s_and_b64 s[28:29], s[30:31], s[28:29]
	v_cmp_gt_i32_e64 s[24:25], 51, v206
	s_and_b64 s[26:27], s[28:29], s[26:27]
	v_cmp_gt_i32_e64 s[22:23], 50, v206
	s_and_b64 s[24:25], s[26:27], s[24:25]
	v_cmp_gt_i32_e64 s[20:21], 49, v206
	s_and_b64 s[22:23], s[24:25], s[22:23]
	v_cmp_gt_i32_e64 s[18:19], 48, v206
	s_and_b64 s[20:21], s[22:23], s[20:21]
	v_cmp_gt_i32_e64 s[16:17], 43, v206
	s_and_b64 s[18:19], s[20:21], s[18:19]
	v_cmp_gt_i32_e64 s[14:15], 42, v206
	s_and_b64 s[16:17], s[18:19], s[16:17]
	v_cmp_gt_i32_e64 s[12:13], 41, v206
	s_and_b64 s[14:15], s[16:17], s[14:15]
	v_cmp_gt_i32_e64 s[10:11], 40, v206
	s_and_b64 s[12:13], s[14:15], s[12:13]
	v_cmp_gt_i32_e64 s[8:9], 35, v206
	s_and_b64 s[10:11], s[12:13], s[10:11]
	v_cmp_gt_i32_e64 s[6:7], 34, v206
	s_and_b64 s[8:9], s[10:11], s[8:9]
	v_cmp_gt_i32_e64 s[4:5], 33, v206
	s_and_b64 s[6:7], s[8:9], s[6:7]
	v_cmp_gt_i32_e32 vcc, 32, v206
	s_and_b64 s[4:5], s[6:7], s[4:5]
	s_and_b64 vcc, s[4:5], vcc
	v_cndmask_b32_e64 v129, v129, v183, s[64:65]
	v_cndmask_b32_e64 v128, v128, v183, s[62:63]
	v_cndmask_b32_e64 v127, v127, v183, s[60:61]
	v_cndmask_b32_e64 v126, v126, v183, s[58:59]
	v_cndmask_b32_e64 v125, v125, v183, s[56:57]
	v_cndmask_b32_e64 v124, v124, v183, s[54:55]
	v_cndmask_b32_e64 v123, v123, v183, s[52:53]
	v_cndmask_b32_e64 v122, v122, v183, s[50:51]
	v_cndmask_b32_e64 v121, v121, v183, s[48:49]
	v_cndmask_b32_e64 v120, v120, v183, s[46:47]
	v_cndmask_b32_e64 v119, v119, v183, s[44:45]
	v_cndmask_b32_e64 v118, v118, v183, s[42:43]
	v_cndmask_b32_e64 v117, v117, v183, s[40:41]
	v_cndmask_b32_e64 v116, v116, v183, s[38:39]
	v_cndmask_b32_e64 v115, v115, v183, s[36:37]
	v_cndmask_b32_e64 v113, v113, v183, s[34:35]
	v_cndmask_b32_e64 v112, v112, v183, s[30:31]
	v_cndmask_b32_e64 v111, v111, v183, s[28:29]
	v_cndmask_b32_e64 v110, v110, v183, s[26:27]
	v_cndmask_b32_e64 v109, v109, v183, s[24:25]
	v_cndmask_b32_e64 v108, v108, v183, s[22:23]
	v_cndmask_b32_e64 v107, v107, v183, s[20:21]
	v_cndmask_b32_e64 v106, v106, v183, s[18:19]
	v_cndmask_b32_e64 v105, v105, v183, s[16:17]
	v_cndmask_b32_e64 v104, v104, v183, s[14:15]
	v_cndmask_b32_e64 v103, v103, v183, s[12:13]
	v_cndmask_b32_e64 v102, v102, v183, s[10:11]
	v_cndmask_b32_e64 v101, v101, v183, s[8:9]
	v_cndmask_b32_e64 v100, v100, v183, s[6:7]
	v_cndmask_b32_e64 v99, v99, v183, s[4:5]
	v_cndmask_b32_e32 v98, v98, v183, vcc
.LBB0_225:
	s_nop 8
	v_max_f32_e32 v235, v99, v99
	v_max_f32_e32 v236, v98, v98
	v_max_f32_e32 v235, v236, v235
	v_max3_f32 v217, v114, v115, v116
	v_max3_f32 v236, v106, v107, v108
	v_max3_f32 v235, v235, v100, v101
	v_max3_f32 v234, v122, v123, v124
	v_max3_f32 v217, v217, v117, v118
	v_max3_f32 v236, v236, v109, v110
	v_max3_f32 v235, v235, v102, v103
	v_max3_f32 v234, v234, v125, v126
	v_max3_f32 v217, v217, v119, v120
	v_max3_f32 v236, v236, v111, v112
	v_max3_f32 v235, v235, v104, v105
	v_max3_f32 v234, v234, v127, v128
	v_max3_f32 v217, v217, v121, v129
	v_max3_f32 v235, v235, v113, v236
	v_max3_f32 v217, v217, v234, v235
	v_mov_b32_e32 v234, v217
	s_nop 1
	v_permlane32_swap_b32_e32 v217, v234
	v_max_f32_e32 v234, v234, v234
	v_max_f32_e32 v217, v217, v217
	v_max_f32_e32 v217, v217, v234
	v_sub_f32_e32 v234, v217, v216
	v_cmp_ge_f32_e32 vcc, s78, v234
	s_cmp_eq_u64 vcc, exec
	s_cselect_b64 s[4:5], -1, 0
	v_cvt_pk_bf16_f32 v218, v66, v67
	v_cvt_pk_bf16_f32 v219, v68, v69
	v_cvt_pk_bf16_f32 v220, v70, v71
	v_cvt_pk_bf16_f32 v221, v72, v73
	v_cvt_pk_bf16_f32 v222, v74, v75
	v_cvt_pk_bf16_f32 v223, v76, v77
	v_cvt_pk_bf16_f32 v224, v78, v79
	v_cvt_pk_bf16_f32 v225, v80, v81
	v_cvt_pk_bf16_f32 v226, v82, v83
	v_cvt_pk_bf16_f32 v227, v84, v85
	v_cvt_pk_bf16_f32 v228, v86, v87
	v_cvt_pk_bf16_f32 v229, v88, v89
	v_cvt_pk_bf16_f32 v230, v90, v91
	v_cvt_pk_bf16_f32 v231, v92, v93
	v_cvt_pk_bf16_f32 v232, v94, v95
	v_cvt_pk_bf16_f32 v233, v96, v97
	ds_read_b64_tr_b16 v[234:235], v196 offset:0x200
	ds_read_b64_tr_b16 v[236:237], v196 offset:0xa00
	ds_read_b64_tr_b16 v[238:239], v196 offset:0x1200
	ds_read_b64_tr_b16 v[240:241], v196 offset:0x1a00
	ds_read_b64_tr_b16 v[242:243], v196 offset:0x2200
	ds_read_b64_tr_b16 v[244:245], v196 offset:0x2a00
	ds_read_b64_tr_b16 v[246:247], v196 offset:0x3200
	ds_read_b64_tr_b16 v[248:249], v196 offset:0x3a00
	s_waitcnt lgkmcnt(8)
	v_mfma_f32_32x32x16_bf16 v[50:65], v[218:221], v[174:177], v[50:65]
	v_mfma_f32_32x32x16_bf16 v[50:65], v[222:225], v[170:173], v[50:65]
	v_mfma_f32_32x32x16_bf16 v[50:65], v[226:229], v[166:169], v[50:65]
	v_mfma_f32_32x32x16_bf16 v[50:65], v[230:233], v[162:165], v[50:65]
	ds_read_b64_tr_b16 v[162:163], v196 offset:0x400
	ds_read_b64_tr_b16 v[164:165], v196 offset:0xc00
	ds_read_b64_tr_b16 v[166:167], v196 offset:0x1400
	ds_read_b64_tr_b16 v[168:169], v196 offset:0x1c00
	ds_read_b64_tr_b16 v[170:171], v196 offset:0x2400
	ds_read_b64_tr_b16 v[172:173], v196 offset:0x2c00
	ds_read_b64_tr_b16 v[174:175], v196 offset:0x3400
	ds_read_b64_tr_b16 v[176:177], v196 offset:0x3c00
	s_waitcnt lgkmcnt(8)
	v_mfma_f32_32x32x16_bf16 v[34:49], v[230:233], v[246:249], v[34:49]
	v_mfma_f32_32x32x16_bf16 v[34:49], v[226:229], v[242:245], v[34:49]
	v_mfma_f32_32x32x16_bf16 v[34:49], v[222:225], v[238:241], v[34:49]
	v_mfma_f32_32x32x16_bf16 v[34:49], v[218:221], v[234:237], v[34:49]
	ds_read_b64_tr_b16 v[234:235], v196 offset:0x600
	ds_read_b64_tr_b16 v[236:237], v196 offset:0xe00
	ds_read_b64_tr_b16 v[238:239], v196 offset:0x1600
	ds_read_b64_tr_b16 v[240:241], v196 offset:0x1e00
	ds_read_b64_tr_b16 v[242:243], v196 offset:0x2600
	ds_read_b64_tr_b16 v[244:245], v196 offset:0x2e00
	ds_read_b64_tr_b16 v[246:247], v196 offset:0x3600
	ds_read_b64_tr_b16 v[248:249], v196 offset:0x3e00
	s_waitcnt lgkmcnt(8)
	v_mfma_f32_32x32x16_bf16 v[18:33], v[218:221], v[162:165], v[18:33]
	v_mfma_f32_32x32x16_bf16 v[18:33], v[222:225], v[166:169], v[18:33]
	v_mfma_f32_32x32x16_bf16 v[18:33], v[226:229], v[170:173], v[18:33]
	v_mfma_f32_32x32x16_bf16 v[18:33], v[230:233], v[174:177], v[18:33]
	s_waitcnt lgkmcnt(0)
	v_mfma_f32_32x32x16_bf16 v[2:17], v[218:221], v[234:237], v[2:17]
	s_andn2_b64 vcc, exec, s[72:73]
	v_mfma_f32_32x32x16_bf16 v[2:17], v[222:225], v[238:241], v[2:17]
	v_mfma_f32_32x32x16_bf16 v[2:17], v[226:229], v[242:245], v[2:17]
	v_mfma_f32_32x32x16_bf16 v[2:17], v[230:233], v[246:249], v[2:17]
	s_cbranch_vccnz .LBB0_227
	s_waitcnt vmcnt(0)

.LBB0_249:
	s_add_i32 s62, s76, 1
	s_cmp_lt_u32 s62, s65
	s_cselect_b32 s2, s62, s76
	s_lshl_b32 s2, s2, 2
	s_lshr_b32 s2, s96, s2
	s_lshl_b32 s2, s2, 8
	s_and_b32 s33, s2, 0xf00
	v_or_b32_e32 v111, s33, v201
	v_add_u32_e32 v114, s78, v111
	v_ashrrev_i32_e32 v115, 31, v114
	v_lshlrev_b64 v[114:115], 8, v[114:115]
	v_lshl_add_u64 v[114:115], s[86:87], 0, v[114:115]
	v_lshl_add_u64 v[114:115], v[114:115], 0, v[174:175]
	global_load_dwordx4 v[170:173], v[114:115], off
	global_load_dwordx4 v[166:169], v[114:115], off offset:32
	global_load_dwordx4 v[162:165], v[114:115], off offset:64
	global_load_dwordx4 v[158:161], v[114:115], off offset:96
	global_load_dwordx4 v[154:157], v[114:115], off offset:128
	global_load_dwordx4 v[150:153], v[114:115], off offset:160
	global_load_dwordx4 v[146:149], v[114:115], off offset:192
	global_load_dwordx4 v[142:145], v[114:115], off offset:224
	v_exp_f32_e32 v132, v110
	v_exp_f32_e32 v140, v1
	v_exp_f32_e32 v130, v104
	v_exp_f32_e32 v138, v105
	v_exp_f32_e32 v136, v112
	v_exp_f32_e32 v134, v102
	v_exp_f32_e32 v182, v113
	v_exp_f32_e32 v180, v103
	v_exp_f32_e32 v178, v108
	v_exp_f32_e32 v176, v100
	v_exp_f32_e32 v190, v109
	v_exp_f32_e32 v188, v101
	v_exp_f32_e32 v184, v98
	v_exp_f32_e32 v192, v99
	v_pk_add_f32 v[98:99], v[132:133], v[140:141]
	v_pk_add_f32 v[100:101], v[130:131], v[138:139]
	v_exp_f32_e32 v186, v106
	v_pk_add_f32 v[98:99], v[136:137], v[98:99]
	v_pk_add_f32 v[100:101], v[134:135], v[100:101]
	v_exp_f32_e32 v194, v107
	v_pk_add_f32 v[98:99], v[182:183], v[98:99]
	v_pk_add_f32 v[100:101], v[180:181], v[100:101]
	v_add_u32_e32 v174, s69, v206
	ds_read_b64_tr_b16 v[114:115], v174 offset:0
	v_pk_add_f32 v[98:99], v[178:179], v[98:99]
	v_pk_add_f32 v[100:101], v[176:177], v[100:101]
	ds_read_b64_tr_b16 v[116:117], v174 offset:0x800
	v_pk_add_f32 v[98:99], v[190:191], v[98:99]
	v_pk_add_f32 v[100:101], v[188:189], v[100:101]
	ds_read_b64_tr_b16 v[118:119], v174 offset:0x1000
	v_pk_add_f32 v[98:99], v[186:187], v[98:99]
	v_pk_add_f32 v[100:101], v[184:185], v[100:101]
	ds_read_b64_tr_b16 v[120:121], v174 offset:0x1800
	v_pk_add_f32 v[98:99], v[194:195], v[98:99]
	v_pk_add_f32 v[100:101], v[192:193], v[100:101]
	ds_read_b64_tr_b16 v[110:111], v174 offset:0x2000
	ds_read_b64_tr_b16 v[112:113], v174 offset:0x2800
	ds_read_b64_tr_b16 v[122:123], v174 offset:0x3000
	ds_read_b64_tr_b16 v[124:125], v174 offset:0x3800
	v_cvt_pk_bf16_f32 v102, v131, v139
	v_pk_add_f32 v[98:99], v[100:101], v[98:99]
	v_cvt_pk_bf16_f32 v100, v179, v191
	v_pk_add_f32 v[98:99], v[98:99], v[98:99] op_sel:[0,1] op_sel_hi:[1,0]
	v_cvt_pk_bf16_f32 v101, v187, v195
	v_mov_b32_e32 v1, v98
	s_nop 1
	v_permlane32_swap_b32_e32 v98, v1
	v_add_f32_e32 v1, v98, v1
	v_fmac_f32_e32 v1, v209, v208
	v_cvt_pk_bf16_f32 v98, v133, v141
	v_cvt_pk_bf16_f32 v99, v137, v183
	v_cvt_pk_bf16_f32 v103, v135, v181
	v_cvt_pk_bf16_f32 v104, v177, v189
	v_cvt_pk_bf16_f32 v105, v185, v193
	v_cvt_pk_bf16_f32 v106, v132, v140
	v_cvt_pk_bf16_f32 v107, v136, v182
	v_cvt_pk_bf16_f32 v108, v178, v190
	v_cvt_pk_bf16_f32 v109, v186, v194
	v_cvt_pk_bf16_f32 v126, v130, v138
	v_cvt_pk_bf16_f32 v127, v134, v180
	v_cvt_pk_bf16_f32 v128, v176, v188
	v_cvt_pk_bf16_f32 v129, v184, v192
	ds_read_b64_tr_b16 v[130:131], v174 offset:0x200
	ds_read_b64_tr_b16 v[132:133], v174 offset:0xa00
	ds_read_b64_tr_b16 v[134:135], v174 offset:0x1200
	ds_read_b64_tr_b16 v[136:137], v174 offset:0x1a00
	ds_read_b64_tr_b16 v[138:139], v174 offset:0x2200
	ds_read_b64_tr_b16 v[140:141], v174 offset:0x2a00
	ds_read_b64_tr_b16 v[176:177], v174 offset:0x3200
	ds_read_b64_tr_b16 v[178:179], v174 offset:0x3a00
	s_waitcnt lgkmcnt(8)
	v_mfma_f32_32x32x16_bf16 v[50:65], v[98:101], v[114:117], v[50:65]
	v_mfma_f32_32x32x16_bf16 v[50:65], v[102:105], v[118:121], v[50:65]
	v_mfma_f32_32x32x16_bf16 v[50:65], v[106:109], v[110:113], v[50:65]
	v_mfma_f32_32x32x16_bf16 v[50:65], v[126:129], v[122:125], v[50:65]
	ds_read_b64_tr_b16 v[110:111], v174 offset:0x400
	ds_read_b64_tr_b16 v[112:113], v174 offset:0xc00
	ds_read_b64_tr_b16 v[114:115], v174 offset:0x1400
	ds_read_b64_tr_b16 v[116:117], v174 offset:0x1c00
	ds_read_b64_tr_b16 v[118:119], v174 offset:0x2400
	ds_read_b64_tr_b16 v[120:121], v174 offset:0x2c00
	ds_read_b64_tr_b16 v[122:123], v174 offset:0x3400
	ds_read_b64_tr_b16 v[124:125], v174 offset:0x3c00
	s_waitcnt lgkmcnt(8)
	v_mfma_f32_32x32x16_bf16 v[34:49], v[126:129], v[176:179], v[34:49]
	v_mfma_f32_32x32x16_bf16 v[34:49], v[106:109], v[138:141], v[34:49]
	v_mfma_f32_32x32x16_bf16 v[34:49], v[102:105], v[134:137], v[34:49]
	v_mfma_f32_32x32x16_bf16 v[34:49], v[98:101], v[130:133], v[34:49]
	ds_read_b64_tr_b16 v[130:131], v174 offset:0x600
	ds_read_b64_tr_b16 v[132:133], v174 offset:0xe00
	ds_read_b64_tr_b16 v[134:135], v174 offset:0x1600
	ds_read_b64_tr_b16 v[136:137], v174 offset:0x1e00
	ds_read_b64_tr_b16 v[138:139], v174 offset:0x2600
	ds_read_b64_tr_b16 v[140:141], v174 offset:0x2e00
	ds_read_b64_tr_b16 v[176:177], v174 offset:0x3600
	ds_read_b64_tr_b16 v[178:179], v174 offset:0x3e00
	s_waitcnt lgkmcnt(8)
	v_mfma_f32_32x32x16_bf16 v[18:33], v[98:101], v[110:113], v[18:33]
	v_mfma_f32_32x32x16_bf16 v[18:33], v[102:105], v[114:117], v[18:33]
	v_mfma_f32_32x32x16_bf16 v[18:33], v[106:109], v[118:121], v[18:33]
	v_mfma_f32_32x32x16_bf16 v[18:33], v[126:129], v[122:125], v[18:33]
	s_waitcnt lgkmcnt(0)
	v_mfma_f32_32x32x16_bf16 v[2:17], v[98:101], v[130:133], v[2:17]
	s_andn2_b64 vcc, exec, s[0:1]
	v_mfma_f32_32x32x16_bf16 v[2:17], v[102:105], v[134:137], v[2:17]
	v_mfma_f32_32x32x16_bf16 v[2:17], v[106:109], v[138:141], v[2:17]
	v_mfma_f32_32x32x16_bf16 v[2:17], v[126:129], v[176:179], v[2:17]
	s_cbranch_vccnz .LBB0_257
	s_sub_i32 s0, s77, s79
	s_lshl_b32 s0, s0, 6
	s_or_b32 s1, s0, 63
	s_cmp_le_i32 s1, s66
	s_cbranch_scc1 .LBB0_252
	v_subrev_u32_e32 v98, s0, v205
	v_cmp_gt_i32_e64 s[58:59], 26, v98
	v_cmp_gt_i32_e64 s[60:61], 27, v98
	v_cmp_gt_i32_e64 s[56:57], 25, v98
	s_and_b64 s[58:59], s[60:61], s[58:59]
	v_cmp_gt_i32_e64 s[54:55], 24, v98
	s_and_b64 s[56:57], s[58:59], s[56:57]
	v_cmp_gt_i32_e64 s[52:53], 19, v98
	s_and_b64 s[54:55], s[56:57], s[54:55]
	v_cmp_gt_i32_e64 s[50:51], 18, v98
	s_and_b64 s[52:53], s[54:55], s[52:53]
	v_cmp_gt_i32_e64 s[48:49], 17, v98
	s_and_b64 s[50:51], s[52:53], s[50:51]
	v_cmp_gt_i32_e64 s[46:47], 16, v98
	s_and_b64 s[48:49], s[50:51], s[48:49]
	v_cmp_gt_i32_e64 s[44:45], 11, v98
	s_and_b64 s[46:47], s[48:49], s[46:47]
	v_cmp_gt_i32_e64 s[42:43], 10, v98
	s_and_b64 s[44:45], s[46:47], s[44:45]
	v_cmp_gt_i32_e64 s[40:41], 9, v98
	s_and_b64 s[42:43], s[44:45], s[42:43]
	v_cmp_gt_i32_e64 s[38:39], 8, v98
	s_and_b64 s[40:41], s[42:43], s[40:41]
	v_cmp_gt_i32_e64 s[36:37], 3, v98
	s_and_b64 s[38:39], s[40:41], s[38:39]
	v_cmp_gt_i32_e64 s[34:35], 2, v98
	s_and_b64 s[36:37], s[38:39], s[36:37]
	v_cmp_gt_i32_e64 s[30:31], 1, v98
	s_and_b64 s[34:35], s[36:37], s[34:35]
	v_cmp_gt_i32_e64 s[28:29], 0, v98
	s_and_b64 s[30:31], s[34:35], s[30:31]
	s_and_b64 s[28:29], s[30:31], s[28:29]
	v_cmp_gt_i32_e64 s[26:27], 58, v98
	v_cndmask_b32_e64 v66, v66, v199, s[28:29]
	v_cmp_gt_i32_e64 s[28:29], 59, v98
	v_cmp_gt_i32_e64 s[24:25], 57, v98
	s_and_b64 s[26:27], s[28:29], s[26:27]
	v_cmp_gt_i32_e64 s[22:23], 56, v98
	s_and_b64 s[24:25], s[26:27], s[24:25]
	v_cmp_gt_i32_e64 s[20:21], 51, v98
	s_and_b64 s[22:23], s[24:25], s[22:23]
	v_cmp_gt_i32_e64 s[18:19], 50, v98
	s_and_b64 s[20:21], s[22:23], s[20:21]
	v_cmp_gt_i32_e64 s[16:17], 49, v98
	s_and_b64 s[18:19], s[20:21], s[18:19]
	v_cmp_gt_i32_e64 s[14:15], 48, v98
	s_and_b64 s[16:17], s[18:19], s[16:17]
	v_cmp_gt_i32_e64 s[12:13], 43, v98
	s_and_b64 s[14:15], s[16:17], s[14:15]
	v_cmp_gt_i32_e64 s[10:11], 42, v98
	s_and_b64 s[12:13], s[14:15], s[12:13]
	v_cmp_gt_i32_e64 s[8:9], 41, v98
	s_and_b64 s[10:11], s[12:13], s[10:11]
	v_cmp_gt_i32_e64 s[6:7], 40, v98
	s_and_b64 s[8:9], s[10:11], s[8:9]
	v_cmp_gt_i32_e64 s[4:5], 35, v98
	s_and_b64 s[6:7], s[8:9], s[6:7]
	v_cmp_gt_i32_e64 s[2:3], 34, v98
	s_and_b64 s[4:5], s[6:7], s[4:5]
	v_cmp_gt_i32_e64 s[0:1], 33, v98
	s_and_b64 s[2:3], s[4:5], s[2:3]
	v_cmp_gt_i32_e32 vcc, 32, v98
	s_and_b64 s[0:1], s[2:3], s[0:1]
	s_and_b64 vcc, s[0:1], vcc
	v_cndmask_b32_e64 v81, v81, v199, s[60:61]
	v_cndmask_b32_e64 v80, v80, v199, s[58:59]
	v_cndmask_b32_e64 v79, v79, v199, s[56:57]
	v_cndmask_b32_e64 v78, v78, v199, s[54:55]
	v_cndmask_b32_e64 v77, v77, v199, s[52:53]
	v_cndmask_b32_e64 v76, v76, v199, s[50:51]
	v_cndmask_b32_e64 v75, v75, v199, s[48:49]
	v_cndmask_b32_e64 v74, v74, v199, s[46:47]
	v_cndmask_b32_e64 v73, v73, v199, s[44:45]
	v_cndmask_b32_e64 v72, v72, v199, s[42:43]
	v_cndmask_b32_e64 v71, v71, v199, s[40:41]
	v_cndmask_b32_e64 v70, v70, v199, s[38:39]
	v_cndmask_b32_e64 v69, v69, v199, s[36:37]
	v_cndmask_b32_e64 v68, v68, v199, s[34:35]
	v_cndmask_b32_e64 v67, v67, v199, s[30:31]
	v_cndmask_b32_e64 v97, v97, v199, s[28:29]
	v_cndmask_b32_e64 v96, v96, v199, s[26:27]
	v_cndmask_b32_e64 v95, v95, v199, s[24:25]
	v_cndmask_b32_e64 v94, v94, v199, s[22:23]
	v_cndmask_b32_e64 v93, v93, v199, s[20:21]
	v_cndmask_b32_e64 v92, v92, v199, s[18:19]
	v_cndmask_b32_e64 v91, v91, v199, s[16:17]
	v_cndmask_b32_e64 v90, v90, v199, s[14:15]
	v_cndmask_b32_e64 v89, v89, v199, s[12:13]
	v_cndmask_b32_e64 v88, v88, v199, s[10:11]
	v_cndmask_b32_e64 v87, v87, v199, s[8:9]
	v_cndmask_b32_e64 v86, v86, v199, s[6:7]
	v_cndmask_b32_e64 v85, v85, v199, s[4:5]
	v_cndmask_b32_e64 v84, v84, v199, s[2:3]
	v_cndmask_b32_e64 v83, v83, v199, s[0:1]
	v_cndmask_b32_e32 v82, v82, v199, vcc

.LBB0_256:
	v_cndmask_b32_e64 v98, v98, v207, s[0:1]
	v_sub_f32_e32 v66, v66, v98
	v_sub_f32_e32 v67, v67, v98
	v_sub_f32_e32 v70, v70, v98
	v_sub_f32_e32 v74, v74, v98
	v_sub_f32_e32 v68, v68, v98
	v_sub_f32_e32 v99, v69, v98
	v_sub_f32_e32 v71, v71, v98
	v_sub_f32_e32 v72, v72, v98
	v_sub_f32_e32 v100, v73, v98
	v_sub_f32_e32 v75, v75, v98
	v_sub_f32_e32 v76, v76, v98
	v_sub_f32_e32 v102, v77, v98
	v_sub_f32_e32 v104, v81, v98
	v_exp_f32_e32 v69, v66
	v_exp_f32_e32 v77, v67
	v_exp_f32_e32 v81, v70
	v_exp_f32_e32 v67, v74
	v_sub_f32_e32 v66, v82, v98
	v_sub_f32_e32 v70, v83, v98
	v_sub_f32_e32 v74, v85, v98
	v_sub_f32_e32 v110, v90, v98
	v_sub_f32_e32 v115, v91, v98
	v_exp_f32_e32 v73, v68
	v_exp_f32_e32 v109, v71
	v_exp_f32_e32 v105, v72
	v_exp_f32_e32 v113, v100
	v_exp_f32_e32 v75, v75
	v_exp_f32_e32 v71, v76
	v_sub_f32_e32 v72, v84, v98
	v_sub_f32_e32 v116, v92, v98
	v_exp_f32_e32 v68, v66
	v_exp_f32_e32 v76, v70
	v_exp_f32_e32 v100, v74
	v_exp_f32_e32 v66, v110
	v_exp_f32_e32 v74, v115
	v_sub_f32_e32 v78, v78, v98
	v_sub_f32_e32 v117, v93, v98
	v_exp_f32_e32 v72, v72
	v_exp_f32_e32 v70, v116
	v_sub_f32_e32 v103, v79, v98
	v_sub_f32_e32 v80, v80, v98
	v_exp_f32_e32 v101, v99
	v_exp_f32_e32 v99, v102
	v_exp_f32_e32 v79, v78
	v_exp_f32_e32 v111, v104
	v_sub_f32_e32 v78, v86, v98
	v_sub_f32_e32 v102, v87, v98
	v_sub_f32_e32 v104, v88, v98
	v_sub_f32_e32 v106, v89, v98
	v_sub_f32_e32 v118, v94, v98
	v_sub_f32_e32 v119, v95, v98
	v_sub_f32_e32 v120, v96, v98
	v_sub_f32_e32 v121, v97, v98
	v_exp_f32_e32 v98, v117
	v_exp_f32_e32 v107, v103
	v_exp_f32_e32 v103, v80
	v_exp_f32_e32 v80, v78
	v_exp_f32_e32 v78, v118
	v_exp_f32_e32 v108, v102
	v_exp_f32_e32 v112, v106
	v_exp_f32_e32 v106, v119
	v_pk_add_f32 v[116:117], v[68:69], v[76:77]
	v_pk_add_f32 v[118:119], v[66:67], v[74:75]
	v_exp_f32_e32 v104, v104
	v_exp_f32_e32 v102, v120
	v_pk_add_f32 v[116:117], v[72:73], v[116:117]
	v_pk_add_f32 v[118:119], v[70:71], v[118:119]
	v_add_u32_e32 v126, s68, v206
	ds_read_b64_tr_b16 v[82:83], v126 offset:0
	v_exp_f32_e32 v110, v121
	v_pk_add_f32 v[116:117], v[100:101], v[116:117]
	v_pk_add_f32 v[118:119], v[98:99], v[118:119]
	ds_read_b64_tr_b16 v[84:85], v126 offset:0x800
	v_pk_add_f32 v[116:117], v[80:81], v[116:117]
	v_pk_add_f32 v[118:119], v[78:79], v[118:119]
	ds_read_b64_tr_b16 v[86:87], v126 offset:0x1000
	v_pk_add_f32 v[116:117], v[108:109], v[116:117]
	v_pk_add_f32 v[118:119], v[106:107], v[118:119]
	ds_read_b64_tr_b16 v[88:89], v126 offset:0x1800
	v_pk_add_f32 v[116:117], v[104:105], v[116:117]
	v_pk_add_f32 v[118:119], v[102:103], v[118:119]
	ds_read_b64_tr_b16 v[90:91], v126 offset:0x2000
	v_pk_add_f32 v[116:117], v[112:113], v[116:117]
	v_pk_add_f32 v[118:119], v[110:111], v[118:119]
	ds_read_b64_tr_b16 v[92:93], v126 offset:0x2800
	ds_read_b64_tr_b16 v[94:95], v126 offset:0x3000
	ds_read_b64_tr_b16 v[96:97], v126 offset:0x3800
	v_cvt_pk_bf16_f32 v120, v79, v107
	v_pk_add_f32 v[116:117], v[118:119], v[116:117]
	v_cvt_pk_bf16_f32 v118, v67, v75
	v_pk_add_f32 v[116:117], v[116:117], v[116:117] op_sel:[0,1] op_sel_hi:[1,0]
	v_cvt_pk_bf16_f32 v119, v71, v99
	v_mov_b32_e32 v115, v116
	s_nop 1
	v_permlane32_swap_b32_e32 v116, v115
	v_add_f32_e32 v127, v116, v115
	v_fmac_f32_e32 v127, v1, v114
	v_cvt_pk_bf16_f32 v114, v69, v77
	v_cvt_pk_bf16_f32 v115, v73, v101
	v_cvt_pk_bf16_f32 v116, v81, v109
	v_cvt_pk_bf16_f32 v117, v105, v113
	v_cvt_pk_bf16_f32 v121, v103, v111
	v_cvt_pk_bf16_f32 v122, v68, v76
	v_cvt_pk_bf16_f32 v123, v72, v100
	v_cvt_pk_bf16_f32 v124, v80, v108
	v_cvt_pk_bf16_f32 v125, v104, v112
	v_cvt_pk_bf16_f32 v66, v66, v74
	v_cvt_pk_bf16_f32 v67, v70, v98
	v_cvt_pk_bf16_f32 v68, v78, v106
	v_cvt_pk_bf16_f32 v69, v102, v110
	ds_read_b64_tr_b16 v[70:71], v126 offset:0x200
	ds_read_b64_tr_b16 v[72:73], v126 offset:0xa00
	ds_read_b64_tr_b16 v[74:75], v126 offset:0x1200
	ds_read_b64_tr_b16 v[76:77], v126 offset:0x1a00
	ds_read_b64_tr_b16 v[78:79], v126 offset:0x2200
	ds_read_b64_tr_b16 v[80:81], v126 offset:0x2a00
	ds_read_b64_tr_b16 v[98:99], v126 offset:0x3200
	ds_read_b64_tr_b16 v[100:101], v126 offset:0x3a00
	s_waitcnt lgkmcnt(8)
	v_mfma_f32_32x32x16_bf16 v[50:65], v[114:117], v[82:85], v[50:65]
	v_mfma_f32_32x32x16_bf16 v[50:65], v[118:121], v[86:89], v[50:65]
	v_mfma_f32_32x32x16_bf16 v[50:65], v[122:125], v[90:93], v[50:65]
	v_mfma_f32_32x32x16_bf16 v[50:65], v[66:69], v[94:97], v[50:65]
	ds_read_b64_tr_b16 v[82:83], v126 offset:0x400
	ds_read_b64_tr_b16 v[84:85], v126 offset:0xc00
	ds_read_b64_tr_b16 v[86:87], v126 offset:0x1400
	ds_read_b64_tr_b16 v[88:89], v126 offset:0x1c00
	ds_read_b64_tr_b16 v[90:91], v126 offset:0x2400
	ds_read_b64_tr_b16 v[92:93], v126 offset:0x2c00
	ds_read_b64_tr_b16 v[94:95], v126 offset:0x3400
	ds_read_b64_tr_b16 v[96:97], v126 offset:0x3c00
	s_waitcnt lgkmcnt(8)
	v_mfma_f32_32x32x16_bf16 v[34:49], v[66:69], v[98:101], v[34:49]
	v_mfma_f32_32x32x16_bf16 v[34:49], v[122:125], v[78:81], v[34:49]
	v_mfma_f32_32x32x16_bf16 v[34:49], v[118:121], v[74:77], v[34:49]
	v_mfma_f32_32x32x16_bf16 v[34:49], v[114:117], v[70:73], v[34:49]
	ds_read_b64_tr_b16 v[70:71], v126 offset:0x600
	ds_read_b64_tr_b16 v[72:73], v126 offset:0xe00
	ds_read_b64_tr_b16 v[74:75], v126 offset:0x1600
	ds_read_b64_tr_b16 v[76:77], v126 offset:0x1e00
	ds_read_b64_tr_b16 v[78:79], v126 offset:0x2600
	ds_read_b64_tr_b16 v[80:81], v126 offset:0x2e00
	ds_read_b64_tr_b16 v[98:99], v126 offset:0x3600
	ds_read_b64_tr_b16 v[100:101], v126 offset:0x3e00
	s_waitcnt lgkmcnt(8)
	v_mfma_f32_32x32x16_bf16 v[18:33], v[114:117], v[82:85], v[18:33]
	v_mfma_f32_32x32x16_bf16 v[18:33], v[118:121], v[86:89], v[18:33]
	v_mfma_f32_32x32x16_bf16 v[18:33], v[122:125], v[90:93], v[18:33]
	v_mfma_f32_32x32x16_bf16 v[18:33], v[66:69], v[94:97], v[18:33]
	s_waitcnt lgkmcnt(0)
	v_mfma_f32_32x32x16_bf16 v[2:17], v[114:117], v[70:73], v[2:17]
	v_mov_b32_e32 v1, v127
	v_mfma_f32_32x32x16_bf16 v[2:17], v[118:121], v[74:77], v[2:17]
	v_mfma_f32_32x32x16_bf16 v[2:17], v[122:125], v[78:81], v[2:17]
	v_mfma_f32_32x32x16_bf16 v[2:17], v[66:69], v[98:101], v[2:17]

.LBB0_260:
	s_mov_b32 m0, s84
	s_add_i32 s5, s97, 0xfeffff80
	buffer_load_dwordx4 v202, s[92:95], s5 offen lds
	s_add_i32 s5, s97, 0xff001f80
	s_mov_b32 m0, s85
	s_add_i32 s6, s97, 0xffffff80
	buffer_load_dwordx4 v202, s[92:95], s5 offen lds
	s_add_i32 s5, s82, s69
	s_mov_b32 m0, s5
	s_nop 0
	buffer_load_dwordx4 v186, s[92:95], s6 offen lds
	s_add_i32 m0, s5, 0x400
	s_nop 0
	buffer_load_dwordx4 v186, s[92:95], s97 offen lds
	ds_read_b128 v[114:117], v213 offset:256
	ds_read_b128 v[118:121], v213 offset:288
	ds_read_b128 v[70:73], v213 offset:384
	ds_read_b128 v[74:77], v213 offset:416
	ds_read_b128 v[122:125], v213 offset:320
	ds_read_b128 v[126:129], v213 offset:352
	ds_read_b128 v[78:81], v213 offset:448
	ds_read_b128 v[82:85], v213 offset:480
	ds_read_b128 v[66:69], v214
	ds_read_b128 v[86:89], v214 offset:8192
	ds_read_b128 v[90:93], v215 offset:8192
	ds_read_b128 v[94:97], v215
	ds_read_b128 v[218:221], v216
	ds_read_b128 v[222:225], v216 offset:8192
	ds_read_b128 v[226:229], v217 offset:8192
	ds_read_b128 v[230:233], v217
	s_waitcnt lgkmcnt(7)
	v_mfma_f32_32x32x16_bf16 v[114:129], v[66:69], v[170:173], v[114:129]
	ds_read_b128 v[66:69], v214 offset:128
	ds_read_b128 v[234:237], v214 offset:8320
	s_waitcnt lgkmcnt(8)
	v_mfma_f32_32x32x16_bf16 v[70:85], v[86:89], v[170:173], v[70:85]
	s_waitcnt lgkmcnt(7)
	v_mfma_f32_32x32x16_bf16 v[70:85], v[90:93], v[166:169], v[70:85]
	ds_read_b128 v[86:89], v215 offset:8320
	ds_read_b128 v[90:93], v215 offset:128
	s_waitcnt lgkmcnt(8)
	v_mfma_f32_32x32x16_bf16 v[114:129], v[94:97], v[166:169], v[114:129]
	s_waitcnt lgkmcnt(7)
	v_mfma_f32_32x32x16_bf16 v[114:129], v[218:221], v[162:165], v[114:129]
	ds_read_b128 v[94:97], v216 offset:128
	ds_read_b128 v[218:221], v216 offset:8320
	s_waitcnt lgkmcnt(8)
	v_mfma_f32_32x32x16_bf16 v[70:85], v[222:225], v[162:165], v[70:85]
	s_waitcnt lgkmcnt(7)
	v_mfma_f32_32x32x16_bf16 v[70:85], v[226:229], v[158:161], v[70:85]
	ds_read_b128 v[222:225], v217 offset:8320
	ds_read_b128 v[226:229], v217 offset:128
	s_waitcnt lgkmcnt(8)
	v_mfma_f32_32x32x16_bf16 v[114:129], v[230:233], v[158:161], v[114:129]
	s_waitcnt lgkmcnt(7)
	v_mfma_f32_32x32x16_bf16 v[114:129], v[66:69], v[154:157], v[114:129]
	s_waitcnt lgkmcnt(6)
	v_mfma_f32_32x32x16_bf16 v[70:85], v[234:237], v[154:157], v[70:85]
	s_waitcnt lgkmcnt(5)
	v_mfma_f32_32x32x16_bf16 v[70:85], v[86:89], v[150:153], v[70:85]
	s_waitcnt lgkmcnt(4)
	v_mfma_f32_32x32x16_bf16 v[114:129], v[90:93], v[150:153], v[114:129]
	s_waitcnt lgkmcnt(3)
	v_mfma_f32_32x32x16_bf16 v[114:129], v[94:97], v[146:149], v[114:129]
	s_waitcnt lgkmcnt(2)
	v_mfma_f32_32x32x16_bf16 v[70:85], v[218:221], v[146:149], v[70:85]
	s_waitcnt lgkmcnt(1)
	v_mfma_f32_32x32x16_bf16 v[70:85], v[222:225], v[142:145], v[70:85]
	s_waitcnt lgkmcnt(0)
	v_mfma_f32_32x32x16_bf16 v[114:129], v[226:229], v[142:145], v[114:129]
	v_exp_f32_e32 v110, v110
	v_exp_f32_e32 v111, v1
	v_exp_f32_e32 v134, v104
	v_exp_f32_e32 v136, v105
	v_exp_f32_e32 v112, v112
	v_exp_f32_e32 v138, v102
	v_exp_f32_e32 v113, v113
	v_exp_f32_e32 v140, v103
	v_exp_f32_e32 v108, v108
	v_exp_f32_e32 v180, v100
	v_exp_f32_e32 v109, v109
	v_exp_f32_e32 v182, v101
	v_exp_f32_e32 v184, v98
	v_exp_f32_e32 v219, v99
	v_add_f32_e32 v1, v133, v141
	v_add_f32_e32 v98, v131, v139
	v_add_f32_e32 v99, v110, v111
	v_add_f32_e32 v100, v134, v136
	v_add_u32_e32 v178, s4, v206
	ds_read_b64_tr_b16 v[66:67], v178 offset:0
	v_exp_f32_e32 v130, v106
	v_add_f32_e32 v1, v137, v1
	v_add_f32_e32 v98, v135, v98
	v_add_f32_e32 v99, v112, v99
	v_add_f32_e32 v100, v138, v100
	ds_read_b64_tr_b16 v[68:69], v178 offset:0x800
	v_exp_f32_e32 v132, v107
	v_add_f32_e32 v1, v183, v1
	v_add_f32_e32 v98, v181, v98
	v_add_f32_e32 v99, v113, v99
	v_add_f32_e32 v100, v140, v100
	ds_read_b64_tr_b16 v[86:87], v178 offset:0x1000
	v_add_f32_e32 v1, v179, v1
	v_add_f32_e32 v98, v177, v98
	v_add_f32_e32 v99, v108, v99
	v_add_f32_e32 v100, v180, v100
	ds_read_b64_tr_b16 v[88:89], v178 offset:0x1800
	v_add_f32_e32 v1, v191, v1
	v_add_f32_e32 v98, v189, v98
	v_add_f32_e32 v99, v109, v99
	v_add_f32_e32 v100, v182, v100
	ds_read_b64_tr_b16 v[90:91], v178 offset:0x2000
	v_add_f32_e32 v1, v187, v1
	v_add_f32_e32 v98, v185, v98
	v_add_f32_e32 v99, v130, v99
	v_add_f32_e32 v100, v184, v100
	ds_read_b64_tr_b16 v[92:93], v178 offset:0x2800
	v_add_f32_e32 v1, v195, v1
	v_add_f32_e32 v98, v193, v98
	v_add_f32_e32 v99, v132, v99
	v_add_f32_e32 v100, v219, v100
	ds_read_b64_tr_b16 v[94:95], v178 offset:0x3000
	v_add_f32_e32 v1, v98, v1
	v_add_f32_e32 v98, v100, v99
	ds_read_b64_tr_b16 v[96:97], v178 offset:0x3800
	v_add_f32_e32 v1, v1, v98
	v_mov_b32_e32 v218, v1
	s_nop 1
	v_permlane32_swap_b32_e32 v1, v218
	v_cvt_pk_bf16_f32 v98, v133, v141
	v_cvt_pk_bf16_f32 v99, v137, v183
	v_cvt_pk_bf16_f32 v100, v179, v191
	v_cvt_pk_bf16_f32 v101, v187, v195
	v_cvt_pk_bf16_f32 v102, v131, v139
	v_cvt_pk_bf16_f32 v103, v135, v181
	v_cvt_pk_bf16_f32 v104, v177, v189
	v_cvt_pk_bf16_f32 v105, v185, v193
	v_cvt_pk_bf16_f32 v106, v110, v111
	v_cvt_pk_bf16_f32 v107, v112, v113
	v_cvt_pk_bf16_f32 v108, v108, v109
	v_cvt_pk_bf16_f32 v109, v130, v132
	v_cvt_pk_bf16_f32 v110, v134, v136
	v_cvt_pk_bf16_f32 v111, v138, v140
	v_cvt_pk_bf16_f32 v112, v180, v182
	v_cvt_pk_bf16_f32 v113, v184, v219
	ds_read_b64_tr_b16 v[130:131], v178 offset:0x200
	ds_read_b64_tr_b16 v[132:133], v178 offset:0xa00
	ds_read_b64_tr_b16 v[134:135], v178 offset:0x1200
	ds_read_b64_tr_b16 v[136:137], v178 offset:0x1a00
	ds_read_b64_tr_b16 v[138:139], v178 offset:0x2200
	ds_read_b64_tr_b16 v[140:141], v178 offset:0x2a00
	ds_read_b64_tr_b16 v[220:221], v178 offset:0x3200
	ds_read_b64_tr_b16 v[222:223], v178 offset:0x3a00
	s_waitcnt lgkmcnt(8)
	v_mfma_f32_32x32x16_bf16 v[50:65], v[98:101], v[66:69], v[50:65]
	v_mfma_f32_32x32x16_bf16 v[50:65], v[102:105], v[86:89], v[50:65]
	v_mfma_f32_32x32x16_bf16 v[50:65], v[106:109], v[90:93], v[50:65]
	v_mfma_f32_32x32x16_bf16 v[50:65], v[110:113], v[94:97], v[50:65]
	ds_read_b64_tr_b16 v[66:67], v178 offset:0x400
	ds_read_b64_tr_b16 v[68:69], v178 offset:0xc00
	ds_read_b64_tr_b16 v[86:87], v178 offset:0x1400
	ds_read_b64_tr_b16 v[88:89], v178 offset:0x1c00
	ds_read_b64_tr_b16 v[90:91], v178 offset:0x2400
	ds_read_b64_tr_b16 v[92:93], v178 offset:0x2c00
	ds_read_b64_tr_b16 v[94:95], v178 offset:0x3400
	ds_read_b64_tr_b16 v[96:97], v178 offset:0x3c00
	s_waitcnt lgkmcnt(8)
	v_mfma_f32_32x32x16_bf16 v[34:49], v[110:113], v[220:223], v[34:49]
	v_mfma_f32_32x32x16_bf16 v[34:49], v[106:109], v[138:141], v[34:49]
	v_mfma_f32_32x32x16_bf16 v[34:49], v[102:105], v[134:137], v[34:49]
	v_mfma_f32_32x32x16_bf16 v[34:49], v[98:101], v[130:133], v[34:49]
	ds_read_b64_tr_b16 v[130:131], v178 offset:0x600
	ds_read_b64_tr_b16 v[132:133], v178 offset:0xe00
	ds_read_b64_tr_b16 v[134:135], v178 offset:0x1600
	ds_read_b64_tr_b16 v[136:137], v178 offset:0x1e00
	ds_read_b64_tr_b16 v[138:139], v178 offset:0x2600
	ds_read_b64_tr_b16 v[140:141], v178 offset:0x2e00
	ds_read_b64_tr_b16 v[220:221], v178 offset:0x3600
	ds_read_b64_tr_b16 v[222:223], v178 offset:0x3e00
	s_waitcnt lgkmcnt(8)
	v_mfma_f32_32x32x16_bf16 v[18:33], v[98:101], v[66:69], v[18:33]
	v_mfma_f32_32x32x16_bf16 v[18:33], v[102:105], v[86:89], v[18:33]
	v_mfma_f32_32x32x16_bf16 v[18:33], v[106:109], v[90:93], v[18:33]
	v_mfma_f32_32x32x16_bf16 v[18:33], v[110:113], v[94:97], v[18:33]
	s_waitcnt lgkmcnt(0)
	v_mfma_f32_32x32x16_bf16 v[2:17], v[98:101], v[130:133], v[2:17]
	s_add_i32 s4, s89, 64
	s_cmp_le_i32 s4, s66
	v_mfma_f32_32x32x16_bf16 v[2:17], v[102:105], v[134:137], v[2:17]
	v_mfma_f32_32x32x16_bf16 v[2:17], v[106:109], v[138:141], v[2:17]
	v_mfma_f32_32x32x16_bf16 v[2:17], v[110:113], v[220:223], v[2:17]
	s_cbranch_scc1 .LBB0_262
	v_subrev_u32_e32 v66, 64, v212
	v_cmp_gt_i32_e64 s[62:63], 26, v66
	v_cmp_gt_i32_e64 s[64:65], 27, v66
	v_cmp_gt_i32_e64 s[60:61], 25, v66
	s_and_b64 s[62:63], s[64:65], s[62:63]
	v_cmp_gt_i32_e64 s[58:59], 24, v66
	s_and_b64 s[60:61], s[62:63], s[60:61]
	v_cmp_gt_i32_e64 s[56:57], 19, v66
	s_and_b64 s[58:59], s[60:61], s[58:59]
	v_cmp_gt_i32_e64 s[54:55], 18, v66
	s_and_b64 s[56:57], s[58:59], s[56:57]
	v_cmp_gt_i32_e64 s[52:53], 17, v66
	s_and_b64 s[54:55], s[56:57], s[54:55]
	v_cmp_gt_i32_e64 s[50:51], 16, v66
	s_and_b64 s[52:53], s[54:55], s[52:53]
	v_cmp_gt_i32_e64 s[48:49], 11, v66
	s_and_b64 s[50:51], s[52:53], s[50:51]
	v_cmp_gt_i32_e64 s[46:47], 10, v66
	s_and_b64 s[48:49], s[50:51], s[48:49]
	v_cmp_gt_i32_e64 s[44:45], 9, v66
	s_and_b64 s[46:47], s[48:49], s[46:47]
	v_cmp_gt_i32_e64 s[42:43], 8, v66
	s_and_b64 s[44:45], s[46:47], s[44:45]
	v_cmp_gt_i32_e64 s[40:41], 3, v66
	s_and_b64 s[42:43], s[44:45], s[42:43]
	v_cmp_gt_i32_e64 s[38:39], 2, v66
	s_and_b64 s[40:41], s[42:43], s[40:41]
	v_cmp_gt_i32_e64 s[36:37], 1, v66
	s_and_b64 s[38:39], s[40:41], s[38:39]
	v_cmp_gt_i32_e64 s[34:35], 0, v66
	s_and_b64 s[36:37], s[38:39], s[36:37]
	s_and_b64 s[34:35], s[36:37], s[34:35]
	v_cmp_gt_i32_e64 s[30:31], 58, v66
	v_cndmask_b32_e64 v114, v114, v199, s[34:35]
	v_cmp_gt_i32_e64 s[34:35], 59, v66
	v_cmp_gt_i32_e64 s[28:29], 57, v66
	s_and_b64 s[30:31], s[34:35], s[30:31]
	v_cmp_gt_i32_e64 s[26:27], 56, v66
	s_and_b64 s[28:29], s[30:31], s[28:29]
	v_cmp_gt_i32_e64 s[24:25], 51, v66
	s_and_b64 s[26:27], s[28:29], s[26:27]
	v_cmp_gt_i32_e64 s[22:23], 50, v66
	s_and_b64 s[24:25], s[26:27], s[24:25]
	v_cmp_gt_i32_e64 s[20:21], 49, v66
	s_and_b64 s[22:23], s[24:25], s[22:23]
	v_cmp_gt_i32_e64 s[18:19], 48, v66
	s_and_b64 s[20:21], s[22:23], s[20:21]
	v_cmp_gt_i32_e64 s[16:17], 43, v66
	s_and_b64 s[18:19], s[20:21], s[18:19]
	v_cmp_gt_i32_e64 s[14:15], 42, v66
	s_and_b64 s[16:17], s[18:19], s[16:17]
	v_cmp_gt_i32_e64 s[12:13], 41, v66
	s_and_b64 s[14:15], s[16:17], s[14:15]
	v_cmp_gt_i32_e64 s[10:11], 40, v66
	s_and_b64 s[12:13], s[14:15], s[12:13]
	v_cmp_gt_i32_e64 s[8:9], 35, v66
	s_and_b64 s[10:11], s[12:13], s[10:11]
	v_cmp_gt_i32_e64 s[6:7], 34, v66
	s_and_b64 s[8:9], s[10:11], s[8:9]
	v_cmp_gt_i32_e64 s[4:5], 33, v66
	s_and_b64 s[6:7], s[8:9], s[6:7]
	v_cmp_gt_i32_e32 vcc, 32, v66
	s_and_b64 s[4:5], s[6:7], s[4:5]
	s_and_b64 vcc, s[4:5], vcc
	v_cndmask_b32_e64 v129, v129, v199, s[64:65]
	v_cndmask_b32_e64 v128, v128, v199, s[62:63]
	v_cndmask_b32_e64 v127, v127, v199, s[60:61]
	v_cndmask_b32_e64 v126, v126, v199, s[58:59]
	v_cndmask_b32_e64 v125, v125, v199, s[56:57]
	v_cndmask_b32_e64 v124, v124, v199, s[54:55]
	v_cndmask_b32_e64 v123, v123, v199, s[52:53]
	v_cndmask_b32_e64 v122, v122, v199, s[50:51]
	v_cndmask_b32_e64 v121, v121, v199, s[48:49]
	v_cndmask_b32_e64 v120, v120, v199, s[46:47]
	v_cndmask_b32_e64 v119, v119, v199, s[44:45]
	v_cndmask_b32_e64 v118, v118, v199, s[42:43]
	v_cndmask_b32_e64 v117, v117, v199, s[40:41]
	v_cndmask_b32_e64 v116, v116, v199, s[38:39]
	v_cndmask_b32_e64 v115, v115, v199, s[36:37]
	v_cndmask_b32_e64 v85, v85, v199, s[34:35]
	v_cndmask_b32_e64 v84, v84, v199, s[30:31]
	v_cndmask_b32_e64 v83, v83, v199, s[28:29]
	v_cndmask_b32_e64 v82, v82, v199, s[26:27]
	v_cndmask_b32_e64 v81, v81, v199, s[24:25]
	v_cndmask_b32_e64 v80, v80, v199, s[22:23]
	v_cndmask_b32_e64 v79, v79, v199, s[20:21]
	v_cndmask_b32_e64 v78, v78, v199, s[18:19]
	v_cndmask_b32_e64 v77, v77, v199, s[16:17]
	v_cndmask_b32_e64 v76, v76, v199, s[14:15]
	v_cndmask_b32_e64 v75, v75, v199, s[12:13]
	v_cndmask_b32_e64 v74, v74, v199, s[10:11]
	v_cndmask_b32_e64 v73, v73, v199, s[8:9]
	v_cndmask_b32_e64 v72, v72, v199, s[6:7]
	v_cndmask_b32_e64 v71, v71, v199, s[4:5]
	v_cndmask_b32_e32 v70, v70, v199, vcc

.LBB0_268:
	v_cndmask_b32_e64 v98, v66, v207, s[4:5]
	v_sub_f32_e32 v66, v114, v98
	v_sub_f32_e32 v67, v115, v98
	v_sub_f32_e32 v68, v116, v98
	v_sub_f32_e32 v69, v117, v98
	v_sub_f32_e32 v86, v118, v98
	v_sub_f32_e32 v87, v119, v98
	v_sub_f32_e32 v88, v120, v98
	v_sub_f32_e32 v89, v121, v98
	v_sub_f32_e32 v90, v122, v98
	v_sub_f32_e32 v91, v123, v98
	v_sub_f32_e32 v92, v124, v98
	v_sub_f32_e32 v93, v125, v98
	v_sub_f32_e32 v94, v126, v98
	v_sub_f32_e32 v95, v127, v98
	v_sub_f32_e32 v96, v128, v98
	v_sub_f32_e32 v97, v129, v98
	v_sub_f32_e32 v99, v70, v98
	v_sub_f32_e32 v108, v71, v98
	v_sub_f32_e32 v109, v72, v98
	v_sub_f32_e32 v177, v73, v98
	v_sub_f32_e32 v178, v74, v98
	v_sub_f32_e32 v179, v75, v98
	v_sub_f32_e32 v180, v76, v98
	v_sub_f32_e32 v181, v77, v98
	v_sub_f32_e32 v182, v78, v98
	v_sub_f32_e32 v183, v79, v98
	v_sub_f32_e32 v184, v80, v98
	v_sub_f32_e32 v185, v81, v98
	v_exp_f32_e32 v66, v66
	v_exp_f32_e32 v67, v67
	v_exp_f32_e32 v68, v68
	v_exp_f32_e32 v69, v69
	v_exp_f32_e32 v70, v86
	v_exp_f32_e32 v71, v87
	v_exp_f32_e32 v72, v88
	v_exp_f32_e32 v73, v89
	v_exp_f32_e32 v74, v90
	v_exp_f32_e32 v75, v91
	v_exp_f32_e32 v76, v92
	v_exp_f32_e32 v77, v93
	v_exp_f32_e32 v78, v94
	v_exp_f32_e32 v79, v95
	v_exp_f32_e32 v80, v96
	v_exp_f32_e32 v81, v97
	v_sub_f32_e32 v187, v82, v98
	v_sub_f32_e32 v189, v83, v98
	v_sub_f32_e32 v191, v84, v98
	v_sub_f32_e32 v193, v85, v98
	ds_read_b128 v[126:129], v213
	ds_read_b128 v[130:133], v213 offset:32
	ds_read_b128 v[110:113], v213 offset:128
	ds_read_b128 v[114:117], v213 offset:160
	ds_read_b128 v[134:137], v213 offset:64
	ds_read_b128 v[138:141], v213 offset:96
	ds_read_b128 v[118:121], v213 offset:192
	ds_read_b128 v[122:125], v213 offset:224
	ds_read_b128 v[82:85], v188 offset:49152
	ds_read_b128 v[86:89], v188 offset:57344
	ds_read_b128 v[90:93], v190 offset:57344
	ds_read_b128 v[94:97], v190 offset:49152
	ds_read_b128 v[100:103], v192 offset:49152
	ds_read_b128 v[104:107], v192 offset:57344
	ds_read_b128 v[220:223], v194 offset:57344
	ds_read_b128 v[224:227], v194 offset:49152
	s_waitcnt lgkmcnt(7)
	v_mfma_f32_32x32x16_bf16 v[126:141], v[82:85], v[170:173], v[126:141]
	ds_read_b128 v[82:85], v188 offset:49280
	ds_read_b128 v[228:231], v188 offset:57472
	s_waitcnt lgkmcnt(8)
	v_mfma_f32_32x32x16_bf16 v[110:125], v[86:89], v[170:173], v[110:125]
	s_waitcnt lgkmcnt(7)
	v_mfma_f32_32x32x16_bf16 v[110:125], v[90:93], v[166:169], v[110:125]
	ds_read_b128 v[86:89], v190 offset:57472
	ds_read_b128 v[90:93], v190 offset:49280
	s_waitcnt lgkmcnt(8)
	v_mfma_f32_32x32x16_bf16 v[126:141], v[94:97], v[166:169], v[126:141]
	s_waitcnt lgkmcnt(7)
	v_mfma_f32_32x32x16_bf16 v[126:141], v[100:103], v[162:165], v[126:141]
	ds_read_b128 v[94:97], v192 offset:49280
	ds_read_b128 v[100:103], v192 offset:57472
	s_waitcnt lgkmcnt(8)
	v_mfma_f32_32x32x16_bf16 v[110:125], v[104:107], v[162:165], v[110:125]
	s_waitcnt lgkmcnt(7)
	v_mfma_f32_32x32x16_bf16 v[110:125], v[220:223], v[158:161], v[110:125]
	ds_read_b128 v[104:107], v194 offset:57472
	ds_read_b128 v[220:223], v194 offset:49280
	s_waitcnt lgkmcnt(8)
	v_mfma_f32_32x32x16_bf16 v[126:141], v[224:227], v[158:161], v[126:141]
	s_waitcnt lgkmcnt(7)
	v_mfma_f32_32x32x16_bf16 v[126:141], v[82:85], v[154:157], v[126:141]
	s_waitcnt lgkmcnt(6)
	v_mfma_f32_32x32x16_bf16 v[110:125], v[228:231], v[154:157], v[110:125]
	s_waitcnt lgkmcnt(5)
	v_mfma_f32_32x32x16_bf16 v[110:125], v[86:89], v[150:153], v[110:125]
	s_waitcnt lgkmcnt(4)
	v_mfma_f32_32x32x16_bf16 v[126:141], v[90:93], v[150:153], v[126:141]
	s_waitcnt lgkmcnt(3)
	v_mfma_f32_32x32x16_bf16 v[126:141], v[94:97], v[146:149], v[126:141]
	s_waitcnt lgkmcnt(2)
	v_mfma_f32_32x32x16_bf16 v[110:125], v[100:103], v[146:149], v[110:125]
	s_waitcnt lgkmcnt(1)
	v_mfma_f32_32x32x16_bf16 v[110:125], v[104:107], v[142:145], v[110:125]
	s_waitcnt lgkmcnt(0)
	v_mfma_f32_32x32x16_bf16 v[126:141], v[220:223], v[142:145], v[126:141]
	v_exp_f32_e32 v82, v99
	v_exp_f32_e32 v83, v108
	v_exp_f32_e32 v90, v182
	v_exp_f32_e32 v91, v183
	v_exp_f32_e32 v84, v109
	v_exp_f32_e32 v92, v184
	v_exp_f32_e32 v85, v177
	v_exp_f32_e32 v93, v185
	v_exp_f32_e32 v86, v178
	v_exp_f32_e32 v94, v187
	v_exp_f32_e32 v87, v179
	v_exp_f32_e32 v95, v189
	v_add_f32_e32 v99, v66, v67
	v_add_f32_e32 v108, v74, v75
	v_add_f32_e32 v109, v82, v83
	v_add_f32_e32 v177, v90, v91
	v_add_u32_e32 v195, s33, v206
	ds_read_b64_tr_b16 v[100:101], v195 offset:0
	v_exp_f32_e32 v88, v180
	v_exp_f32_e32 v96, v191
	v_add_f32_e32 v99, v68, v99
	v_add_f32_e32 v108, v76, v108
	v_add_f32_e32 v109, v84, v109
	v_add_f32_e32 v177, v92, v177
	ds_read_b64_tr_b16 v[102:103], v195 offset:0x800
	v_exp_f32_e32 v89, v181
	v_exp_f32_e32 v97, v193
	v_add_f32_e32 v99, v69, v99
	v_add_f32_e32 v108, v77, v108
	v_add_f32_e32 v109, v85, v109
	v_add_f32_e32 v177, v93, v177
	ds_read_b64_tr_b16 v[104:105], v195 offset:0x1000
	v_add_f32_e32 v99, v70, v99
	v_add_f32_e32 v108, v78, v108
	v_add_f32_e32 v109, v86, v109
	v_add_f32_e32 v177, v94, v177
	ds_read_b64_tr_b16 v[106:107], v195 offset:0x1800
	v_add_f32_e32 v99, v71, v99
	v_add_f32_e32 v108, v79, v108
	v_add_f32_e32 v109, v87, v109
	v_add_f32_e32 v177, v95, v177
	ds_read_b64_tr_b16 v[222:223], v195 offset:0x2000
	v_add_f32_e32 v99, v72, v99
	v_add_f32_e32 v108, v80, v108
	v_add_f32_e32 v109, v88, v109
	v_add_f32_e32 v177, v96, v177
	ds_read_b64_tr_b16 v[224:225], v195 offset:0x2800
	v_add_f32_e32 v99, v73, v99
	v_add_f32_e32 v108, v81, v108
	v_add_f32_e32 v109, v89, v109
	v_add_f32_e32 v177, v97, v177
	ds_read_b64_tr_b16 v[226:227], v195 offset:0x3000
	v_add_f32_e32 v99, v108, v99
	v_add_f32_e32 v108, v177, v109
	ds_read_b64_tr_b16 v[228:229], v195 offset:0x3800
	v_add_f32_e32 v220, v108, v99
	v_mov_b32_e32 v221, v220
	s_nop 1
	v_permlane32_swap_b32_e32 v220, v221
	v_cvt_pk_bf16_f32 v230, v66, v67
	v_cvt_pk_bf16_f32 v231, v68, v69
	v_cvt_pk_bf16_f32 v232, v70, v71
	v_cvt_pk_bf16_f32 v233, v72, v73
	v_cvt_pk_bf16_f32 v234, v74, v75
	v_cvt_pk_bf16_f32 v235, v76, v77
	v_cvt_pk_bf16_f32 v236, v78, v79
	v_cvt_pk_bf16_f32 v237, v80, v81
	v_cvt_pk_bf16_f32 v238, v82, v83
	v_cvt_pk_bf16_f32 v239, v84, v85
	v_cvt_pk_bf16_f32 v240, v86, v87
	v_cvt_pk_bf16_f32 v241, v88, v89
	v_cvt_pk_bf16_f32 v242, v90, v91
	v_cvt_pk_bf16_f32 v243, v92, v93
	v_cvt_pk_bf16_f32 v244, v94, v95
	v_cvt_pk_bf16_f32 v245, v96, v97
	ds_read_b64_tr_b16 v[246:247], v195 offset:0x200
	ds_read_b64_tr_b16 v[248:249], v195 offset:0xa00
	ds_read_b64_tr_b16 v[250:251], v195 offset:0x1200
	ds_read_b64_tr_b16 v[252:253], v195 offset:0x1a00
	ds_read_b64_tr_b16 v[178:179], v195 offset:0x2200
	ds_read_b64_tr_b16 v[180:181], v195 offset:0x2a00
	ds_read_b64_tr_b16 v[182:183], v195 offset:0x3200
	ds_read_b64_tr_b16 v[184:185], v195 offset:0x3a00
	s_waitcnt lgkmcnt(8)
	v_mfma_f32_32x32x16_bf16 v[50:65], v[230:233], v[100:103], v[50:65]
	v_mfma_f32_32x32x16_bf16 v[50:65], v[234:237], v[104:107], v[50:65]
	v_mfma_f32_32x32x16_bf16 v[50:65], v[238:241], v[222:225], v[50:65]
	v_mfma_f32_32x32x16_bf16 v[50:65], v[242:245], v[226:229], v[50:65]
	ds_read_b64_tr_b16 v[100:101], v195 offset:0x400
	ds_read_b64_tr_b16 v[102:103], v195 offset:0xc00
	ds_read_b64_tr_b16 v[104:105], v195 offset:0x1400
	ds_read_b64_tr_b16 v[106:107], v195 offset:0x1c00
	ds_read_b64_tr_b16 v[222:223], v195 offset:0x2400
	ds_read_b64_tr_b16 v[224:225], v195 offset:0x2c00
	ds_read_b64_tr_b16 v[226:227], v195 offset:0x3400
	ds_read_b64_tr_b16 v[228:229], v195 offset:0x3c00
	s_waitcnt lgkmcnt(8)
	v_mfma_f32_32x32x16_bf16 v[34:49], v[242:245], v[182:185], v[34:49]
	v_mfma_f32_32x32x16_bf16 v[34:49], v[238:241], v[178:181], v[34:49]
	v_mfma_f32_32x32x16_bf16 v[34:49], v[234:237], v[250:253], v[34:49]
	v_mfma_f32_32x32x16_bf16 v[34:49], v[230:233], v[246:249], v[34:49]
	ds_read_b64_tr_b16 v[178:179], v195 offset:0x600
	ds_read_b64_tr_b16 v[180:181], v195 offset:0xe00
	ds_read_b64_tr_b16 v[182:183], v195 offset:0x1600
	ds_read_b64_tr_b16 v[184:185], v195 offset:0x1e00
	ds_read_b64_tr_b16 v[246:247], v195 offset:0x2600
	ds_read_b64_tr_b16 v[248:249], v195 offset:0x2e00
	ds_read_b64_tr_b16 v[250:251], v195 offset:0x3600
	ds_read_b64_tr_b16 v[252:253], v195 offset:0x3e00
	s_waitcnt lgkmcnt(8)
	v_mfma_f32_32x32x16_bf16 v[18:33], v[230:233], v[100:103], v[18:33]
	v_mfma_f32_32x32x16_bf16 v[18:33], v[234:237], v[104:107], v[18:33]
	v_mfma_f32_32x32x16_bf16 v[18:33], v[238:241], v[222:225], v[18:33]
	v_mfma_f32_32x32x16_bf16 v[18:33], v[242:245], v[226:229], v[18:33]
	s_waitcnt lgkmcnt(0)
	v_mfma_f32_32x32x16_bf16 v[2:17], v[230:233], v[178:181], v[2:17]
	s_cmp_le_i32 s89, s66
	v_mfma_f32_32x32x16_bf16 v[2:17], v[234:237], v[182:185], v[2:17]
	v_mfma_f32_32x32x16_bf16 v[2:17], v[238:241], v[246:249], v[2:17]
	v_mfma_f32_32x32x16_bf16 v[2:17], v[242:245], v[250:253], v[2:17]
	s_cbranch_scc1 .LBB0_270
	v_cmp_gt_i32_e64 s[62:63], 26, v212
	v_cmp_gt_i32_e64 s[64:65], 27, v212
	v_cmp_gt_i32_e64 s[60:61], 25, v212
	s_and_b64 s[62:63], s[64:65], s[62:63]
	v_cmp_gt_i32_e64 s[58:59], 24, v212
	s_and_b64 s[60:61], s[62:63], s[60:61]
	v_cmp_gt_i32_e64 s[56:57], 19, v212
	s_and_b64 s[58:59], s[60:61], s[58:59]
	v_cmp_gt_i32_e64 s[54:55], 18, v212
	s_and_b64 s[56:57], s[58:59], s[56:57]
	v_cmp_gt_i32_e64 s[52:53], 17, v212
	s_and_b64 s[54:55], s[56:57], s[54:55]
	v_cmp_gt_i32_e64 s[50:51], 16, v212
	s_and_b64 s[52:53], s[54:55], s[52:53]
	v_cmp_gt_i32_e64 s[48:49], 11, v212
	s_and_b64 s[50:51], s[52:53], s[50:51]
	v_cmp_gt_i32_e64 s[46:47], 10, v212
	s_and_b64 s[48:49], s[50:51], s[48:49]
	v_cmp_gt_i32_e64 s[44:45], 9, v212
	s_and_b64 s[46:47], s[48:49], s[46:47]
	v_cmp_gt_i32_e64 s[42:43], 8, v212
	s_and_b64 s[44:45], s[46:47], s[44:45]
	v_cmp_gt_i32_e64 s[40:41], 3, v212
	s_and_b64 s[42:43], s[44:45], s[42:43]
	v_cmp_gt_i32_e64 s[38:39], 2, v212
	s_and_b64 s[40:41], s[42:43], s[40:41]
	v_cmp_gt_i32_e64 s[36:37], 1, v212
	s_and_b64 s[38:39], s[40:41], s[38:39]
	v_cmp_gt_i32_e64 s[34:35], 0, v212
	s_and_b64 s[36:37], s[38:39], s[36:37]
	s_and_b64 s[34:35], s[36:37], s[34:35]
	v_cmp_gt_i32_e64 s[30:31], 58, v212
	v_cndmask_b32_e64 v126, v126, v199, s[34:35]
	v_cmp_gt_i32_e64 s[34:35], 59, v212
	v_cmp_gt_i32_e64 s[28:29], 57, v212
	s_and_b64 s[30:31], s[34:35], s[30:31]
	v_cmp_gt_i32_e64 s[26:27], 56, v212
	s_and_b64 s[28:29], s[30:31], s[28:29]
	v_cmp_gt_i32_e64 s[24:25], 51, v212
	s_and_b64 s[26:27], s[28:29], s[26:27]
	v_cmp_gt_i32_e64 s[22:23], 50, v212
	s_and_b64 s[24:25], s[26:27], s[24:25]
	v_cmp_gt_i32_e64 s[20:21], 49, v212
	s_and_b64 s[22:23], s[24:25], s[22:23]
	v_cmp_gt_i32_e64 s[18:19], 48, v212
	s_and_b64 s[20:21], s[22:23], s[20:21]
	v_cmp_gt_i32_e64 s[16:17], 43, v212
	s_and_b64 s[18:19], s[20:21], s[18:19]
	v_cmp_gt_i32_e64 s[14:15], 42, v212
	s_and_b64 s[16:17], s[18:19], s[16:17]
	v_cmp_gt_i32_e64 s[12:13], 41, v212
	s_and_b64 s[14:15], s[16:17], s[14:15]
	v_cmp_gt_i32_e64 s[10:11], 40, v212
	s_and_b64 s[12:13], s[14:15], s[12:13]
	v_cmp_gt_i32_e64 s[8:9], 35, v212
	s_and_b64 s[10:11], s[12:13], s[10:11]
	v_cmp_gt_i32_e64 s[6:7], 34, v212
	s_and_b64 s[8:9], s[10:11], s[8:9]
	v_cmp_gt_i32_e64 s[4:5], 33, v212
	s_and_b64 s[6:7], s[8:9], s[6:7]
	v_cmp_gt_i32_e32 vcc, 32, v212
	s_and_b64 s[4:5], s[6:7], s[4:5]
	s_and_b64 vcc, s[4:5], vcc
	v_cndmask_b32_e64 v141, v141, v199, s[64:65]
	v_cndmask_b32_e64 v140, v140, v199, s[62:63]
	v_cndmask_b32_e64 v139, v139, v199, s[60:61]
	v_cndmask_b32_e64 v138, v138, v199, s[58:59]
	v_cndmask_b32_e64 v137, v137, v199, s[56:57]
	v_cndmask_b32_e64 v136, v136, v199, s[54:55]
	v_cndmask_b32_e64 v135, v135, v199, s[52:53]
	v_cndmask_b32_e64 v134, v134, v199, s[50:51]
	v_cndmask_b32_e64 v133, v133, v199, s[48:49]
	v_cndmask_b32_e64 v132, v132, v199, s[46:47]
	v_cndmask_b32_e64 v131, v131, v199, s[44:45]
	v_cndmask_b32_e64 v130, v130, v199, s[42:43]
	v_cndmask_b32_e64 v129, v129, v199, s[40:41]
	v_cndmask_b32_e64 v128, v128, v199, s[38:39]
	v_cndmask_b32_e64 v127, v127, v199, s[36:37]
	v_cndmask_b32_e64 v125, v125, v199, s[34:35]
	v_cndmask_b32_e64 v124, v124, v199, s[30:31]
	v_cndmask_b32_e64 v123, v123, v199, s[28:29]
	v_cndmask_b32_e64 v122, v122, v199, s[26:27]
	v_cndmask_b32_e64 v121, v121, v199, s[24:25]
	v_cndmask_b32_e64 v120, v120, v199, s[22:23]
	v_cndmask_b32_e64 v119, v119, v199, s[20:21]
	v_cndmask_b32_e64 v118, v118, v199, s[18:19]
	v_cndmask_b32_e64 v117, v117, v199, s[16:17]
	v_cndmask_b32_e64 v116, v116, v199, s[14:15]
	v_cndmask_b32_e64 v115, v115, v199, s[12:13]
	v_cndmask_b32_e64 v114, v114, v199, s[10:11]
	v_cndmask_b32_e64 v113, v113, v199, s[8:9]
	v_cndmask_b32_e64 v112, v112, v199, s[6:7]
	v_cndmask_b32_e64 v111, v111, v199, s[4:5]
	v_cndmask_b32_e32 v110, v110, v199, vcc

.LBB0_360:
	s_add_i32 s2, s87, 0xffffff81
	s_lshr_b32 s4, s2, 8
	s_cmp_eq_u32 s4, s78
	v_cvt_pk_bf16_f32 v155, v155, v156
	v_cvt_pk_bf16_f32 v156, v157, v158
	v_cvt_pk_bf16_f32 v157, v159, v160
	s_cselect_b64 s[2:3], -1, 0
	s_lshl_b32 s4, 1, s4
	v_max_f32_e32 v158, v83, v83
	v_max_f32_e32 v159, v82, v82
	v_cvt_pk_bf16_f32 v199, v199, v200
	v_cvt_pk_bf16_f32 v200, v201, v203
	v_cvt_pk_bf16_f32 v203, v206, v208
	v_cvt_pk_bf16_f32 v206, v17, v195
	v_and_b32_e32 v17, s4, v187
	v_max_f32_e32 v158, v159, v158
	v_cmp_ne_u32_e32 vcc, 0, v17
	v_max3_f32 v17, v98, v99, v100
	v_max3_f32 v159, v90, v91, v92
	v_max3_f32 v158, v158, v84, v85
	v_cvt_pk_bf16_f32 v154, v152, v154
	v_max3_f32 v152, v106, v107, v108
	v_max3_f32 v17, v17, v101, v102
	v_max3_f32 v159, v159, v93, v94
	v_max3_f32 v158, v158, v86, v87
	v_max3_f32 v152, v152, v109, v110
	v_max3_f32 v17, v17, v103, v104
	v_max3_f32 v159, v159, v95, v96
	v_max3_f32 v158, v158, v88, v89
	v_max3_f32 v152, v152, v111, v112
	v_max3_f32 v17, v17, v105, v113
	v_max3_f32 v158, v158, v97, v159
	v_max3_f32 v17, v17, v152, v158
	v_mov_b32_e32 v152, v17
	s_nop 1
	v_permlane32_swap_b32_e32 v17, v152
	v_max_f32_e32 v152, v152, v152
	v_max_f32_e32 v17, v17, v17
	v_max_f32_e32 v17, v17, v152
	s_or_b64 s[2:3], s[2:3], vcc
	v_cndmask_b32_e64 v17, v171, v17, s[2:3]
	v_max_f32_e32 v152, v191, v191
	v_max_f32_e32 v152, v152, v17
	v_sub_f32_e32 v158, v17, v191
	v_sub_f32_e32 v17, v191, v152
	v_exp_f32_e32 v17, v17
	v_cmp_ge_f32_e32 vcc, s94, v158
	s_cmp_eq_u64 vcc, exec
	s_cselect_b64 s[4:5], -1, 0
	v_cndmask_b32_e64 v17, v17, 1.0, s[4:5]
	v_cvt_pk_bf16_f32 v198, v197, v198
	v_cvt_pk_bf16_f32 v201, v205, v207
	v_cvt_pk_bf16_f32 v202, v202, v204
	v_cvt_pk_bf16_f32 v204, v209, v210
	v_cvt_pk_bf16_f32 v205, v211, v212
	v_cvt_pk_bf16_f32 v207, v196, v213
	v_cvt_pk_bf16_f32 v208, v214, v215
	v_cvt_pk_bf16_f32 v209, v216, v217
	ds_read_b64_tr_b16 v[158:159], v153 offset:0x200
	ds_read_b64_tr_b16 v[160:161], v153 offset:0xa00
	ds_read_b64_tr_b16 v[210:211], v153 offset:0x1200
	ds_read_b64_tr_b16 v[212:213], v153 offset:0x1a00
	ds_read_b64_tr_b16 v[214:215], v153 offset:0x2200
	ds_read_b64_tr_b16 v[216:217], v153 offset:0x2a00
	ds_read_b64_tr_b16 v[218:219], v153 offset:0x3200
	ds_read_b64_tr_b16 v[220:221], v153 offset:0x3a00
	s_waitcnt lgkmcnt(8)
	v_mfma_f32_32x32x16_bf16 v[66:81], v[198:201], v[146:149], v[66:81]
	v_mfma_f32_32x32x16_bf16 v[66:81], v[202:205], v[12:15], v[66:81]
	v_mfma_f32_32x32x16_bf16 v[66:81], v[206:209], v[8:11], v[66:81]
	v_mfma_f32_32x32x16_bf16 v[66:81], v[154:157], v[4:7], v[66:81]
	ds_read_b64_tr_b16 v[4:5], v153 offset:0x400
	ds_read_b64_tr_b16 v[6:7], v153 offset:0xc00
	ds_read_b64_tr_b16 v[8:9], v153 offset:0x1400
	ds_read_b64_tr_b16 v[10:11], v153 offset:0x1c00
	ds_read_b64_tr_b16 v[12:13], v153 offset:0x2400
	ds_read_b64_tr_b16 v[14:15], v153 offset:0x2c00
	ds_read_b64_tr_b16 v[146:147], v153 offset:0x3400
	ds_read_b64_tr_b16 v[148:149], v153 offset:0x3c00
	s_waitcnt lgkmcnt(8)
	v_mfma_f32_32x32x16_bf16 v[50:65], v[154:157], v[218:221], v[50:65]
	v_mfma_f32_32x32x16_bf16 v[50:65], v[206:209], v[214:217], v[50:65]
	v_mfma_f32_32x32x16_bf16 v[50:65], v[202:205], v[210:213], v[50:65]
	v_mfma_f32_32x32x16_bf16 v[50:65], v[198:201], v[158:161], v[50:65]
	ds_read_b64_tr_b16 v[158:159], v153 offset:0x600
	ds_read_b64_tr_b16 v[160:161], v153 offset:0xe00
	ds_read_b64_tr_b16 v[210:211], v153 offset:0x1600
	ds_read_b64_tr_b16 v[212:213], v153 offset:0x1e00
	ds_read_b64_tr_b16 v[214:215], v153 offset:0x2600
	ds_read_b64_tr_b16 v[216:217], v153 offset:0x2e00
	ds_read_b64_tr_b16 v[218:219], v153 offset:0x3600
	ds_read_b64_tr_b16 v[220:221], v153 offset:0x3e00
	s_waitcnt lgkmcnt(8)
	v_mfma_f32_32x32x16_bf16 v[34:49], v[198:201], v[4:7], v[34:49]
	v_mfma_f32_32x32x16_bf16 v[34:49], v[202:205], v[8:11], v[34:49]
	v_mfma_f32_32x32x16_bf16 v[34:49], v[206:209], v[12:15], v[34:49]
	v_mfma_f32_32x32x16_bf16 v[34:49], v[154:157], v[146:149], v[34:49]
	s_waitcnt lgkmcnt(0)
	v_mfma_f32_32x32x16_bf16 v[18:33], v[198:201], v[158:161], v[18:33]
	s_waitcnt vmcnt(0)
	v_cmp_gt_f32_e32 vcc, 1.0, v17
	v_mfma_f32_32x32x16_bf16 v[18:33], v[202:205], v[210:213], v[18:33]
	v_mfma_f32_32x32x16_bf16 v[18:33], v[206:209], v[214:217], v[18:33]
	v_mfma_f32_32x32x16_bf16 v[18:33], v[154:157], v[218:221], v[18:33]
	s_cbranch_vccz .LBB0_364
	s_and_saveexec_b64 s[6:7], s[0:1]
	ds_write_b32 v178, v17 offset:128
	s_or_b64 exec, exec, s[6:7]
	s_waitcnt lgkmcnt(0)
	ds_read_b128 v[4:7], v177 offset:224
	ds_read_b128 v[8:11], v177 offset:192
	ds_read_b128 v[12:15], v177 offset:160
	ds_read_b128 v[146:149], v177 offset:128
	s_waitcnt lgkmcnt(3)
	v_pk_mul_f32 v[80:81], v[80:81], v[6:7]
	s_waitcnt lgkmcnt(2)
	v_pk_mul_f32 v[76:77], v[76:77], v[10:11]
	s_waitcnt lgkmcnt(1)
	v_pk_mul_f32 v[72:73], v[72:73], v[14:15]
	s_waitcnt lgkmcnt(0)
	v_pk_mul_f32 v[68:69], v[68:69], v[148:149]
	v_pk_mul_f32 v[78:79], v[78:79], v[4:5]
	v_pk_mul_f32 v[74:75], v[74:75], v[8:9]
	v_pk_mul_f32 v[70:71], v[70:71], v[12:13]
	v_pk_mul_f32 v[66:67], v[66:67], v[146:147]
	v_pk_mul_f32 v[64:65], v[64:65], v[6:7]
	v_pk_mul_f32 v[60:61], v[60:61], v[10:11]
	v_pk_mul_f32 v[56:57], v[56:57], v[14:15]
	v_pk_mul_f32 v[52:53], v[52:53], v[148:149]
	v_pk_mul_f32 v[62:63], v[62:63], v[4:5]
	v_pk_mul_f32 v[58:59], v[58:59], v[8:9]
	v_pk_mul_f32 v[54:55], v[54:55], v[12:13]
	v_pk_mul_f32 v[50:51], v[50:51], v[146:147]
	v_pk_mul_f32 v[48:49], v[48:49], v[6:7]
	v_pk_mul_f32 v[44:45], v[44:45], v[10:11]
	v_pk_mul_f32 v[40:41], v[40:41], v[14:15]
	v_pk_mul_f32 v[36:37], v[36:37], v[148:149]
	v_pk_mul_f32 v[46:47], v[46:47], v[4:5]
	v_pk_mul_f32 v[42:43], v[42:43], v[8:9]
	v_pk_mul_f32 v[38:39], v[38:39], v[12:13]
	v_pk_mul_f32 v[34:35], v[34:35], v[146:147]
	v_pk_mul_f32 v[32:33], v[32:33], v[6:7]
	v_pk_mul_f32 v[28:29], v[28:29], v[10:11]
	v_pk_mul_f32 v[24:25], v[24:25], v[14:15]
	v_pk_mul_f32 v[20:21], v[20:21], v[148:149]
	v_pk_mul_f32 v[30:31], v[30:31], v[4:5]
	v_pk_mul_f32 v[26:27], v[26:27], v[8:9]
	v_pk_mul_f32 v[22:23], v[22:23], v[12:13]
	v_pk_mul_f32 v[18:19], v[18:19], v[146:147]

.LBB0_368:
	s_lshr_b32 s4, s84, 2
	s_cmp_eq_u32 s4, s78
	v_cvt_pk_bf16_f32 v220, v161, v191
	v_cvt_pk_bf16_f32 v221, v197, v200
	s_cselect_b64 s[2:3], -1, 0
	s_lshl_b32 s4, 1, s4
	s_nop 2
	v_max_f32_e32 v191, v83, v83
	v_max_f32_e32 v197, v82, v82
	v_cvt_pk_bf16_f32 v218, v154, v156
	v_and_b32_e32 v154, s4, v187
	v_max_f32_e32 v191, v197, v191
	v_cmp_ne_u32_e32 vcc, 0, v154
	v_max3_f32 v154, v98, v99, v100
	v_max3_f32 v197, v90, v91, v92
	v_max3_f32 v191, v191, v84, v85
	v_cvt_pk_bf16_f32 v156, v155, v158
	v_max3_f32 v155, v106, v107, v108
	v_max3_f32 v154, v154, v101, v102
	v_max3_f32 v197, v197, v93, v94
	v_max3_f32 v191, v191, v86, v87
	v_max3_f32 v155, v155, v109, v110
	v_max3_f32 v154, v154, v103, v104
	v_max3_f32 v197, v197, v95, v96
	v_max3_f32 v191, v191, v88, v89
	v_max3_f32 v155, v155, v111, v112
	v_max3_f32 v154, v154, v105, v113
	v_max3_f32 v191, v191, v97, v197
	v_max3_f32 v154, v154, v155, v191
	v_mov_b32_e32 v155, v154
	s_nop 1
	v_permlane32_swap_b32_e32 v154, v155
	v_max_f32_e32 v155, v155, v155
	v_max_f32_e32 v154, v154, v154
	v_max_f32_e32 v154, v154, v155
	s_or_b64 s[2:3], s[2:3], vcc
	v_cndmask_b32_e64 v154, v171, v154, s[2:3]
	v_sub_f32_e32 v155, v154, v152
	v_cmp_ge_f32_e64 s[4:5], s94, v155
	v_cvt_pk_bf16_f32 v219, v157, v160
	v_cvt_pk_bf16_f32 v157, v159, v162
	v_cvt_pk_bf16_f32 v158, v163, v198
	v_cvt_pk_bf16_f32 v159, v199, v201
	v_cvt_pk_bf16_f32 v160, v202, v204
	v_cvt_pk_bf16_f32 v161, v205, v208
	v_cvt_pk_bf16_f32 v162, v209, v212
	v_cvt_pk_bf16_f32 v163, v213, v216
	v_cvt_pk_bf16_f32 v198, v203, v206
	v_cvt_pk_bf16_f32 v199, v207, v210
	v_cvt_pk_bf16_f32 v200, v211, v214
	v_cvt_pk_bf16_f32 v201, v215, v217
	ds_read_b64_tr_b16 v[202:203], v153 offset:0x200
	ds_read_b64_tr_b16 v[204:205], v153 offset:0xa00
	ds_read_b64_tr_b16 v[206:207], v153 offset:0x1200
	ds_read_b64_tr_b16 v[208:209], v153 offset:0x1a00
	ds_read_b64_tr_b16 v[210:211], v153 offset:0x2200
	ds_read_b64_tr_b16 v[212:213], v153 offset:0x2a00
	ds_read_b64_tr_b16 v[214:215], v153 offset:0x3200
	ds_read_b64_tr_b16 v[216:217], v153 offset:0x3a00
	s_waitcnt lgkmcnt(8)
	v_mfma_f32_32x32x16_bf16 v[66:81], v[218:221], v[146:149], v[66:81]
	v_mfma_f32_32x32x16_bf16 v[66:81], v[156:159], v[12:15], v[66:81]
	v_mfma_f32_32x32x16_bf16 v[66:81], v[160:163], v[8:11], v[66:81]
	v_mfma_f32_32x32x16_bf16 v[66:81], v[198:201], v[4:7], v[66:81]
	ds_read_b64_tr_b16 v[4:5], v153 offset:0x400
	ds_read_b64_tr_b16 v[6:7], v153 offset:0xc00
	ds_read_b64_tr_b16 v[8:9], v153 offset:0x1400
	ds_read_b64_tr_b16 v[10:11], v153 offset:0x1c00
	ds_read_b64_tr_b16 v[12:13], v153 offset:0x2400
	ds_read_b64_tr_b16 v[14:15], v153 offset:0x2c00
	ds_read_b64_tr_b16 v[146:147], v153 offset:0x3400
	ds_read_b64_tr_b16 v[148:149], v153 offset:0x3c00
	s_waitcnt lgkmcnt(8)
	v_mfma_f32_32x32x16_bf16 v[50:65], v[198:201], v[214:217], v[50:65]
	v_mfma_f32_32x32x16_bf16 v[50:65], v[160:163], v[210:213], v[50:65]
	v_mfma_f32_32x32x16_bf16 v[50:65], v[156:159], v[206:209], v[50:65]
	v_mfma_f32_32x32x16_bf16 v[50:65], v[218:221], v[202:205], v[50:65]
	ds_read_b64_tr_b16 v[202:203], v153 offset:0x600
	ds_read_b64_tr_b16 v[204:205], v153 offset:0xe00
	ds_read_b64_tr_b16 v[206:207], v153 offset:0x1600
	ds_read_b64_tr_b16 v[208:209], v153 offset:0x1e00
	ds_read_b64_tr_b16 v[210:211], v153 offset:0x2600
	ds_read_b64_tr_b16 v[212:213], v153 offset:0x2e00
	ds_read_b64_tr_b16 v[214:215], v153 offset:0x3600
	ds_read_b64_tr_b16 v[216:217], v153 offset:0x3e00
	s_waitcnt lgkmcnt(8)
	v_mfma_f32_32x32x16_bf16 v[34:49], v[218:221], v[4:7], v[34:49]
	v_mfma_f32_32x32x16_bf16 v[34:49], v[156:159], v[8:11], v[34:49]
	v_mfma_f32_32x32x16_bf16 v[34:49], v[160:163], v[12:15], v[34:49]
	v_mfma_f32_32x32x16_bf16 v[34:49], v[198:201], v[146:149], v[34:49]
	s_waitcnt lgkmcnt(0)
	v_mfma_f32_32x32x16_bf16 v[18:33], v[218:221], v[202:205], v[18:33]
	s_andn2_b64 vcc, exec, s[72:73]
	v_mfma_f32_32x32x16_bf16 v[18:33], v[156:159], v[206:209], v[18:33]
	v_mfma_f32_32x32x16_bf16 v[18:33], v[160:163], v[210:213], v[18:33]
	v_mfma_f32_32x32x16_bf16 v[18:33], v[198:201], v[214:217], v[18:33]
	s_cbranch_vccnz .LBB0_370
	s_waitcnt vmcnt(0)

.LBB0_376:
	s_add_i32 s70, s76, 1
	s_cmp_lt_u32 s70, s68
	s_cselect_b32 s2, s70, s76
	s_lshl_b32 s2, s2, 2
	s_lshr_b32 s2, s33, s2
	s_lshl_b32 s2, s2, 8
	s_and_b32 s2, s2, 0xf00
	ds_read_b128 v[6:9], v192
	ds_read_b128 v[10:13], v192 offset:8192
	ds_read_b128 v[14:17], v190
	ds_read_b128 v[182:185], v190 offset:8192
	ds_read_b128 v[214:217], v189
	ds_read_b128 v[218:221], v189 offset:8192
	ds_read_b128 v[222:225], v188
	ds_read_b128 v[226:229], v188 offset:8192
	s_waitcnt lgkmcnt(7)
	v_mfma_f32_32x32x16_bf16 v[98:113], v[6:9], v[142:145], 0
	ds_read_b128 v[6:9], v192 offset:128
	ds_read_b128 v[192:195], v192 offset:8320
	s_waitcnt lgkmcnt(8)
	v_mfma_f32_32x32x16_bf16 v[82:97], v[10:13], v[142:145], 0
	s_waitcnt lgkmcnt(7)
	v_mfma_f32_32x32x16_bf16 v[98:113], v[14:17], v[138:141], v[98:113]
	ds_read_b128 v[10:13], v190 offset:128
	ds_read_b128 v[14:17], v190 offset:8320
	s_waitcnt lgkmcnt(8)
	v_mfma_f32_32x32x16_bf16 v[82:97], v[182:185], v[138:141], v[82:97]
	s_waitcnt lgkmcnt(7)
	v_mfma_f32_32x32x16_bf16 v[98:113], v[214:217], v[134:137], v[98:113]
	ds_read_b128 v[138:141], v189 offset:128
	ds_read_b128 v[142:145], v189 offset:8320
	s_waitcnt lgkmcnt(8)
	v_mfma_f32_32x32x16_bf16 v[82:97], v[218:221], v[134:137], v[82:97]
	s_waitcnt lgkmcnt(7)
	v_mfma_f32_32x32x16_bf16 v[98:113], v[222:225], v[130:133], v[98:113]
	ds_read_b128 v[134:137], v188 offset:128
	ds_read_b128 v[182:185], v188 offset:8320
	s_waitcnt lgkmcnt(8)
	v_mfma_f32_32x32x16_bf16 v[82:97], v[226:229], v[130:133], v[82:97]
	s_waitcnt lgkmcnt(7)
	v_mfma_f32_32x32x16_bf16 v[98:113], v[6:9], v[126:129], v[98:113]
	s_waitcnt lgkmcnt(6)
	v_mfma_f32_32x32x16_bf16 v[82:97], v[192:195], v[126:129], v[82:97]
	s_waitcnt lgkmcnt(5)
	v_mfma_f32_32x32x16_bf16 v[98:113], v[10:13], v[122:125], v[98:113]
	s_waitcnt lgkmcnt(4)
	v_mfma_f32_32x32x16_bf16 v[82:97], v[14:17], v[122:125], v[82:97]
	s_waitcnt lgkmcnt(3)
	v_mfma_f32_32x32x16_bf16 v[98:113], v[138:141], v[118:121], v[98:113]
	s_waitcnt lgkmcnt(2)
	v_mfma_f32_32x32x16_bf16 v[82:97], v[142:145], v[118:121], v[82:97]
	s_waitcnt lgkmcnt(1)
	v_mfma_f32_32x32x16_bf16 v[98:113], v[134:137], v[114:117], v[98:113]
	s_waitcnt lgkmcnt(0)
	v_mfma_f32_32x32x16_bf16 v[82:97], v[182:185], v[114:117], v[82:97]
	v_or_b32_e32 v2, s2, v151
	v_add_u32_e32 v6, s77, v2
	v_ashrrev_i32_e32 v7, 31, v6
	v_lshlrev_b64 v[6:7], 8, v[6:7]
	v_lshl_add_u64 v[6:7], s[80:81], 0, v[6:7]
	v_mov_b32_e32 v151, v3
	v_lshl_add_u64 v[6:7], v[6:7], 0, v[150:151]
	global_load_dwordx4 v[142:145], v[6:7], off
	global_load_dwordx4 v[138:141], v[6:7], off offset:32
	global_load_dwordx4 v[134:137], v[6:7], off offset:64
	global_load_dwordx4 v[130:133], v[6:7], off offset:96
	global_load_dwordx4 v[126:129], v[6:7], off offset:128
	global_load_dwordx4 v[122:125], v[6:7], off offset:160
	global_load_dwordx4 v[118:121], v[6:7], off offset:192
	global_load_dwordx4 v[114:117], v[6:7], off offset:224
	v_exp_f32_e32 v186, v146
	v_exp_f32_e32 v187, v147
	v_exp_f32_e32 v196, v156
	v_exp_f32_e32 v213, v157
	v_exp_f32_e32 v188, v148
	v_exp_f32_e32 v214, v158
	v_exp_f32_e32 v189, v149
	v_exp_f32_e32 v159, v159
	v_exp_f32_e32 v192, v152
	v_exp_f32_e32 v160, v160
	v_exp_f32_e32 v193, v153
	v_exp_f32_e32 v161, v161
	v_add_f32_e32 v2, v197, v198
	v_add_f32_e32 v5, v202, v204
	v_add_f32_e32 v146, v186, v187
	v_add_f32_e32 v147, v196, v213
	v_add_u32_e32 v190, s86, v181
	ds_read_b64_tr_b16 v[6:7], v190 offset:0
	v_exp_f32_e32 v194, v154
	v_exp_f32_e32 v162, v162
	v_add_f32_e32 v2, v199, v2
	v_add_f32_e32 v5, v206, v5
	v_add_f32_e32 v146, v188, v146
	v_add_f32_e32 v147, v214, v147
	ds_read_b64_tr_b16 v[8:9], v190 offset:0x800
	v_exp_f32_e32 v195, v155
	v_exp_f32_e32 v163, v163
	v_add_f32_e32 v2, v200, v2
	v_add_f32_e32 v5, v208, v5
	v_add_f32_e32 v146, v189, v146
	v_add_f32_e32 v147, v159, v147
	ds_read_b64_tr_b16 v[10:11], v190 offset:0x1000
	v_add_f32_e32 v2, v201, v2
	v_add_f32_e32 v5, v209, v5
	v_add_f32_e32 v146, v192, v146
	v_add_f32_e32 v147, v160, v147
	ds_read_b64_tr_b16 v[12:13], v190 offset:0x1800
	v_add_f32_e32 v2, v203, v2
	v_add_f32_e32 v5, v210, v5
	v_add_f32_e32 v146, v193, v146
	v_add_f32_e32 v147, v161, v147
	ds_read_b64_tr_b16 v[14:15], v190 offset:0x2000
	v_add_f32_e32 v2, v205, v2
	v_add_f32_e32 v5, v211, v5
	v_add_f32_e32 v146, v194, v146
	v_add_f32_e32 v147, v162, v147
	ds_read_b64_tr_b16 v[16:17], v190 offset:0x2800
	v_add_f32_e32 v2, v207, v2
	v_add_f32_e32 v5, v212, v5
	v_add_f32_e32 v146, v195, v146
	v_add_f32_e32 v147, v163, v147
	ds_read_b64_tr_b16 v[182:183], v190 offset:0x3000
	v_add_f32_e32 v2, v5, v2
	v_add_f32_e32 v5, v147, v146
	ds_read_b64_tr_b16 v[184:185], v190 offset:0x3800
	v_add_f32_e32 v2, v5, v2
	v_mov_b32_e32 v5, v2
	s_nop 1
	v_permlane32_swap_b32_e32 v2, v5
	v_cvt_pk_bf16_f32 v146, v197, v198
	v_cvt_pk_bf16_f32 v147, v199, v200
	v_cvt_pk_bf16_f32 v148, v201, v203
	v_cvt_pk_bf16_f32 v149, v205, v207
	v_cvt_pk_bf16_f32 v150, v202, v204
	v_cvt_pk_bf16_f32 v151, v206, v208
	v_cvt_pk_bf16_f32 v152, v209, v210
	v_cvt_pk_bf16_f32 v153, v211, v212
	v_cvt_pk_bf16_f32 v154, v186, v187
	v_cvt_pk_bf16_f32 v155, v188, v189
	v_cvt_pk_bf16_f32 v156, v192, v193
	v_cvt_pk_bf16_f32 v157, v194, v195
	v_cvt_pk_bf16_f32 v158, v196, v213
	v_cvt_pk_bf16_f32 v159, v214, v159
	v_cvt_pk_bf16_f32 v160, v160, v161
	v_cvt_pk_bf16_f32 v161, v162, v163
	ds_read_b64_tr_b16 v[186:187], v190 offset:0x200
	ds_read_b64_tr_b16 v[188:189], v190 offset:0xa00
	ds_read_b64_tr_b16 v[192:193], v190 offset:0x1200
	ds_read_b64_tr_b16 v[194:195], v190 offset:0x1a00
	ds_read_b64_tr_b16 v[196:197], v190 offset:0x2200
	ds_read_b64_tr_b16 v[198:199], v190 offset:0x2a00
	ds_read_b64_tr_b16 v[200:201], v190 offset:0x3200
	ds_read_b64_tr_b16 v[202:203], v190 offset:0x3a00
	s_waitcnt lgkmcnt(8)
	v_mfma_f32_32x32x16_bf16 v[66:81], v[146:149], v[6:9], v[66:81]
	v_mfma_f32_32x32x16_bf16 v[66:81], v[150:153], v[10:13], v[66:81]
	v_mfma_f32_32x32x16_bf16 v[66:81], v[154:157], v[14:17], v[66:81]
	v_mfma_f32_32x32x16_bf16 v[66:81], v[158:161], v[182:185], v[66:81]
	ds_read_b64_tr_b16 v[6:7], v190 offset:0x400
	ds_read_b64_tr_b16 v[8:9], v190 offset:0xc00
	ds_read_b64_tr_b16 v[10:11], v190 offset:0x1400
	ds_read_b64_tr_b16 v[12:13], v190 offset:0x1c00
	ds_read_b64_tr_b16 v[14:15], v190 offset:0x2400
	ds_read_b64_tr_b16 v[16:17], v190 offset:0x2c00
	ds_read_b64_tr_b16 v[182:183], v190 offset:0x3400
	ds_read_b64_tr_b16 v[184:185], v190 offset:0x3c00
	s_waitcnt lgkmcnt(8)
	v_mfma_f32_32x32x16_bf16 v[50:65], v[158:161], v[200:203], v[50:65]
	v_mfma_f32_32x32x16_bf16 v[50:65], v[154:157], v[196:199], v[50:65]
	v_mfma_f32_32x32x16_bf16 v[50:65], v[150:153], v[192:195], v[50:65]
	v_mfma_f32_32x32x16_bf16 v[50:65], v[146:149], v[186:189], v[50:65]
	ds_read_b64_tr_b16 v[186:187], v190 offset:0x600
	ds_read_b64_tr_b16 v[188:189], v190 offset:0xe00
	ds_read_b64_tr_b16 v[192:193], v190 offset:0x1600
	ds_read_b64_tr_b16 v[194:195], v190 offset:0x1e00
	ds_read_b64_tr_b16 v[196:197], v190 offset:0x2600
	ds_read_b64_tr_b16 v[198:199], v190 offset:0x2e00
	ds_read_b64_tr_b16 v[200:201], v190 offset:0x3600
	ds_read_b64_tr_b16 v[202:203], v190 offset:0x3e00
	s_waitcnt lgkmcnt(8)
	v_mfma_f32_32x32x16_bf16 v[34:49], v[146:149], v[6:9], v[34:49]
	v_mfma_f32_32x32x16_bf16 v[34:49], v[150:153], v[10:13], v[34:49]
	v_mfma_f32_32x32x16_bf16 v[34:49], v[154:157], v[14:17], v[34:49]
	v_mfma_f32_32x32x16_bf16 v[34:49], v[158:161], v[182:185], v[34:49]
	s_waitcnt lgkmcnt(0)
	v_mfma_f32_32x32x16_bf16 v[18:33], v[146:149], v[186:189], v[18:33]
	s_cmp_gt_i32 s95, 7
	v_mfma_f32_32x32x16_bf16 v[18:33], v[150:153], v[192:195], v[18:33]
	v_mfma_f32_32x32x16_bf16 v[18:33], v[154:157], v[196:199], v[18:33]
	v_mfma_f32_32x32x16_bf16 v[18:33], v[158:161], v[200:203], v[18:33]
	s_cbranch_scc1 .LBB0_378
	s_or_b32 s2, s97, 0xc0
	v_subrev_u32_e32 v6, s2, v180
	v_cmp_gt_i32_e64 s[60:61], 26, v6
	v_cmp_gt_i32_e64 s[62:63], 27, v6
	v_cmp_gt_i32_e64 s[58:59], 25, v6
	s_and_b64 s[60:61], s[62:63], s[60:61]
	v_cmp_gt_i32_e64 s[56:57], 24, v6
	s_and_b64 s[58:59], s[60:61], s[58:59]
	v_cmp_gt_i32_e64 s[54:55], 19, v6
	s_and_b64 s[56:57], s[58:59], s[56:57]
	v_cmp_gt_i32_e64 s[52:53], 18, v6
	s_and_b64 s[54:55], s[56:57], s[54:55]
	v_cmp_gt_i32_e64 s[50:51], 17, v6
	s_and_b64 s[52:53], s[54:55], s[52:53]
	v_cmp_gt_i32_e64 s[48:49], 16, v6
	s_and_b64 s[50:51], s[52:53], s[50:51]
	v_cmp_gt_i32_e64 s[46:47], 11, v6
	s_and_b64 s[48:49], s[50:51], s[48:49]
	v_cmp_gt_i32_e64 s[44:45], 10, v6
	s_and_b64 s[46:47], s[48:49], s[46:47]
	v_cmp_gt_i32_e64 s[42:43], 9, v6
	s_and_b64 s[44:45], s[46:47], s[44:45]
	v_cmp_gt_i32_e64 s[40:41], 8, v6
	s_and_b64 s[42:43], s[44:45], s[42:43]
	v_cmp_gt_i32_e64 s[38:39], 3, v6
	s_and_b64 s[40:41], s[42:43], s[40:41]
	v_cmp_gt_i32_e64 s[36:37], 2, v6
	s_and_b64 s[38:39], s[40:41], s[38:39]
	v_cmp_gt_i32_e64 s[34:35], 1, v6
	s_and_b64 s[36:37], s[38:39], s[36:37]
	v_cmp_gt_i32_e64 s[30:31], 0, v6
	s_and_b64 s[34:35], s[36:37], s[34:35]
	s_and_b64 s[30:31], s[34:35], s[30:31]
	v_cmp_gt_i32_e64 s[28:29], 58, v6
	v_cndmask_b32_e64 v98, v98, v171, s[30:31]
	v_cmp_gt_i32_e64 s[30:31], 59, v6
	v_cmp_gt_i32_e64 s[26:27], 57, v6
	s_and_b64 s[28:29], s[30:31], s[28:29]
	v_cmp_gt_i32_e64 s[24:25], 56, v6
	s_and_b64 s[26:27], s[28:29], s[26:27]
	v_cmp_gt_i32_e64 s[22:23], 51, v6
	s_and_b64 s[24:25], s[26:27], s[24:25]
	v_cmp_gt_i32_e64 s[20:21], 50, v6
	s_and_b64 s[22:23], s[24:25], s[22:23]
	v_cmp_gt_i32_e64 s[18:19], 49, v6
	s_and_b64 s[20:21], s[22:23], s[20:21]
	v_cmp_gt_i32_e64 s[16:17], 48, v6
	s_and_b64 s[18:19], s[20:21], s[18:19]
	v_cmp_gt_i32_e64 s[14:15], 43, v6
	s_and_b64 s[16:17], s[18:19], s[16:17]
	v_cmp_gt_i32_e64 s[12:13], 42, v6
	s_and_b64 s[14:15], s[16:17], s[14:15]
	v_cmp_gt_i32_e64 s[10:11], 41, v6
	s_and_b64 s[12:13], s[14:15], s[12:13]
	v_cmp_gt_i32_e64 s[8:9], 40, v6
	s_and_b64 s[10:11], s[12:13], s[10:11]
	v_cmp_gt_i32_e64 s[6:7], 35, v6
	s_and_b64 s[8:9], s[10:11], s[8:9]
	v_cmp_gt_i32_e64 s[4:5], 34, v6
	s_and_b64 s[6:7], s[8:9], s[6:7]
	v_cmp_gt_i32_e64 s[2:3], 33, v6
	s_and_b64 s[4:5], s[6:7], s[4:5]
	v_cmp_gt_i32_e32 vcc, 32, v6
	s_and_b64 s[2:3], s[4:5], s[2:3]
	s_and_b64 vcc, s[2:3], vcc
	v_cndmask_b32_e64 v113, v113, v171, s[62:63]
	v_cndmask_b32_e64 v112, v112, v171, s[60:61]
	v_cndmask_b32_e64 v111, v111, v171, s[58:59]
	v_cndmask_b32_e64 v110, v110, v171, s[56:57]
	v_cndmask_b32_e64 v109, v109, v171, s[54:55]
	v_cndmask_b32_e64 v108, v108, v171, s[52:53]
	v_cndmask_b32_e64 v107, v107, v171, s[50:51]
	v_cndmask_b32_e64 v106, v106, v171, s[48:49]
	v_cndmask_b32_e64 v105, v105, v171, s[46:47]
	v_cndmask_b32_e64 v104, v104, v171, s[44:45]
	v_cndmask_b32_e64 v103, v103, v171, s[42:43]
	v_cndmask_b32_e64 v102, v102, v171, s[40:41]
	v_cndmask_b32_e64 v101, v101, v171, s[38:39]
	v_cndmask_b32_e64 v100, v100, v171, s[36:37]
	v_cndmask_b32_e64 v99, v99, v171, s[34:35]
	v_cndmask_b32_e64 v97, v97, v171, s[30:31]
	v_cndmask_b32_e64 v96, v96, v171, s[28:29]
	v_cndmask_b32_e64 v95, v95, v171, s[26:27]
	v_cndmask_b32_e64 v94, v94, v171, s[24:25]
	v_cndmask_b32_e64 v93, v93, v171, s[22:23]
	v_cndmask_b32_e64 v92, v92, v171, s[20:21]
	v_cndmask_b32_e64 v91, v91, v171, s[18:19]
	v_cndmask_b32_e64 v90, v90, v171, s[16:17]
	v_cndmask_b32_e64 v89, v89, v171, s[14:15]
	v_cndmask_b32_e64 v88, v88, v171, s[12:13]
	v_cndmask_b32_e64 v87, v87, v171, s[10:11]
	v_cndmask_b32_e64 v86, v86, v171, s[8:9]
	v_cndmask_b32_e64 v85, v85, v171, s[6:7]
	v_cndmask_b32_e64 v84, v84, v171, s[4:5]
	v_cndmask_b32_e64 v83, v83, v171, s[2:3]
	v_cndmask_b32_e32 v82, v82, v171, vcc

.LBB0_382:
	v_cndmask_b32_e64 v7, v7, v191, s[2:3]
	v_sub_f32_e32 v8, v98, v7
	v_sub_f32_e32 v13, v101, v7
	v_sub_f32_e32 v14, v102, v7
	v_sub_f32_e32 v101, v105, v7
	v_sub_f32_e32 v105, v108, v7
	v_sub_f32_e32 v10, v99, v7
	v_sub_f32_e32 v17, v103, v7
	v_sub_f32_e32 v98, v104, v7
	v_sub_f32_e32 v102, v106, v7
	v_sub_f32_e32 v104, v107, v7
	v_sub_f32_e32 v106, v109, v7
	v_sub_f32_e32 v107, v110, v7
	v_sub_f32_e32 v109, v112, v7
	v_sub_f32_e32 v110, v113, v7
	v_exp_f32_e32 v9, v8
	v_exp_f32_e32 v16, v14
	v_exp_f32_e32 v14, v105
	v_sub_f32_e32 v8, v82, v7
	v_sub_f32_e32 v105, v83, v7
	v_sub_f32_e32 v112, v90, v7
	v_sub_f32_e32 v113, v91, v7
	v_sub_f32_e32 v12, v100, v7
	v_exp_f32_e32 v11, v10
	v_exp_f32_e32 v15, v13
	v_exp_f32_e32 v99, v17
	v_exp_f32_e32 v10, v102
	v_exp_f32_e32 v13, v104
	v_exp_f32_e32 v17, v106
	v_sub_f32_e32 v106, v84, v7
	v_sub_f32_e32 v146, v92, v7
	v_exp_f32_e32 v151, v8
	v_exp_f32_e32 v105, v105
	v_exp_f32_e32 v112, v112
	v_exp_f32_e32 v113, v113
	v_sub_f32_e32 v108, v111, v7
	v_exp_f32_e32 v12, v12
	v_exp_f32_e32 v100, v98
	v_exp_f32_e32 v98, v107
	v_sub_f32_e32 v107, v85, v7
	v_sub_f32_e32 v147, v93, v7
	v_exp_f32_e32 v152, v106
	v_exp_f32_e32 v146, v146
	v_exp_f32_e32 v103, v101
	v_exp_f32_e32 v101, v108
	v_sub_f32_e32 v108, v86, v7
	v_sub_f32_e32 v148, v94, v7
	v_exp_f32_e32 v153, v107
	v_exp_f32_e32 v147, v147
	v_exp_f32_e32 v102, v109
	v_exp_f32_e32 v104, v110
	v_sub_f32_e32 v109, v87, v7
	v_sub_f32_e32 v110, v88, v7
	v_sub_f32_e32 v111, v89, v7
	v_sub_f32_e32 v149, v95, v7
	v_sub_f32_e32 v150, v96, v7
	v_sub_f32_e32 v7, v97, v7
	v_exp_f32_e32 v155, v108
	v_exp_f32_e32 v148, v148
	v_exp_f32_e32 v156, v109
	v_exp_f32_e32 v149, v149
	v_exp_f32_e32 v157, v7
	v_add_f32_e32 v7, v9, v11
	v_add_f32_e32 v8, v10, v13
	v_add_f32_e32 v106, v151, v105
	v_add_f32_e32 v107, v112, v113
	v_add_u32_e32 v154, s89, v181
	ds_read_b64_tr_b16 v[82:83], v154 offset:0
	v_exp_f32_e32 v110, v110
	v_exp_f32_e32 v150, v150
	v_add_f32_e32 v7, v12, v7
	v_add_f32_e32 v8, v14, v8
	v_add_f32_e32 v106, v152, v106
	v_add_f32_e32 v107, v146, v107
	ds_read_b64_tr_b16 v[84:85], v154 offset:0x800
	v_exp_f32_e32 v111, v111
	v_add_f32_e32 v7, v15, v7
	v_add_f32_e32 v8, v17, v8
	v_add_f32_e32 v106, v153, v106
	v_add_f32_e32 v107, v147, v107
	ds_read_b64_tr_b16 v[86:87], v154 offset:0x1000
	v_add_f32_e32 v7, v16, v7
	v_add_f32_e32 v8, v98, v8
	v_add_f32_e32 v106, v155, v106
	v_add_f32_e32 v107, v148, v107
	ds_read_b64_tr_b16 v[88:89], v154 offset:0x1800
	v_add_f32_e32 v7, v99, v7
	v_add_f32_e32 v8, v101, v8
	v_add_f32_e32 v106, v156, v106
	v_add_f32_e32 v107, v149, v107
	ds_read_b64_tr_b16 v[90:91], v154 offset:0x2000
	v_add_f32_e32 v7, v100, v7
	v_add_f32_e32 v8, v102, v8
	v_add_f32_e32 v106, v110, v106
	v_add_f32_e32 v107, v150, v107
	ds_read_b64_tr_b16 v[92:93], v154 offset:0x2800
	v_add_f32_e32 v7, v103, v7
	v_add_f32_e32 v8, v104, v8
	v_add_f32_e32 v106, v111, v106
	v_add_f32_e32 v107, v157, v107
	ds_read_b64_tr_b16 v[94:95], v154 offset:0x3000
	v_add_f32_e32 v7, v8, v7
	v_add_f32_e32 v8, v107, v106
	ds_read_b64_tr_b16 v[96:97], v154 offset:0x3800
	v_add_f32_e32 v7, v8, v7
	v_mov_b32_e32 v8, v7
	s_nop 1
	v_permlane32_swap_b32_e32 v7, v8
	v_cvt_pk_bf16_f32 v106, v9, v11
	v_cvt_pk_bf16_f32 v107, v12, v15
	v_cvt_pk_bf16_f32 v108, v16, v99
	v_cvt_pk_bf16_f32 v109, v100, v103
	v_cvt_pk_bf16_f32 v10, v10, v13
	v_cvt_pk_bf16_f32 v11, v14, v17
	v_cvt_pk_bf16_f32 v12, v98, v101
	v_cvt_pk_bf16_f32 v13, v102, v104
	v_cvt_pk_bf16_f32 v14, v151, v105
	v_cvt_pk_bf16_f32 v15, v152, v153
	v_cvt_pk_bf16_f32 v16, v155, v156
	v_cvt_pk_bf16_f32 v17, v110, v111
	v_cvt_pk_bf16_f32 v98, v112, v113
	v_cvt_pk_bf16_f32 v99, v146, v147
	v_cvt_pk_bf16_f32 v100, v148, v149
	v_cvt_pk_bf16_f32 v101, v150, v157
	ds_read_b64_tr_b16 v[102:103], v154 offset:0x200
	ds_read_b64_tr_b16 v[104:105], v154 offset:0xa00
	ds_read_b64_tr_b16 v[110:111], v154 offset:0x1200
	ds_read_b64_tr_b16 v[112:113], v154 offset:0x1a00
	ds_read_b64_tr_b16 v[146:147], v154 offset:0x2200
	ds_read_b64_tr_b16 v[148:149], v154 offset:0x2a00
	ds_read_b64_tr_b16 v[150:151], v154 offset:0x3200
	ds_read_b64_tr_b16 v[152:153], v154 offset:0x3a00
	s_waitcnt lgkmcnt(8)
	v_mfma_f32_32x32x16_bf16 v[66:81], v[106:109], v[82:85], v[66:81]
	v_mfma_f32_32x32x16_bf16 v[66:81], v[10:13], v[86:89], v[66:81]
	v_mfma_f32_32x32x16_bf16 v[66:81], v[14:17], v[90:93], v[66:81]
	v_mfma_f32_32x32x16_bf16 v[66:81], v[98:101], v[94:97], v[66:81]
	ds_read_b64_tr_b16 v[82:83], v154 offset:0x400
	ds_read_b64_tr_b16 v[84:85], v154 offset:0xc00
	ds_read_b64_tr_b16 v[86:87], v154 offset:0x1400
	ds_read_b64_tr_b16 v[88:89], v154 offset:0x1c00
	ds_read_b64_tr_b16 v[90:91], v154 offset:0x2400
	ds_read_b64_tr_b16 v[92:93], v154 offset:0x2c00
	ds_read_b64_tr_b16 v[94:95], v154 offset:0x3400
	ds_read_b64_tr_b16 v[96:97], v154 offset:0x3c00
	s_waitcnt lgkmcnt(8)
	v_mfma_f32_32x32x16_bf16 v[50:65], v[98:101], v[150:153], v[50:65]
	v_mfma_f32_32x32x16_bf16 v[50:65], v[14:17], v[146:149], v[50:65]
	v_mfma_f32_32x32x16_bf16 v[50:65], v[10:13], v[110:113], v[50:65]
	v_mfma_f32_32x32x16_bf16 v[50:65], v[106:109], v[102:105], v[50:65]
	ds_read_b64_tr_b16 v[102:103], v154 offset:0x600
	ds_read_b64_tr_b16 v[104:105], v154 offset:0xe00
	ds_read_b64_tr_b16 v[110:111], v154 offset:0x1600
	ds_read_b64_tr_b16 v[112:113], v154 offset:0x1e00
	ds_read_b64_tr_b16 v[146:147], v154 offset:0x2600
	ds_read_b64_tr_b16 v[148:149], v154 offset:0x2e00
	ds_read_b64_tr_b16 v[150:151], v154 offset:0x3600
	ds_read_b64_tr_b16 v[152:153], v154 offset:0x3e00
	s_waitcnt lgkmcnt(8)
	v_mfma_f32_32x32x16_bf16 v[34:49], v[106:109], v[82:85], v[34:49]
	v_mfma_f32_32x32x16_bf16 v[34:49], v[10:13], v[86:89], v[34:49]
	v_mfma_f32_32x32x16_bf16 v[34:49], v[14:17], v[90:93], v[34:49]
	v_mfma_f32_32x32x16_bf16 v[34:49], v[98:101], v[94:97], v[34:49]
	s_waitcnt lgkmcnt(0)
	v_mfma_f32_32x32x16_bf16 v[18:33], v[98:101], v[150:153], v[18:33]
	v_mfma_f32_32x32x16_bf16 v[18:33], v[14:17], v[146:149], v[18:33]
	v_mfma_f32_32x32x16_bf16 v[18:33], v[10:13], v[110:113], v[18:33]
	v_mfma_f32_32x32x16_bf16 v[18:33], v[106:109], v[102:105], v[18:33]
	s_mov_b32 m0, s96
	s_movk_i32 s2, 0x2000
	buffer_load_dwordx4 v175, s[64:67], 0 offen lds
	s_mov_b32 m0, s93
	s_nop 0
	buffer_load_dwordx4 v175, s[64:67], s2 offen lds
	s_and_saveexec_b64 s[2:3], s[0:1]
	s_cbranch_execz .LBB0_354
	v_add_f32_e32 v2, v2, v5
	v_fmac_f32_e32 v2, v179, v4
	v_add_f32_e32 v4, v7, v8
	v_fmac_f32_e32 v4, v2, v6
	ds_write_b32 v178, v4
	s_branch .LBB0_354

.LBB0_393:
	s_mov_b32 m0, s92
	s_add_i32 s2, s88, 0xff000000
	buffer_load_dwordx4 v175, s[64:67], s2 offen lds
	s_add_i32 s2, s88, 0xff002000
	s_mov_b32 m0, s71
	s_nop 0
	buffer_load_dwordx4 v175, s[64:67], s2 offen lds
	s_add_i32 s2, s95, s86
	s_mov_b32 m0, s2
	s_nop 0
	buffer_load_dwordx4 v182, s[64:67], s88 offen lds
	s_add_i32 m0, s2, 0x400
	s_add_i32 s2, s88, 0x80
	buffer_load_dwordx4 v182, s[64:67], s2 offen lds
	ds_read_b128 v[4:7], v192
	ds_read_b128 v[8:11], v192 offset:8192
	ds_read_b128 v[12:15], v191
	ds_read_b128 v[212:215], v191 offset:8192
	ds_read_b128 v[216:219], v190
	ds_read_b128 v[220:223], v190 offset:8192
	ds_read_b128 v[224:227], v189
	ds_read_b128 v[228:231], v189 offset:8192
	s_waitcnt lgkmcnt(7)
	v_mfma_f32_32x32x16_bf16 v[98:113], v[4:7], v[142:145], 0
	ds_read_b128 v[4:7], v192 offset:128
	ds_read_b128 v[232:235], v192 offset:8320
	s_waitcnt lgkmcnt(8)
	v_mfma_f32_32x32x16_bf16 v[82:97], v[8:11], v[142:145], 0
	s_waitcnt lgkmcnt(7)
	v_mfma_f32_32x32x16_bf16 v[98:113], v[12:15], v[138:141], v[98:113]
	ds_read_b128 v[8:11], v191 offset:128
	ds_read_b128 v[12:15], v191 offset:8320
	s_waitcnt lgkmcnt(8)
	v_mfma_f32_32x32x16_bf16 v[82:97], v[212:215], v[138:141], v[82:97]
	s_waitcnt lgkmcnt(7)
	v_mfma_f32_32x32x16_bf16 v[98:113], v[216:219], v[134:137], v[98:113]
	ds_read_b128 v[212:215], v190 offset:128
	ds_read_b128 v[216:219], v190 offset:8320
	s_waitcnt lgkmcnt(8)
	v_mfma_f32_32x32x16_bf16 v[82:97], v[220:223], v[134:137], v[82:97]
	s_waitcnt lgkmcnt(7)
	v_mfma_f32_32x32x16_bf16 v[98:113], v[224:227], v[130:133], v[98:113]
	ds_read_b128 v[220:223], v189 offset:128
	ds_read_b128 v[224:227], v189 offset:8320
	s_waitcnt lgkmcnt(8)
	v_mfma_f32_32x32x16_bf16 v[82:97], v[228:231], v[130:133], v[82:97]
	s_waitcnt lgkmcnt(7)
	v_mfma_f32_32x32x16_bf16 v[98:113], v[4:7], v[126:129], v[98:113]
	s_waitcnt lgkmcnt(6)
	v_mfma_f32_32x32x16_bf16 v[82:97], v[232:235], v[126:129], v[82:97]
	s_waitcnt lgkmcnt(5)
	v_mfma_f32_32x32x16_bf16 v[98:113], v[8:11], v[122:125], v[98:113]
	s_waitcnt lgkmcnt(4)
	v_mfma_f32_32x32x16_bf16 v[82:97], v[12:15], v[122:125], v[82:97]
	s_waitcnt lgkmcnt(3)
	v_mfma_f32_32x32x16_bf16 v[98:113], v[212:215], v[118:121], v[98:113]
	s_waitcnt lgkmcnt(2)
	v_mfma_f32_32x32x16_bf16 v[82:97], v[216:219], v[118:121], v[82:97]
	s_waitcnt lgkmcnt(1)
	v_mfma_f32_32x32x16_bf16 v[98:113], v[220:223], v[114:117], v[98:113]
	s_waitcnt lgkmcnt(0)
	v_mfma_f32_32x32x16_bf16 v[82:97], v[224:227], v[114:117], v[82:97]
	v_exp_f32_e32 v211, v148
	v_exp_f32_e32 v216, v149
	v_exp_f32_e32 v223, v156
	v_exp_f32_e32 v224, v157
	v_exp_f32_e32 v217, v150
	v_exp_f32_e32 v225, v158
	v_exp_f32_e32 v218, v151
	v_exp_f32_e32 v226, v159
	v_exp_f32_e32 v219, v152
	v_exp_f32_e32 v227, v160
	v_exp_f32_e32 v220, v153
	v_exp_f32_e32 v228, v161
	v_add_f32_e32 v2, v195, v196
	v_add_f32_e32 v4, v200, v202
	v_add_f32_e32 v148, v211, v216
	v_add_f32_e32 v149, v223, v224
	v_add_u32_e32 v5, s4, v181
	ds_read_b64_tr_b16 v[6:7], v5 offset:0
	v_exp_f32_e32 v221, v154
	v_exp_f32_e32 v229, v162
	v_add_f32_e32 v2, v197, v2
	v_add_f32_e32 v4, v204, v4
	v_add_f32_e32 v148, v217, v148
	v_add_f32_e32 v149, v225, v149
	ds_read_b64_tr_b16 v[8:9], v5 offset:0x800
	v_exp_f32_e32 v222, v155
	v_exp_f32_e32 v163, v163
	v_add_f32_e32 v2, v198, v2
	v_add_f32_e32 v4, v206, v4
	v_add_f32_e32 v148, v218, v148
	v_add_f32_e32 v149, v226, v149
	ds_read_b64_tr_b16 v[10:11], v5 offset:0x1000
	v_add_f32_e32 v2, v199, v2
	v_add_f32_e32 v4, v207, v4
	v_add_f32_e32 v148, v219, v148
	v_add_f32_e32 v149, v227, v149
	ds_read_b64_tr_b16 v[12:13], v5 offset:0x1800
	v_add_f32_e32 v2, v201, v2
	v_add_f32_e32 v4, v208, v4
	v_add_f32_e32 v148, v220, v148
	v_add_f32_e32 v149, v228, v149
	ds_read_b64_tr_b16 v[14:15], v5 offset:0x2000
	v_add_f32_e32 v2, v203, v2
	v_add_f32_e32 v4, v209, v4
	v_add_f32_e32 v148, v221, v148
	v_add_f32_e32 v149, v229, v149
	ds_read_b64_tr_b16 v[16:17], v5 offset:0x2800
	v_add_f32_e32 v2, v205, v2
	v_add_f32_e32 v4, v210, v4
	v_add_f32_e32 v148, v222, v148
	v_add_f32_e32 v149, v163, v149
	ds_read_b64_tr_b16 v[212:213], v5 offset:0x3000
	v_add_f32_e32 v2, v4, v2
	v_add_f32_e32 v4, v149, v148
	ds_read_b64_tr_b16 v[214:215], v5 offset:0x3800
	v_add_f32_e32 v2, v2, v4
	v_mov_b32_e32 v4, v2
	s_nop 1
	v_permlane32_swap_b32_e32 v2, v4
	v_cvt_pk_bf16_f32 v148, v195, v196
	v_cvt_pk_bf16_f32 v149, v197, v198
	v_cvt_pk_bf16_f32 v150, v199, v201
	v_cvt_pk_bf16_f32 v151, v203, v205
	v_cvt_pk_bf16_f32 v152, v200, v202
	v_cvt_pk_bf16_f32 v153, v204, v206
	v_cvt_pk_bf16_f32 v154, v207, v208
	v_cvt_pk_bf16_f32 v155, v209, v210
	v_cvt_pk_bf16_f32 v156, v211, v216
	v_cvt_pk_bf16_f32 v157, v217, v218
	v_cvt_pk_bf16_f32 v158, v219, v220
	v_cvt_pk_bf16_f32 v159, v221, v222
	v_cvt_pk_bf16_f32 v160, v223, v224
	v_cvt_pk_bf16_f32 v161, v225, v226
	v_cvt_pk_bf16_f32 v162, v227, v228
	v_cvt_pk_bf16_f32 v163, v229, v163
	ds_read_b64_tr_b16 v[196:197], v5 offset:0x200
	ds_read_b64_tr_b16 v[198:199], v5 offset:0xa00
	ds_read_b64_tr_b16 v[200:201], v5 offset:0x1200
	ds_read_b64_tr_b16 v[202:203], v5 offset:0x1a00
	ds_read_b64_tr_b16 v[204:205], v5 offset:0x2200
	ds_read_b64_tr_b16 v[206:207], v5 offset:0x2a00
	ds_read_b64_tr_b16 v[208:209], v5 offset:0x3200
	ds_read_b64_tr_b16 v[210:211], v5 offset:0x3a00
	s_waitcnt lgkmcnt(8)
	v_mfma_f32_32x32x16_bf16 v[66:81], v[148:151], v[6:9], v[66:81]
	v_mfma_f32_32x32x16_bf16 v[66:81], v[152:155], v[10:13], v[66:81]
	v_mfma_f32_32x32x16_bf16 v[66:81], v[156:159], v[14:17], v[66:81]
	v_mfma_f32_32x32x16_bf16 v[66:81], v[160:163], v[212:215], v[66:81]
	ds_read_b64_tr_b16 v[6:7], v5 offset:0x400
	ds_read_b64_tr_b16 v[8:9], v5 offset:0xc00
	ds_read_b64_tr_b16 v[10:11], v5 offset:0x1400
	ds_read_b64_tr_b16 v[12:13], v5 offset:0x1c00
	ds_read_b64_tr_b16 v[14:15], v5 offset:0x2400
	ds_read_b64_tr_b16 v[16:17], v5 offset:0x2c00
	ds_read_b64_tr_b16 v[212:213], v5 offset:0x3400
	ds_read_b64_tr_b16 v[214:215], v5 offset:0x3c00
	s_waitcnt lgkmcnt(8)
	v_mfma_f32_32x32x16_bf16 v[50:65], v[160:163], v[208:211], v[50:65]
	v_mfma_f32_32x32x16_bf16 v[50:65], v[156:159], v[204:207], v[50:65]
	v_mfma_f32_32x32x16_bf16 v[50:65], v[152:155], v[200:203], v[50:65]
	v_mfma_f32_32x32x16_bf16 v[50:65], v[148:151], v[196:199], v[50:65]
	ds_read_b64_tr_b16 v[196:197], v5 offset:0x600
	ds_read_b64_tr_b16 v[198:199], v5 offset:0xe00
	ds_read_b64_tr_b16 v[200:201], v5 offset:0x1600
	ds_read_b64_tr_b16 v[202:203], v5 offset:0x1e00
	ds_read_b64_tr_b16 v[204:205], v5 offset:0x2600
	ds_read_b64_tr_b16 v[206:207], v5 offset:0x2e00
	ds_read_b64_tr_b16 v[208:209], v5 offset:0x3600
	ds_read_b64_tr_b16 v[210:211], v5 offset:0x3e00
	s_waitcnt lgkmcnt(8)
	v_mfma_f32_32x32x16_bf16 v[34:49], v[148:151], v[6:9], v[34:49]
	v_mfma_f32_32x32x16_bf16 v[34:49], v[152:155], v[10:13], v[34:49]
	v_mfma_f32_32x32x16_bf16 v[34:49], v[156:159], v[14:17], v[34:49]
	v_mfma_f32_32x32x16_bf16 v[34:49], v[160:163], v[212:215], v[34:49]
	s_waitcnt lgkmcnt(0)
	v_mfma_f32_32x32x16_bf16 v[18:33], v[148:151], v[196:199], v[18:33]
	s_sub_i32 s2, s87, 64
	s_cmp_le_i32 s2, s70
	v_mfma_f32_32x32x16_bf16 v[18:33], v[152:155], v[200:203], v[18:33]
	v_mfma_f32_32x32x16_bf16 v[18:33], v[156:159], v[204:207], v[18:33]
	v_mfma_f32_32x32x16_bf16 v[18:33], v[160:163], v[208:211], v[18:33]
	s_cbranch_scc1 .LBB0_395
	v_add_u32_e32 v5, 64, v193
	v_cmp_gt_i32_e64 s[60:61], 26, v5
	v_cmp_gt_i32_e64 s[62:63], 27, v5
	v_cmp_gt_i32_e64 s[58:59], 25, v5
	s_and_b64 s[60:61], s[62:63], s[60:61]
	v_cmp_gt_i32_e64 s[56:57], 24, v5
	s_and_b64 s[58:59], s[60:61], s[58:59]
	v_cmp_gt_i32_e64 s[54:55], 19, v5
	s_and_b64 s[56:57], s[58:59], s[56:57]
	v_cmp_gt_i32_e64 s[52:53], 18, v5
	s_and_b64 s[54:55], s[56:57], s[54:55]
	v_cmp_gt_i32_e64 s[50:51], 17, v5
	s_and_b64 s[52:53], s[54:55], s[52:53]
	v_cmp_gt_i32_e64 s[48:49], 16, v5
	s_and_b64 s[50:51], s[52:53], s[50:51]
	v_cmp_gt_i32_e64 s[46:47], 11, v5
	s_and_b64 s[48:49], s[50:51], s[48:49]
	v_cmp_gt_i32_e64 s[44:45], 10, v5
	s_and_b64 s[46:47], s[48:49], s[46:47]
	v_cmp_gt_i32_e64 s[42:43], 9, v5
	s_and_b64 s[44:45], s[46:47], s[44:45]
	v_cmp_gt_i32_e64 s[40:41], 8, v5
	s_and_b64 s[42:43], s[44:45], s[42:43]
	v_cmp_gt_i32_e64 s[38:39], 3, v5
	s_and_b64 s[40:41], s[42:43], s[40:41]
	v_cmp_gt_i32_e64 s[36:37], 2, v5
	s_and_b64 s[38:39], s[40:41], s[38:39]
	v_cmp_gt_i32_e64 s[34:35], 1, v5
	s_and_b64 s[36:37], s[38:39], s[36:37]
	v_cmp_gt_i32_e64 s[30:31], 0, v5
	s_and_b64 s[34:35], s[36:37], s[34:35]
	s_and_b64 s[30:31], s[34:35], s[30:31]
	v_cmp_gt_i32_e64 s[28:29], 58, v5
	v_cndmask_b32_e64 v98, v98, v171, s[30:31]
	v_cmp_gt_i32_e64 s[30:31], 59, v5
	v_cmp_gt_i32_e64 s[26:27], 57, v5
	s_and_b64 s[28:29], s[30:31], s[28:29]
	v_cmp_gt_i32_e64 s[24:25], 56, v5
	s_and_b64 s[26:27], s[28:29], s[26:27]
	v_cmp_gt_i32_e64 s[22:23], 51, v5
	s_and_b64 s[24:25], s[26:27], s[24:25]
	v_cmp_gt_i32_e64 s[20:21], 50, v5
	s_and_b64 s[22:23], s[24:25], s[22:23]
	v_cmp_gt_i32_e64 s[18:19], 49, v5
	s_and_b64 s[20:21], s[22:23], s[20:21]
	v_cmp_gt_i32_e64 s[16:17], 48, v5
	s_and_b64 s[18:19], s[20:21], s[18:19]
	v_cmp_gt_i32_e64 s[14:15], 43, v5
	s_and_b64 s[16:17], s[18:19], s[16:17]
	v_cmp_gt_i32_e64 s[12:13], 42, v5
	s_and_b64 s[14:15], s[16:17], s[14:15]
	v_cmp_gt_i32_e64 s[10:11], 41, v5
	s_and_b64 s[12:13], s[14:15], s[12:13]
	v_cmp_gt_i32_e64 s[8:9], 40, v5
	s_and_b64 s[10:11], s[12:13], s[10:11]
	v_cmp_gt_i32_e64 s[6:7], 35, v5
	s_and_b64 s[8:9], s[10:11], s[8:9]
	v_cmp_gt_i32_e64 s[4:5], 34, v5
	s_and_b64 s[6:7], s[8:9], s[6:7]
	v_cmp_gt_i32_e64 s[2:3], 33, v5
	s_and_b64 s[4:5], s[6:7], s[4:5]
	v_cmp_gt_i32_e32 vcc, 32, v5
	s_and_b64 s[2:3], s[4:5], s[2:3]
	s_and_b64 vcc, s[2:3], vcc
	v_cndmask_b32_e64 v113, v113, v171, s[62:63]
	v_cndmask_b32_e64 v112, v112, v171, s[60:61]
	v_cndmask_b32_e64 v111, v111, v171, s[58:59]
	v_cndmask_b32_e64 v110, v110, v171, s[56:57]
	v_cndmask_b32_e64 v109, v109, v171, s[54:55]
	v_cndmask_b32_e64 v108, v108, v171, s[52:53]
	v_cndmask_b32_e64 v107, v107, v171, s[50:51]
	v_cndmask_b32_e64 v106, v106, v171, s[48:49]
	v_cndmask_b32_e64 v105, v105, v171, s[46:47]
	v_cndmask_b32_e64 v104, v104, v171, s[44:45]
	v_cndmask_b32_e64 v103, v103, v171, s[42:43]
	v_cndmask_b32_e64 v102, v102, v171, s[40:41]
	v_cndmask_b32_e64 v101, v101, v171, s[38:39]
	v_cndmask_b32_e64 v100, v100, v171, s[36:37]
	v_cndmask_b32_e64 v99, v99, v171, s[34:35]
	v_cndmask_b32_e64 v97, v97, v171, s[30:31]
	v_cndmask_b32_e64 v96, v96, v171, s[28:29]
	v_cndmask_b32_e64 v95, v95, v171, s[26:27]
	v_cndmask_b32_e64 v94, v94, v171, s[24:25]
	v_cndmask_b32_e64 v93, v93, v171, s[22:23]
	v_cndmask_b32_e64 v92, v92, v171, s[20:21]
	v_cndmask_b32_e64 v91, v91, v171, s[18:19]
	v_cndmask_b32_e64 v90, v90, v171, s[16:17]
	v_cndmask_b32_e64 v89, v89, v171, s[14:15]
	v_cndmask_b32_e64 v88, v88, v171, s[12:13]
	v_cndmask_b32_e64 v87, v87, v171, s[10:11]
	v_cndmask_b32_e64 v86, v86, v171, s[8:9]
	v_cndmask_b32_e64 v85, v85, v171, s[6:7]
	v_cndmask_b32_e64 v84, v84, v171, s[4:5]
	v_cndmask_b32_e64 v83, v83, v171, s[2:3]
	v_cndmask_b32_e32 v82, v82, v171, vcc

.LBB0_401:
	v_cndmask_b32_e64 v7, v5, v188, s[4:5]
	v_cndmask_b32_e64 v5, v174, v7, s[2:3]
	v_sub_f32_e32 v8, v98, v5
	v_sub_f32_e32 v9, v99, v5
	v_sub_f32_e32 v10, v100, v5
	v_sub_f32_e32 v11, v101, v5
	v_sub_f32_e32 v12, v102, v5
	v_sub_f32_e32 v13, v103, v5
	v_sub_f32_e32 v14, v104, v5
	v_sub_f32_e32 v15, v105, v5
	v_sub_f32_e32 v16, v106, v5
	v_sub_f32_e32 v17, v107, v5
	v_sub_f32_e32 v98, v108, v5
	v_sub_f32_e32 v99, v109, v5
	v_sub_f32_e32 v100, v110, v5
	v_sub_f32_e32 v101, v111, v5
	v_sub_f32_e32 v102, v112, v5
	v_sub_f32_e32 v103, v113, v5
	v_sub_f32_e32 v188, v82, v5
	v_sub_f32_e32 v195, v83, v5
	v_sub_f32_e32 v208, v84, v5
	v_sub_f32_e32 v209, v85, v5
	v_sub_f32_e32 v210, v86, v5
	v_sub_f32_e32 v211, v87, v5
	v_sub_f32_e32 v212, v88, v5
	v_sub_f32_e32 v213, v89, v5
	v_sub_f32_e32 v214, v90, v5
	v_sub_f32_e32 v215, v91, v5
	v_sub_f32_e32 v216, v92, v5
	v_sub_f32_e32 v217, v93, v5
	v_sub_f32_e32 v218, v94, v5
	v_exp_f32_e32 v219, v8
	v_exp_f32_e32 v220, v9
	v_exp_f32_e32 v221, v10
	v_exp_f32_e32 v222, v11
	v_exp_f32_e32 v223, v12
	v_exp_f32_e32 v224, v13
	v_exp_f32_e32 v225, v14
	v_exp_f32_e32 v226, v15
	v_exp_f32_e32 v227, v16
	v_exp_f32_e32 v228, v17
	v_exp_f32_e32 v229, v98
	v_exp_f32_e32 v230, v99
	v_exp_f32_e32 v231, v100
	v_exp_f32_e32 v232, v101
	v_exp_f32_e32 v233, v102
	v_exp_f32_e32 v234, v103
	v_sub_f32_e32 v235, v95, v5
	v_sub_f32_e32 v236, v96, v5
	v_sub_f32_e32 v5, v97, v5
	ds_read_b128 v[8:11], v183 offset:49152
	ds_read_b128 v[12:15], v183 offset:57344
	ds_read_b128 v[148:151], v184 offset:49152
	ds_read_b128 v[152:155], v184 offset:57344
	ds_read_b128 v[156:159], v185 offset:49152
	ds_read_b128 v[160:163], v185 offset:57344
	ds_read_b128 v[196:199], v186 offset:49152
	ds_read_b128 v[200:203], v186 offset:57344
	s_waitcnt lgkmcnt(7)
	v_mfma_f32_32x32x16_bf16 v[98:113], v[8:11], v[142:145], 0
	ds_read_b128 v[8:11], v183 offset:49280
	ds_read_b128 v[204:207], v183 offset:57472
	s_waitcnt lgkmcnt(8)
	v_mfma_f32_32x32x16_bf16 v[82:97], v[12:15], v[142:145], 0
	s_waitcnt lgkmcnt(7)
	v_mfma_f32_32x32x16_bf16 v[98:113], v[148:151], v[138:141], v[98:113]
	ds_read_b128 v[12:15], v184 offset:49280
	ds_read_b128 v[148:151], v184 offset:57472
	s_waitcnt lgkmcnt(8)
	v_mfma_f32_32x32x16_bf16 v[82:97], v[152:155], v[138:141], v[82:97]
	s_waitcnt lgkmcnt(7)
	v_mfma_f32_32x32x16_bf16 v[98:113], v[156:159], v[134:137], v[98:113]
	ds_read_b128 v[152:155], v185 offset:49280
	ds_read_b128 v[156:159], v185 offset:57472
	s_waitcnt lgkmcnt(8)
	v_mfma_f32_32x32x16_bf16 v[82:97], v[160:163], v[134:137], v[82:97]
	s_waitcnt lgkmcnt(7)
	v_mfma_f32_32x32x16_bf16 v[98:113], v[196:199], v[130:133], v[98:113]
	ds_read_b128 v[160:163], v186 offset:49280
	ds_read_b128 v[196:199], v186 offset:57472
	s_waitcnt lgkmcnt(8)
	v_mfma_f32_32x32x16_bf16 v[82:97], v[200:203], v[130:133], v[82:97]
	s_waitcnt lgkmcnt(7)
	v_mfma_f32_32x32x16_bf16 v[98:113], v[8:11], v[126:129], v[98:113]
	s_waitcnt lgkmcnt(6)
	v_mfma_f32_32x32x16_bf16 v[82:97], v[204:207], v[126:129], v[82:97]
	s_waitcnt lgkmcnt(5)
	v_mfma_f32_32x32x16_bf16 v[98:113], v[12:15], v[122:125], v[98:113]
	s_waitcnt lgkmcnt(4)
	v_mfma_f32_32x32x16_bf16 v[82:97], v[148:151], v[122:125], v[82:97]
	s_waitcnt lgkmcnt(3)
	v_mfma_f32_32x32x16_bf16 v[98:113], v[152:155], v[118:121], v[98:113]
	s_waitcnt lgkmcnt(2)
	v_mfma_f32_32x32x16_bf16 v[82:97], v[156:159], v[118:121], v[82:97]
	s_waitcnt lgkmcnt(1)
	v_mfma_f32_32x32x16_bf16 v[98:113], v[160:163], v[114:117], v[98:113]
	s_waitcnt lgkmcnt(0)
	v_mfma_f32_32x32x16_bf16 v[82:97], v[196:199], v[114:117], v[82:97]
	v_exp_f32_e32 v188, v188
	v_exp_f32_e32 v195, v195
	v_exp_f32_e32 v203, v214
	v_exp_f32_e32 v204, v215
	v_exp_f32_e32 v197, v208
	v_exp_f32_e32 v205, v216
	v_exp_f32_e32 v198, v209
	v_exp_f32_e32 v206, v217
	v_exp_f32_e32 v199, v210
	v_exp_f32_e32 v207, v218
	v_exp_f32_e32 v200, v211
	v_exp_f32_e32 v208, v235
	v_add_f32_e32 v8, v219, v220
	v_add_f32_e32 v9, v227, v228
	v_add_f32_e32 v156, v188, v195
	v_add_f32_e32 v157, v203, v204
	v_add_u32_e32 v237, s75, v181
	ds_read_b64_tr_b16 v[10:11], v237 offset:0
	v_exp_f32_e32 v201, v212
	v_exp_f32_e32 v209, v236
	v_add_f32_e32 v8, v221, v8
	v_add_f32_e32 v9, v229, v9
	v_add_f32_e32 v156, v197, v156
	v_add_f32_e32 v157, v205, v157
	ds_read_b64_tr_b16 v[12:13], v237 offset:0x800
	v_exp_f32_e32 v202, v213
	v_exp_f32_e32 v5, v5
	v_add_f32_e32 v8, v222, v8
	v_add_f32_e32 v9, v230, v9
	v_add_f32_e32 v156, v198, v156
	v_add_f32_e32 v157, v206, v157
	ds_read_b64_tr_b16 v[14:15], v237 offset:0x1000
	v_add_f32_e32 v8, v223, v8
	v_add_f32_e32 v9, v231, v9
	v_add_f32_e32 v156, v199, v156
	v_add_f32_e32 v157, v207, v157
	ds_read_b64_tr_b16 v[16:17], v237 offset:0x1800
	v_add_f32_e32 v8, v224, v8
	v_add_f32_e32 v9, v232, v9
	v_add_f32_e32 v156, v200, v156
	v_add_f32_e32 v157, v208, v157
	ds_read_b64_tr_b16 v[148:149], v237 offset:0x2000
	v_add_f32_e32 v8, v225, v8
	v_add_f32_e32 v9, v233, v9
	v_add_f32_e32 v156, v201, v156
	v_add_f32_e32 v157, v209, v157
	ds_read_b64_tr_b16 v[150:151], v237 offset:0x2800
	v_add_f32_e32 v8, v226, v8
	v_add_f32_e32 v9, v234, v9
	v_add_f32_e32 v156, v202, v156
	v_add_f32_e32 v157, v5, v157
	ds_read_b64_tr_b16 v[152:153], v237 offset:0x3000
	v_add_f32_e32 v8, v9, v8
	v_add_f32_e32 v9, v157, v156
	ds_read_b64_tr_b16 v[154:155], v237 offset:0x3800
	v_add_f32_e32 v8, v9, v8
	v_mov_b32_e32 v9, v8
	s_nop 1
	v_permlane32_swap_b32_e32 v8, v9
	v_cvt_pk_bf16_f32 v156, v219, v220
	v_cvt_pk_bf16_f32 v157, v221, v222
	v_cvt_pk_bf16_f32 v158, v223, v224
	v_cvt_pk_bf16_f32 v159, v225, v226
	v_cvt_pk_bf16_f32 v160, v227, v228
	v_cvt_pk_bf16_f32 v161, v229, v230
	v_cvt_pk_bf16_f32 v162, v231, v232
	v_cvt_pk_bf16_f32 v163, v233, v234
	v_cvt_pk_bf16_f32 v196, v188, v195
	v_cvt_pk_bf16_f32 v197, v197, v198
	v_cvt_pk_bf16_f32 v198, v199, v200
	v_cvt_pk_bf16_f32 v199, v201, v202
	v_cvt_pk_bf16_f32 v200, v203, v204
	v_cvt_pk_bf16_f32 v201, v205, v206
	v_cvt_pk_bf16_f32 v202, v207, v208
	v_cvt_pk_bf16_f32 v203, v209, v5
	ds_read_b64_tr_b16 v[204:205], v237 offset:0x200
	ds_read_b64_tr_b16 v[206:207], v237 offset:0xa00
	ds_read_b64_tr_b16 v[208:209], v237 offset:0x1200
	ds_read_b64_tr_b16 v[210:211], v237 offset:0x1a00
	ds_read_b64_tr_b16 v[212:213], v237 offset:0x2200
	ds_read_b64_tr_b16 v[214:215], v237 offset:0x2a00
	ds_read_b64_tr_b16 v[216:217], v237 offset:0x3200
	ds_read_b64_tr_b16 v[218:219], v237 offset:0x3a00
	s_waitcnt lgkmcnt(8)
	v_mfma_f32_32x32x16_bf16 v[66:81], v[156:159], v[10:13], v[66:81]
	v_mfma_f32_32x32x16_bf16 v[66:81], v[160:163], v[14:17], v[66:81]
	v_mfma_f32_32x32x16_bf16 v[66:81], v[196:199], v[148:151], v[66:81]
	v_mfma_f32_32x32x16_bf16 v[66:81], v[200:203], v[152:155], v[66:81]
	ds_read_b64_tr_b16 v[10:11], v237 offset:0x400
	ds_read_b64_tr_b16 v[12:13], v237 offset:0xc00
	ds_read_b64_tr_b16 v[14:15], v237 offset:0x1400
	ds_read_b64_tr_b16 v[16:17], v237 offset:0x1c00
	ds_read_b64_tr_b16 v[148:149], v237 offset:0x2400
	ds_read_b64_tr_b16 v[150:151], v237 offset:0x2c00
	ds_read_b64_tr_b16 v[152:153], v237 offset:0x3400
	ds_read_b64_tr_b16 v[154:155], v237 offset:0x3c00
	s_waitcnt lgkmcnt(8)
	v_mfma_f32_32x32x16_bf16 v[50:65], v[200:203], v[216:219], v[50:65]
	v_mfma_f32_32x32x16_bf16 v[50:65], v[196:199], v[212:215], v[50:65]
	v_mfma_f32_32x32x16_bf16 v[50:65], v[160:163], v[208:211], v[50:65]
	v_mfma_f32_32x32x16_bf16 v[50:65], v[156:159], v[204:207], v[50:65]
	ds_read_b64_tr_b16 v[204:205], v237 offset:0x600
	ds_read_b64_tr_b16 v[206:207], v237 offset:0xe00
	ds_read_b64_tr_b16 v[208:209], v237 offset:0x1600
	ds_read_b64_tr_b16 v[210:211], v237 offset:0x1e00
	ds_read_b64_tr_b16 v[212:213], v237 offset:0x2600
	ds_read_b64_tr_b16 v[214:215], v237 offset:0x2e00
	ds_read_b64_tr_b16 v[216:217], v237 offset:0x3600
	ds_read_b64_tr_b16 v[218:219], v237 offset:0x3e00
	s_waitcnt lgkmcnt(8)
	v_mfma_f32_32x32x16_bf16 v[34:49], v[156:159], v[10:13], v[34:49]
	v_mfma_f32_32x32x16_bf16 v[34:49], v[160:163], v[14:17], v[34:49]
	v_mfma_f32_32x32x16_bf16 v[34:49], v[196:199], v[148:151], v[34:49]
	v_mfma_f32_32x32x16_bf16 v[34:49], v[200:203], v[152:155], v[34:49]
	s_waitcnt lgkmcnt(0)
	v_mfma_f32_32x32x16_bf16 v[18:33], v[156:159], v[204:207], v[18:33]
	s_cmp_le_i32 s87, s70
	v_mfma_f32_32x32x16_bf16 v[18:33], v[160:163], v[208:211], v[18:33]
	v_mfma_f32_32x32x16_bf16 v[18:33], v[196:199], v[212:215], v[18:33]
	v_mfma_f32_32x32x16_bf16 v[18:33], v[200:203], v[216:219], v[18:33]
	s_cbranch_scc1 .LBB0_403
	v_cmp_gt_i32_e64 s[60:61], 26, v193
	v_cmp_gt_i32_e64 s[62:63], 27, v193
	v_cmp_gt_i32_e64 s[58:59], 25, v193
	s_and_b64 s[60:61], s[62:63], s[60:61]
	v_cmp_gt_i32_e64 s[56:57], 24, v193
	s_and_b64 s[58:59], s[60:61], s[58:59]
	v_cmp_gt_i32_e64 s[54:55], 19, v193
	s_and_b64 s[56:57], s[58:59], s[56:57]
	v_cmp_gt_i32_e64 s[52:53], 18, v193
	s_and_b64 s[54:55], s[56:57], s[54:55]
	v_cmp_gt_i32_e64 s[50:51], 17, v193
	s_and_b64 s[52:53], s[54:55], s[52:53]
	v_cmp_gt_i32_e64 s[48:49], 16, v193
	s_and_b64 s[50:51], s[52:53], s[50:51]
	v_cmp_gt_i32_e64 s[46:47], 11, v193
	s_and_b64 s[48:49], s[50:51], s[48:49]
	v_cmp_gt_i32_e64 s[44:45], 10, v193
	s_and_b64 s[46:47], s[48:49], s[46:47]
	v_cmp_gt_i32_e64 s[42:43], 9, v193
	s_and_b64 s[44:45], s[46:47], s[44:45]
	v_cmp_gt_i32_e64 s[40:41], 8, v193
	s_and_b64 s[42:43], s[44:45], s[42:43]
	v_cmp_gt_i32_e64 s[38:39], 3, v193
	s_and_b64 s[40:41], s[42:43], s[40:41]
	v_cmp_gt_i32_e64 s[36:37], 2, v193
	s_and_b64 s[38:39], s[40:41], s[38:39]
	v_cmp_gt_i32_e64 s[34:35], 1, v193
	s_and_b64 s[36:37], s[38:39], s[36:37]
	v_cmp_gt_i32_e64 s[30:31], 0, v193
	s_and_b64 s[34:35], s[36:37], s[34:35]
	s_and_b64 s[30:31], s[34:35], s[30:31]
	v_cmp_gt_i32_e64 s[28:29], 58, v193
	v_cndmask_b32_e64 v98, v98, v171, s[30:31]
	v_cmp_gt_i32_e64 s[30:31], 59, v193
	v_cmp_gt_i32_e64 s[26:27], 57, v193
	s_and_b64 s[28:29], s[30:31], s[28:29]
	v_cmp_gt_i32_e64 s[24:25], 56, v193
	s_and_b64 s[26:27], s[28:29], s[26:27]
	v_cmp_gt_i32_e64 s[22:23], 51, v193
	s_and_b64 s[24:25], s[26:27], s[24:25]
	v_cmp_gt_i32_e64 s[20:21], 50, v193
	s_and_b64 s[22:23], s[24:25], s[22:23]
	v_cmp_gt_i32_e64 s[18:19], 49, v193
	s_and_b64 s[20:21], s[22:23], s[20:21]
	v_cmp_gt_i32_e64 s[16:17], 48, v193
	s_and_b64 s[18:19], s[20:21], s[18:19]
	v_cmp_gt_i32_e64 s[14:15], 43, v193
	s_and_b64 s[16:17], s[18:19], s[16:17]
	v_cmp_gt_i32_e64 s[12:13], 42, v193
	s_and_b64 s[14:15], s[16:17], s[14:15]
	v_cmp_gt_i32_e64 s[10:11], 41, v193
	s_and_b64 s[12:13], s[14:15], s[12:13]
	v_cmp_gt_i32_e64 s[8:9], 40, v193
	s_and_b64 s[10:11], s[12:13], s[10:11]
	v_cmp_gt_i32_e64 s[6:7], 35, v193
	s_and_b64 s[8:9], s[10:11], s[8:9]
	v_cmp_gt_i32_e64 s[4:5], 34, v193
	s_and_b64 s[6:7], s[8:9], s[6:7]
	v_cmp_gt_i32_e64 s[2:3], 33, v193
	s_and_b64 s[4:5], s[6:7], s[4:5]
	v_cmp_gt_i32_e32 vcc, 32, v193
	s_and_b64 s[2:3], s[4:5], s[2:3]
	s_and_b64 vcc, s[2:3], vcc
	v_cndmask_b32_e64 v113, v113, v171, s[62:63]
	v_cndmask_b32_e64 v112, v112, v171, s[60:61]
	v_cndmask_b32_e64 v111, v111, v171, s[58:59]
	v_cndmask_b32_e64 v110, v110, v171, s[56:57]
	v_cndmask_b32_e64 v109, v109, v171, s[54:55]
	v_cndmask_b32_e64 v108, v108, v171, s[52:53]
	v_cndmask_b32_e64 v107, v107, v171, s[50:51]
	v_cndmask_b32_e64 v106, v106, v171, s[48:49]
	v_cndmask_b32_e64 v105, v105, v171, s[46:47]
	v_cndmask_b32_e64 v104, v104, v171, s[44:45]
	v_cndmask_b32_e64 v103, v103, v171, s[42:43]
	v_cndmask_b32_e64 v102, v102, v171, s[40:41]
	v_cndmask_b32_e64 v101, v101, v171, s[38:39]
	v_cndmask_b32_e64 v100, v100, v171, s[36:37]
	v_cndmask_b32_e64 v99, v99, v171, s[34:35]
	v_cndmask_b32_e64 v97, v97, v171, s[30:31]
	v_cndmask_b32_e64 v96, v96, v171, s[28:29]
	v_cndmask_b32_e64 v95, v95, v171, s[26:27]
	v_cndmask_b32_e64 v94, v94, v171, s[24:25]
	v_cndmask_b32_e64 v93, v93, v171, s[22:23]
	v_cndmask_b32_e64 v92, v92, v171, s[20:21]
	v_cndmask_b32_e64 v91, v91, v171, s[18:19]
	v_cndmask_b32_e64 v90, v90, v171, s[16:17]
	v_cndmask_b32_e64 v89, v89, v171, s[14:15]
	v_cndmask_b32_e64 v88, v88, v171, s[12:13]
	v_cndmask_b32_e64 v87, v87, v171, s[10:11]
	v_cndmask_b32_e64 v86, v86, v171, s[8:9]
	v_cndmask_b32_e64 v85, v85, v171, s[6:7]
	v_cndmask_b32_e64 v84, v84, v171, s[4:5]
	v_cndmask_b32_e64 v83, v83, v171, s[2:3]
	v_cndmask_b32_e32 v82, v82, v171, vcc

.LBB0_411:
	s_add_i32 s72, s83, 1
	s_cmp_lt_u32 s72, s68
	s_cselect_b32 s2, s72, s83
	s_lshl_b32 s2, s2, 2
	s_lshr_b32 s2, s33, s2
	s_lshl_b32 s2, s2, 8
	s_and_b32 s2, s2, 0xf00
	ds_read_b128 v[6:9], v192
	ds_read_b128 v[10:13], v192 offset:8192
	ds_read_b128 v[14:17], v191
	ds_read_b128 v[182:185], v191 offset:8192
	ds_read_b128 v[212:215], v190
	ds_read_b128 v[216:219], v190 offset:8192
	ds_read_b128 v[220:223], v189
	ds_read_b128 v[224:227], v189 offset:8192
	s_waitcnt lgkmcnt(7)
	v_mfma_f32_32x32x16_bf16 v[98:113], v[6:9], v[142:145], 0
	ds_read_b128 v[6:9], v192 offset:128
	ds_read_b128 v[228:231], v192 offset:8320
	s_waitcnt lgkmcnt(8)
	v_mfma_f32_32x32x16_bf16 v[82:97], v[10:13], v[142:145], 0
	s_waitcnt lgkmcnt(7)
	v_mfma_f32_32x32x16_bf16 v[98:113], v[14:17], v[138:141], v[98:113]
	ds_read_b128 v[10:13], v191 offset:128
	ds_read_b128 v[14:17], v191 offset:8320
	s_waitcnt lgkmcnt(8)
	v_mfma_f32_32x32x16_bf16 v[82:97], v[182:185], v[138:141], v[82:97]
	s_waitcnt lgkmcnt(7)
	v_mfma_f32_32x32x16_bf16 v[98:113], v[212:215], v[134:137], v[98:113]
	ds_read_b128 v[138:141], v190 offset:128
	ds_read_b128 v[142:145], v190 offset:8320
	s_waitcnt lgkmcnt(8)
	v_mfma_f32_32x32x16_bf16 v[82:97], v[216:219], v[134:137], v[82:97]
	s_waitcnt lgkmcnt(7)
	v_mfma_f32_32x32x16_bf16 v[98:113], v[220:223], v[130:133], v[98:113]
	ds_read_b128 v[134:137], v189 offset:128
	ds_read_b128 v[182:185], v189 offset:8320
	s_waitcnt lgkmcnt(8)
	v_mfma_f32_32x32x16_bf16 v[82:97], v[224:227], v[130:133], v[82:97]
	s_waitcnt lgkmcnt(7)
	v_mfma_f32_32x32x16_bf16 v[98:113], v[6:9], v[126:129], v[98:113]
	s_waitcnt lgkmcnt(6)
	v_mfma_f32_32x32x16_bf16 v[82:97], v[228:231], v[126:129], v[82:97]
	s_waitcnt lgkmcnt(5)
	v_mfma_f32_32x32x16_bf16 v[98:113], v[10:13], v[122:125], v[98:113]
	s_waitcnt lgkmcnt(4)
	v_mfma_f32_32x32x16_bf16 v[82:97], v[14:17], v[122:125], v[82:97]
	s_waitcnt lgkmcnt(3)
	v_mfma_f32_32x32x16_bf16 v[98:113], v[138:141], v[118:121], v[98:113]
	s_waitcnt lgkmcnt(2)
	v_mfma_f32_32x32x16_bf16 v[82:97], v[142:145], v[118:121], v[82:97]
	s_waitcnt lgkmcnt(1)
	v_mfma_f32_32x32x16_bf16 v[98:113], v[134:137], v[114:117], v[98:113]
	s_waitcnt lgkmcnt(0)
	v_mfma_f32_32x32x16_bf16 v[82:97], v[182:185], v[114:117], v[82:97]
	v_or_b32_e32 v2, s2, v147
	v_add_u32_e32 v6, s94, v2
	v_ashrrev_i32_e32 v7, 31, v6
	v_lshlrev_b64 v[6:7], 8, v[6:7]
	v_lshl_add_u64 v[6:7], s[80:81], 0, v[6:7]
	v_mov_b32_e32 v147, v3
	v_lshl_add_u64 v[6:7], v[6:7], 0, v[146:147]
	global_load_dwordx4 v[142:145], v[6:7], off
	global_load_dwordx4 v[138:141], v[6:7], off offset:32
	global_load_dwordx4 v[134:137], v[6:7], off offset:64
	global_load_dwordx4 v[130:133], v[6:7], off offset:96
	global_load_dwordx4 v[126:129], v[6:7], off offset:128
	global_load_dwordx4 v[122:125], v[6:7], off offset:160
	global_load_dwordx4 v[118:121], v[6:7], off offset:192
	global_load_dwordx4 v[114:117], v[6:7], off offset:224
	v_exp_f32_e32 v187, v148
	v_exp_f32_e32 v189, v149
	v_exp_f32_e32 v212, v156
	v_exp_f32_e32 v213, v157
	v_exp_f32_e32 v190, v150
	v_exp_f32_e32 v214, v158
	v_exp_f32_e32 v191, v151
	v_exp_f32_e32 v159, v159
	v_exp_f32_e32 v192, v152
	v_exp_f32_e32 v160, v160
	v_exp_f32_e32 v193, v153
	v_exp_f32_e32 v161, v161
	v_add_f32_e32 v2, v195, v196
	v_add_f32_e32 v4, v200, v202
	v_add_f32_e32 v146, v187, v189
	v_add_f32_e32 v147, v212, v213
	v_add_u32_e32 v186, s86, v181
	ds_read_b64_tr_b16 v[6:7], v186 offset:0
	v_exp_f32_e32 v194, v154
	v_exp_f32_e32 v162, v162
	v_add_f32_e32 v2, v197, v2
	v_add_f32_e32 v4, v204, v4
	v_add_f32_e32 v146, v190, v146
	v_add_f32_e32 v147, v214, v147
	ds_read_b64_tr_b16 v[8:9], v186 offset:0x800
	v_exp_f32_e32 v211, v155
	v_exp_f32_e32 v163, v163
	v_add_f32_e32 v2, v198, v2
	v_add_f32_e32 v4, v206, v4
	v_add_f32_e32 v146, v191, v146
	v_add_f32_e32 v147, v159, v147
	ds_read_b64_tr_b16 v[10:11], v186 offset:0x1000
	v_add_f32_e32 v2, v199, v2
	v_add_f32_e32 v4, v207, v4
	v_add_f32_e32 v146, v192, v146
	v_add_f32_e32 v147, v160, v147
	ds_read_b64_tr_b16 v[12:13], v186 offset:0x1800
	v_add_f32_e32 v2, v201, v2
	v_add_f32_e32 v4, v208, v4
	v_add_f32_e32 v146, v193, v146
	v_add_f32_e32 v147, v161, v147
	ds_read_b64_tr_b16 v[14:15], v186 offset:0x2000
	v_add_f32_e32 v2, v203, v2
	v_add_f32_e32 v4, v209, v4
	v_add_f32_e32 v146, v194, v146
	v_add_f32_e32 v147, v162, v147
	ds_read_b64_tr_b16 v[16:17], v186 offset:0x2800
	v_add_f32_e32 v2, v205, v2
	v_add_f32_e32 v4, v210, v4
	v_add_f32_e32 v146, v211, v146
	v_add_f32_e32 v147, v163, v147
	ds_read_b64_tr_b16 v[182:183], v186 offset:0x3000
	v_add_f32_e32 v2, v4, v2
	v_add_f32_e32 v4, v147, v146
	ds_read_b64_tr_b16 v[184:185], v186 offset:0x3800
	v_add_f32_e32 v2, v4, v2
	v_mov_b32_e32 v4, v2
	s_nop 1
	v_permlane32_swap_b32_e32 v2, v4
	v_cvt_pk_bf16_f32 v146, v195, v196
	v_cvt_pk_bf16_f32 v147, v197, v198
	v_cvt_pk_bf16_f32 v148, v199, v201
	v_cvt_pk_bf16_f32 v149, v203, v205
	v_cvt_pk_bf16_f32 v150, v200, v202
	v_cvt_pk_bf16_f32 v151, v204, v206
	v_cvt_pk_bf16_f32 v152, v207, v208
	v_cvt_pk_bf16_f32 v153, v209, v210
	v_cvt_pk_bf16_f32 v154, v187, v189
	v_cvt_pk_bf16_f32 v155, v190, v191
	v_cvt_pk_bf16_f32 v156, v192, v193
	v_cvt_pk_bf16_f32 v157, v194, v211
	v_cvt_pk_bf16_f32 v158, v212, v213
	v_cvt_pk_bf16_f32 v159, v214, v159
	v_cvt_pk_bf16_f32 v160, v160, v161
	v_cvt_pk_bf16_f32 v161, v162, v163
	ds_read_b64_tr_b16 v[190:191], v186 offset:0x200
	ds_read_b64_tr_b16 v[192:193], v186 offset:0xa00
	ds_read_b64_tr_b16 v[194:195], v186 offset:0x1200
	ds_read_b64_tr_b16 v[196:197], v186 offset:0x1a00
	ds_read_b64_tr_b16 v[198:199], v186 offset:0x2200
	ds_read_b64_tr_b16 v[200:201], v186 offset:0x2a00
	ds_read_b64_tr_b16 v[202:203], v186 offset:0x3200
	ds_read_b64_tr_b16 v[204:205], v186 offset:0x3a00
	s_waitcnt lgkmcnt(8)
	v_mfma_f32_32x32x16_bf16 v[66:81], v[146:149], v[6:9], v[66:81]
	v_mfma_f32_32x32x16_bf16 v[66:81], v[150:153], v[10:13], v[66:81]
	v_mfma_f32_32x32x16_bf16 v[66:81], v[154:157], v[14:17], v[66:81]
	v_mfma_f32_32x32x16_bf16 v[66:81], v[158:161], v[182:185], v[66:81]
	ds_read_b64_tr_b16 v[6:7], v186 offset:0x400
	ds_read_b64_tr_b16 v[8:9], v186 offset:0xc00
	ds_read_b64_tr_b16 v[10:11], v186 offset:0x1400
	ds_read_b64_tr_b16 v[12:13], v186 offset:0x1c00
	ds_read_b64_tr_b16 v[14:15], v186 offset:0x2400
	ds_read_b64_tr_b16 v[16:17], v186 offset:0x2c00
	ds_read_b64_tr_b16 v[182:183], v186 offset:0x3400
	ds_read_b64_tr_b16 v[184:185], v186 offset:0x3c00
	s_waitcnt lgkmcnt(8)
	v_mfma_f32_32x32x16_bf16 v[50:65], v[158:161], v[202:205], v[50:65]
	v_mfma_f32_32x32x16_bf16 v[50:65], v[154:157], v[198:201], v[50:65]
	v_mfma_f32_32x32x16_bf16 v[50:65], v[150:153], v[194:197], v[50:65]
	v_mfma_f32_32x32x16_bf16 v[50:65], v[146:149], v[190:193], v[50:65]
	ds_read_b64_tr_b16 v[190:191], v186 offset:0x600
	ds_read_b64_tr_b16 v[192:193], v186 offset:0xe00
	ds_read_b64_tr_b16 v[194:195], v186 offset:0x1600
	ds_read_b64_tr_b16 v[196:197], v186 offset:0x1e00
	ds_read_b64_tr_b16 v[198:199], v186 offset:0x2600
	ds_read_b64_tr_b16 v[200:201], v186 offset:0x2e00
	ds_read_b64_tr_b16 v[202:203], v186 offset:0x3600
	ds_read_b64_tr_b16 v[204:205], v186 offset:0x3e00
	s_waitcnt lgkmcnt(8)
	v_mfma_f32_32x32x16_bf16 v[34:49], v[146:149], v[6:9], v[34:49]
	v_mfma_f32_32x32x16_bf16 v[34:49], v[150:153], v[10:13], v[34:49]
	v_mfma_f32_32x32x16_bf16 v[34:49], v[154:157], v[14:17], v[34:49]
	v_mfma_f32_32x32x16_bf16 v[34:49], v[158:161], v[182:185], v[34:49]
	s_waitcnt lgkmcnt(0)
	v_mfma_f32_32x32x16_bf16 v[18:33], v[146:149], v[190:193], v[18:33]
	s_cmp_gt_i32 s82, 7
	v_mfma_f32_32x32x16_bf16 v[18:33], v[150:153], v[194:197], v[18:33]
	v_mfma_f32_32x32x16_bf16 v[18:33], v[154:157], v[198:201], v[18:33]
	v_mfma_f32_32x32x16_bf16 v[18:33], v[158:161], v[202:205], v[18:33]
	s_cbranch_scc1 .LBB0_413
	s_or_b32 s2, s93, 0xc0
	v_subrev_u32_e32 v6, s2, v180
	v_cmp_gt_i32_e64 s[60:61], 26, v6
	v_cmp_gt_i32_e64 s[62:63], 27, v6
	v_cmp_gt_i32_e64 s[58:59], 25, v6
	s_and_b64 s[60:61], s[62:63], s[60:61]
	v_cmp_gt_i32_e64 s[56:57], 24, v6
	s_and_b64 s[58:59], s[60:61], s[58:59]
	v_cmp_gt_i32_e64 s[54:55], 19, v6
	s_and_b64 s[56:57], s[58:59], s[56:57]
	v_cmp_gt_i32_e64 s[52:53], 18, v6
	s_and_b64 s[54:55], s[56:57], s[54:55]
	v_cmp_gt_i32_e64 s[50:51], 17, v6
	s_and_b64 s[52:53], s[54:55], s[52:53]
	v_cmp_gt_i32_e64 s[48:49], 16, v6
	s_and_b64 s[50:51], s[52:53], s[50:51]
	v_cmp_gt_i32_e64 s[46:47], 11, v6
	s_and_b64 s[48:49], s[50:51], s[48:49]
	v_cmp_gt_i32_e64 s[44:45], 10, v6
	s_and_b64 s[46:47], s[48:49], s[46:47]
	v_cmp_gt_i32_e64 s[42:43], 9, v6
	s_and_b64 s[44:45], s[46:47], s[44:45]
	v_cmp_gt_i32_e64 s[40:41], 8, v6
	s_and_b64 s[42:43], s[44:45], s[42:43]
	v_cmp_gt_i32_e64 s[38:39], 3, v6
	s_and_b64 s[40:41], s[42:43], s[40:41]
	v_cmp_gt_i32_e64 s[36:37], 2, v6
	s_and_b64 s[38:39], s[40:41], s[38:39]
	v_cmp_gt_i32_e64 s[34:35], 1, v6
	s_and_b64 s[36:37], s[38:39], s[36:37]
	v_cmp_gt_i32_e64 s[30:31], 0, v6
	s_and_b64 s[34:35], s[36:37], s[34:35]
	s_and_b64 s[30:31], s[34:35], s[30:31]
	v_cmp_gt_i32_e64 s[28:29], 58, v6
	v_cndmask_b32_e64 v98, v98, v171, s[30:31]
	v_cmp_gt_i32_e64 s[30:31], 59, v6
	v_cmp_gt_i32_e64 s[26:27], 57, v6
	s_and_b64 s[28:29], s[30:31], s[28:29]
	v_cmp_gt_i32_e64 s[24:25], 56, v6
	s_and_b64 s[26:27], s[28:29], s[26:27]
	v_cmp_gt_i32_e64 s[22:23], 51, v6
	s_and_b64 s[24:25], s[26:27], s[24:25]
	v_cmp_gt_i32_e64 s[20:21], 50, v6
	s_and_b64 s[22:23], s[24:25], s[22:23]
	v_cmp_gt_i32_e64 s[18:19], 49, v6
	s_and_b64 s[20:21], s[22:23], s[20:21]
	v_cmp_gt_i32_e64 s[16:17], 48, v6
	s_and_b64 s[18:19], s[20:21], s[18:19]
	v_cmp_gt_i32_e64 s[14:15], 43, v6
	s_and_b64 s[16:17], s[18:19], s[16:17]
	v_cmp_gt_i32_e64 s[12:13], 42, v6
	s_and_b64 s[14:15], s[16:17], s[14:15]
	v_cmp_gt_i32_e64 s[10:11], 41, v6
	s_and_b64 s[12:13], s[14:15], s[12:13]
	v_cmp_gt_i32_e64 s[8:9], 40, v6
	s_and_b64 s[10:11], s[12:13], s[10:11]
	v_cmp_gt_i32_e64 s[6:7], 35, v6
	s_and_b64 s[8:9], s[10:11], s[8:9]
	v_cmp_gt_i32_e64 s[4:5], 34, v6
	s_and_b64 s[6:7], s[8:9], s[6:7]
	v_cmp_gt_i32_e64 s[2:3], 33, v6
	s_and_b64 s[4:5], s[6:7], s[4:5]
	v_cmp_gt_i32_e32 vcc, 32, v6
	s_and_b64 s[2:3], s[4:5], s[2:3]
	s_and_b64 vcc, s[2:3], vcc
	v_cndmask_b32_e64 v113, v113, v171, s[62:63]
	v_cndmask_b32_e64 v112, v112, v171, s[60:61]
	v_cndmask_b32_e64 v111, v111, v171, s[58:59]
	v_cndmask_b32_e64 v110, v110, v171, s[56:57]
	v_cndmask_b32_e64 v109, v109, v171, s[54:55]
	v_cndmask_b32_e64 v108, v108, v171, s[52:53]
	v_cndmask_b32_e64 v107, v107, v171, s[50:51]
	v_cndmask_b32_e64 v106, v106, v171, s[48:49]
	v_cndmask_b32_e64 v105, v105, v171, s[46:47]
	v_cndmask_b32_e64 v104, v104, v171, s[44:45]
	v_cndmask_b32_e64 v103, v103, v171, s[42:43]
	v_cndmask_b32_e64 v102, v102, v171, s[40:41]
	v_cndmask_b32_e64 v101, v101, v171, s[38:39]
	v_cndmask_b32_e64 v100, v100, v171, s[36:37]
	v_cndmask_b32_e64 v99, v99, v171, s[34:35]
	v_cndmask_b32_e64 v97, v97, v171, s[30:31]
	v_cndmask_b32_e64 v96, v96, v171, s[28:29]
	v_cndmask_b32_e64 v95, v95, v171, s[26:27]
	v_cndmask_b32_e64 v94, v94, v171, s[24:25]
	v_cndmask_b32_e64 v93, v93, v171, s[22:23]
	v_cndmask_b32_e64 v92, v92, v171, s[20:21]
	v_cndmask_b32_e64 v91, v91, v171, s[18:19]
	v_cndmask_b32_e64 v90, v90, v171, s[16:17]
	v_cndmask_b32_e64 v89, v89, v171, s[14:15]
	v_cndmask_b32_e64 v88, v88, v171, s[12:13]
	v_cndmask_b32_e64 v87, v87, v171, s[10:11]
	v_cndmask_b32_e64 v86, v86, v171, s[8:9]
	v_cndmask_b32_e64 v85, v85, v171, s[6:7]
	v_cndmask_b32_e64 v84, v84, v171, s[4:5]
	v_cndmask_b32_e64 v83, v83, v171, s[2:3]
	v_cndmask_b32_e32 v82, v82, v171, vcc

.LBB0_417:
	v_cndmask_b32_e64 v7, v7, v188, s[2:3]
	v_sub_f32_e32 v8, v98, v7
	v_sub_f32_e32 v13, v101, v7
	v_sub_f32_e32 v14, v102, v7
	v_sub_f32_e32 v101, v105, v7
	v_sub_f32_e32 v105, v108, v7
	v_sub_f32_e32 v10, v99, v7
	v_sub_f32_e32 v17, v103, v7
	v_sub_f32_e32 v98, v104, v7
	v_sub_f32_e32 v102, v106, v7
	v_sub_f32_e32 v104, v107, v7
	v_sub_f32_e32 v106, v109, v7
	v_sub_f32_e32 v107, v110, v7
	v_sub_f32_e32 v109, v112, v7
	v_sub_f32_e32 v110, v113, v7
	v_exp_f32_e32 v9, v8
	v_exp_f32_e32 v16, v14
	v_exp_f32_e32 v14, v105
	v_sub_f32_e32 v8, v82, v7
	v_sub_f32_e32 v105, v83, v7
	v_sub_f32_e32 v112, v90, v7
	v_sub_f32_e32 v113, v91, v7
	v_sub_f32_e32 v12, v100, v7
	v_exp_f32_e32 v11, v10
	v_exp_f32_e32 v15, v13
	v_exp_f32_e32 v99, v17
	v_exp_f32_e32 v10, v102
	v_exp_f32_e32 v13, v104
	v_exp_f32_e32 v17, v106
	v_sub_f32_e32 v106, v84, v7
	v_sub_f32_e32 v146, v92, v7
	v_exp_f32_e32 v151, v8
	v_exp_f32_e32 v105, v105
	v_exp_f32_e32 v112, v112
	v_exp_f32_e32 v113, v113
	v_sub_f32_e32 v108, v111, v7
	v_exp_f32_e32 v12, v12
	v_exp_f32_e32 v100, v98
	v_exp_f32_e32 v98, v107
	v_sub_f32_e32 v107, v85, v7
	v_sub_f32_e32 v147, v93, v7
	v_exp_f32_e32 v152, v106
	v_exp_f32_e32 v146, v146
	v_exp_f32_e32 v103, v101
	v_exp_f32_e32 v101, v108
	v_sub_f32_e32 v108, v86, v7
	v_sub_f32_e32 v148, v94, v7
	v_exp_f32_e32 v153, v107
	v_exp_f32_e32 v147, v147
	v_exp_f32_e32 v102, v109
	v_exp_f32_e32 v104, v110
	v_sub_f32_e32 v109, v87, v7
	v_sub_f32_e32 v110, v88, v7
	v_sub_f32_e32 v111, v89, v7
	v_sub_f32_e32 v149, v95, v7
	v_sub_f32_e32 v150, v96, v7
	v_sub_f32_e32 v7, v97, v7
	v_exp_f32_e32 v155, v108
	v_exp_f32_e32 v148, v148
	v_exp_f32_e32 v156, v109
	v_exp_f32_e32 v149, v149
	v_exp_f32_e32 v157, v7
	v_add_f32_e32 v7, v9, v11
	v_add_f32_e32 v8, v10, v13
	v_add_f32_e32 v106, v151, v105
	v_add_f32_e32 v107, v112, v113
	v_add_u32_e32 v154, s89, v181
	ds_read_b64_tr_b16 v[82:83], v154 offset:0
	v_exp_f32_e32 v110, v110
	v_exp_f32_e32 v150, v150
	v_add_f32_e32 v7, v12, v7
	v_add_f32_e32 v8, v14, v8
	v_add_f32_e32 v106, v152, v106
	v_add_f32_e32 v107, v146, v107
	ds_read_b64_tr_b16 v[84:85], v154 offset:0x800
	v_exp_f32_e32 v111, v111
	v_add_f32_e32 v7, v15, v7
	v_add_f32_e32 v8, v17, v8
	v_add_f32_e32 v106, v153, v106
	v_add_f32_e32 v107, v147, v107
	ds_read_b64_tr_b16 v[86:87], v154 offset:0x1000
	v_add_f32_e32 v7, v16, v7
	v_add_f32_e32 v8, v98, v8
	v_add_f32_e32 v106, v155, v106
	v_add_f32_e32 v107, v148, v107
	ds_read_b64_tr_b16 v[88:89], v154 offset:0x1800
	v_add_f32_e32 v7, v99, v7
	v_add_f32_e32 v8, v101, v8
	v_add_f32_e32 v106, v156, v106
	v_add_f32_e32 v107, v149, v107
	ds_read_b64_tr_b16 v[90:91], v154 offset:0x2000
	v_add_f32_e32 v7, v100, v7
	v_add_f32_e32 v8, v102, v8
	v_add_f32_e32 v106, v110, v106
	v_add_f32_e32 v107, v150, v107
	ds_read_b64_tr_b16 v[92:93], v154 offset:0x2800
	v_add_f32_e32 v7, v103, v7
	v_add_f32_e32 v8, v104, v8
	v_add_f32_e32 v106, v111, v106
	v_add_f32_e32 v107, v157, v107
	ds_read_b64_tr_b16 v[94:95], v154 offset:0x3000
	v_add_f32_e32 v7, v8, v7
	v_add_f32_e32 v8, v107, v106
	ds_read_b64_tr_b16 v[96:97], v154 offset:0x3800
	v_add_f32_e32 v7, v8, v7
	v_mov_b32_e32 v8, v7
	s_nop 1
	v_permlane32_swap_b32_e32 v7, v8
	v_cvt_pk_bf16_f32 v106, v9, v11
	v_cvt_pk_bf16_f32 v107, v12, v15
	v_cvt_pk_bf16_f32 v108, v16, v99
	v_cvt_pk_bf16_f32 v109, v100, v103
	v_cvt_pk_bf16_f32 v10, v10, v13
	v_cvt_pk_bf16_f32 v11, v14, v17
	v_cvt_pk_bf16_f32 v12, v98, v101
	v_cvt_pk_bf16_f32 v13, v102, v104
	v_cvt_pk_bf16_f32 v14, v151, v105
	v_cvt_pk_bf16_f32 v15, v152, v153
	v_cvt_pk_bf16_f32 v16, v155, v156
	v_cvt_pk_bf16_f32 v17, v110, v111
	v_cvt_pk_bf16_f32 v98, v112, v113
	v_cvt_pk_bf16_f32 v99, v146, v147
	v_cvt_pk_bf16_f32 v100, v148, v149
	v_cvt_pk_bf16_f32 v101, v150, v157
	ds_read_b64_tr_b16 v[102:103], v154 offset:0x200
	ds_read_b64_tr_b16 v[104:105], v154 offset:0xa00
	ds_read_b64_tr_b16 v[110:111], v154 offset:0x1200
	ds_read_b64_tr_b16 v[112:113], v154 offset:0x1a00
	ds_read_b64_tr_b16 v[146:147], v154 offset:0x2200
	ds_read_b64_tr_b16 v[148:149], v154 offset:0x2a00
	ds_read_b64_tr_b16 v[150:151], v154 offset:0x3200
	ds_read_b64_tr_b16 v[152:153], v154 offset:0x3a00
	s_waitcnt lgkmcnt(8)
	v_mfma_f32_32x32x16_bf16 v[66:81], v[106:109], v[82:85], v[66:81]
	v_mfma_f32_32x32x16_bf16 v[66:81], v[10:13], v[86:89], v[66:81]
	v_mfma_f32_32x32x16_bf16 v[66:81], v[14:17], v[90:93], v[66:81]
	v_mfma_f32_32x32x16_bf16 v[66:81], v[98:101], v[94:97], v[66:81]
	ds_read_b64_tr_b16 v[82:83], v154 offset:0x400
	ds_read_b64_tr_b16 v[84:85], v154 offset:0xc00
	ds_read_b64_tr_b16 v[86:87], v154 offset:0x1400
	ds_read_b64_tr_b16 v[88:89], v154 offset:0x1c00
	ds_read_b64_tr_b16 v[90:91], v154 offset:0x2400
	ds_read_b64_tr_b16 v[92:93], v154 offset:0x2c00
	ds_read_b64_tr_b16 v[94:95], v154 offset:0x3400
	ds_read_b64_tr_b16 v[96:97], v154 offset:0x3c00
	s_waitcnt lgkmcnt(8)
	v_mfma_f32_32x32x16_bf16 v[50:65], v[98:101], v[150:153], v[50:65]
	v_mfma_f32_32x32x16_bf16 v[50:65], v[14:17], v[146:149], v[50:65]
	v_mfma_f32_32x32x16_bf16 v[50:65], v[10:13], v[110:113], v[50:65]
	v_mfma_f32_32x32x16_bf16 v[50:65], v[106:109], v[102:105], v[50:65]
	ds_read_b64_tr_b16 v[102:103], v154 offset:0x600
	ds_read_b64_tr_b16 v[104:105], v154 offset:0xe00
	ds_read_b64_tr_b16 v[110:111], v154 offset:0x1600
	ds_read_b64_tr_b16 v[112:113], v154 offset:0x1e00
	ds_read_b64_tr_b16 v[146:147], v154 offset:0x2600
	ds_read_b64_tr_b16 v[148:149], v154 offset:0x2e00
	ds_read_b64_tr_b16 v[150:151], v154 offset:0x3600
	ds_read_b64_tr_b16 v[152:153], v154 offset:0x3e00
	s_waitcnt lgkmcnt(8)
	v_mfma_f32_32x32x16_bf16 v[34:49], v[106:109], v[82:85], v[34:49]
	v_mfma_f32_32x32x16_bf16 v[34:49], v[10:13], v[86:89], v[34:49]
	v_mfma_f32_32x32x16_bf16 v[34:49], v[14:17], v[90:93], v[34:49]
	v_mfma_f32_32x32x16_bf16 v[34:49], v[98:101], v[94:97], v[34:49]
	s_waitcnt lgkmcnt(0)
	v_mfma_f32_32x32x16_bf16 v[18:33], v[98:101], v[150:153], v[18:33]
	v_mfma_f32_32x32x16_bf16 v[18:33], v[14:17], v[146:149], v[18:33]
	v_mfma_f32_32x32x16_bf16 v[18:33], v[10:13], v[110:113], v[18:33]
	v_mfma_f32_32x32x16_bf16 v[18:33], v[106:109], v[102:105], v[18:33]
	s_mov_b32 m0, s92
	s_movk_i32 s2, 0x2000
	buffer_load_dwordx4 v175, s[64:67], 0 offen lds
	s_mov_b32 m0, s71
	s_nop 0
	buffer_load_dwordx4 v175, s[64:67], s2 offen lds
	s_and_saveexec_b64 s[2:3], s[0:1]
	s_cbranch_execz .LBB0_389
	v_add_f32_e32 v2, v2, v4
	v_fmac_f32_e32 v2, v179, v5
	v_add_f32_e32 v4, v7, v8
	v_fmac_f32_e32 v4, v2, v6
	ds_write_b32 v178, v4
	s_branch .LBB0_389
